# v37 + scal[0] scalar load hoisted from post-scan merge to prologue + k_t2 kernarg loads hoisted to entry
# baseline (speedup 1.0000x reference)
.LBB1_6:
	s_or_b64 exec, exec, s[4:5]
	v_mov_b32_e32 v6, 0x18010
	v_mov_b32_e32 v2, 0x18000
	s_waitcnt lgkmcnt(0)
	s_barrier
	s_load_dword s98, s[12:13], 0x0
	s_waitcnt vmcnt(14)
	ds_read_b128 v[2:5], v2
	ds_read_b128 v[6:9], v6
	s_load_dwordx4 s[36:39], s[0:1], 0x20
	s_movk_i32 s0, 0x2000
	v_lshrrev_b32_e32 v125, 4, v131
	s_waitcnt lgkmcnt(0)
	v_mov_b32_e32 v14, v2
	v_mov_b32_e32 v15, v6
	v_mov_b32_e32 v6, v3
	v_pk_add_f32 v[2:3], v[14:15], v[6:7]
	v_mov_b32_e32 v6, v4
	v_mov_b32_e32 v7, v8
	v_mov_b32_e32 v8, v5
	v_pk_add_f32 v[4:5], v[6:7], v[8:9]
	v_mov_b32_e32 v14, 0x18060
	v_pk_add_f32 v[2:3], v[2:3], v[4:5]
	v_add_co_u32_e32 v42, vcc, s0, v82
	v_add_f32_e32 v2, v2, v3
	v_mul_f32_e32 v132, 0x3a800000, v2
	v_and_b32_e32 v107, 15, v0
	v_mov_b32_e32 v2, 0x18020
	v_mov_b32_e32 v3, 0x18030
	v_lshl_add_u32 v13, v13, 2, v14
	v_pk_add_f32 v[10:11], v[10:11], v[132:133] op_sel_hi:[1,0] neg_lo:[0,1] neg_hi:[0,1]
	v_lshlrev_b32_e32 v85, 13, v1
	v_xor_b32_e32 v114, v125, v0
	v_addc_co_u32_e32 v43, vcc, 0, v83, vcc
	s_movk_i32 s0, 0x3000
	ds_read_b128 v[6:9], v2
	ds_read_b128 v[2:5], v3
	ds_write_b64 v13, v[10:11]
	v_lshl_or_b32 v84, v107, 9, v85
	v_lshlrev_b32_e32 v10, 4, v114
	s_movk_i32 s41, 0xf0
	v_add_co_u32_e32 v44, vcc, s0, v82
	v_lshlrev_b32_e32 v130, 2, v12
	v_and_or_b32 v115, v10, s41, v84
	v_addc_co_u32_e32 v45, vcc, 0, v83, vcc
	global_load_dwordx4 v[34:37], v[42:43], off offset:1024 nt
	global_load_dwordx4 v[30:33], v[42:43], off offset:2048 nt
	global_load_dwordx4 v[26:29], v[42:43], off offset:3072 nt
	global_load_dwordx4 v[38:41], v[44:45], off offset:-4096 nt
	global_load_dwordx4 v[22:25], v[44:45], off nt
	global_load_dwordx4 v[18:21], v[44:45], off offset:1024 nt
	global_load_dwordx4 v[14:17], v[44:45], off offset:2048 nt
	global_load_dwordx4 v[10:13], v[44:45], off offset:3072 nt
	s_waitcnt vmcnt(15)
	v_add_f32_e32 v42, v78, v79
	v_add_f32_e32 v43, v80, v81
	v_add_f32_e32 v42, v42, v43
	s_waitcnt vmcnt(14)
	v_add_f32_e32 v43, v74, v75
	v_add_f32_e32 v44, v76, v77
	v_add_f32_e32 v43, v43, v44
	s_waitcnt vmcnt(13)
	v_add_f32_e32 v44, v70, v71
	v_add_f32_e32 v45, v72, v73
	v_add_f32_e32 v44, v44, v45
	s_waitcnt vmcnt(12)
	v_add_f32_e32 v45, v66, v67
	v_add_f32_e32 v49, v68, v69
	v_add_f32_e32 v45, v45, v49
	s_waitcnt vmcnt(11)
	v_add_f32_e32 v49, v62, v63
	v_add_f32_e32 v86, v64, v65
	v_and_b32_e32 v46, 1, v0
	v_add_f32_e32 v49, v49, v86
	s_waitcnt vmcnt(10)
	v_add_f32_e32 v86, v58, v59
	v_add_f32_e32 v88, v60, v61
	v_add_f32_e32 v86, v86, v88
	s_waitcnt vmcnt(9)
	v_add_f32_e32 v88, v54, v55
	v_add_f32_e32 v89, v56, v57
	v_cmp_eq_u32_e64 s[4:5], 1, v46
	v_add_f32_e32 v88, v88, v89
	s_waitcnt vmcnt(8)
	v_add_f32_e32 v89, v50, v51
	v_add_f32_e32 v90, v52, v53
	v_cndmask_b32_e64 v46, v43, v42, s[4:5]
	v_cndmask_b32_e64 v42, v42, v43, s[4:5]
	v_cndmask_b32_e64 v43, v45, v44, s[4:5]
	v_cndmask_b32_e64 v44, v44, v45, s[4:5]
	v_add_f32_e32 v89, v89, v90
	v_cndmask_b32_e64 v45, v49, v86, s[4:5]
	v_add_f32_dpp v43, v43, v44 quad_perm:[1,0,3,2] row_mask:0xf bank_mask:0xf bound_ctrl:1
	v_cndmask_b32_e64 v44, v86, v49, s[4:5]
	v_and_b32_e32 v47, 2, v0
	v_add_f32_dpp v42, v46, v42 quad_perm:[1,0,3,2] row_mask:0xf bank_mask:0xf bound_ctrl:1
	v_add_f32_dpp v44, v44, v45 quad_perm:[1,0,3,2] row_mask:0xf bank_mask:0xf bound_ctrl:1
	v_cndmask_b32_e64 v45, v89, v88, s[4:5]
	v_cndmask_b32_e64 v46, v88, v89, s[4:5]
	v_cmp_eq_u16_e64 s[6:7], 0, v47
	v_and_b32_e32 v48, 4, v0
	v_add_f32_dpp v45, v45, v46 quad_perm:[1,0,3,2] row_mask:0xf bank_mask:0xf bound_ctrl:1
	v_cndmask_b32_e64 v46, v42, v43, s[6:7]
	v_cndmask_b32_e64 v42, v43, v42, s[6:7]
	v_cndmask_b32_e64 v43, v44, v45, s[6:7]
	v_cndmask_b32_e64 v44, v45, v44, s[6:7]
	v_add_f32_dpp v42, v46, v42 quad_perm:[2,3,0,1] row_mask:0xf bank_mask:0xf bound_ctrl:1
	v_cmp_eq_u16_e64 s[8:9], 0, v48
	v_add_f32_dpp v43, v43, v44 quad_perm:[2,3,0,1] row_mask:0xf bank_mask:0xf bound_ctrl:1
	v_lshlrev_b32_e32 v86, 3, v131
	v_cndmask_b32_e64 v44, v42, v43, s[8:9]
	v_cndmask_b32_e64 v42, v43, v42, s[8:9]
	v_mov_b32_e32 v43, v44
	v_and_b32_e32 v87, 8, v87
	v_mov_b32_e32 v116, 0x3727c5ac
	v_mov_b32_dpp v43, v43 row_shl:4 row_mask:0xf bank_mask:0x5
	v_mov_b32_e32 v117, 0x260
	v_bitop3_b32 v141, v125, v0, 4 bitop3:0x36
	v_mov_b32_dpp v43, v44 row_shr:4 row_mask:0xf bank_mask:0xa
	v_add_f32_e32 v42, v42, v43
	v_bitop3_b32 v142, v125, v0, 8 bitop3:0x36
	v_bitop3_b32 v143, v125, v0, 12 bitop3:0x36
	v_add_f32_dpp v42, v42, v42 row_ror:8 row_mask:0xf bank_mask:0xf bound_ctrl:1
	v_mov_b32_e32 v43, v42
	s_nop 1
	v_permlane16_swap_b32_e32 v42, v43
	v_add_f32_e32 v42, v42, v43
	v_mov_b32_e32 v43, v42
	s_nop 1
	v_permlane32_swap_b32_e32 v42, v43
	v_add_f32_e32 v42, v42, v43
	v_mul_f32_e32 v42, 0x3b800000, v42
	s_mov_b32 s3, 0
	v_readlane_b32 s40, v42, 0
	v_readlane_b32 s42, v42, 1
	v_readlane_b32 s44, v42, 2
	v_readlane_b32 s46, v42, 3
	v_readlane_b32 s48, v42, 4
	v_readlane_b32 s50, v42, 5
	v_readlane_b32 s34, v42, 6
	v_readlane_b32 s0, v42, 7
	v_pk_add_f32 v[90:91], v[78:79], s[40:41] op_sel_hi:[1,0] neg_lo:[0,1] neg_hi:[0,1]
	v_pk_add_f32 v[80:81], v[80:81], s[40:41] op_sel_hi:[1,0] neg_lo:[0,1] neg_hi:[0,1]
	v_and_b32_e32 v78, 0x1f0, v86
	v_pk_add_f32 v[76:77], v[76:77], s[42:43] op_sel_hi:[1,0] neg_lo:[0,1] neg_hi:[0,1]
	v_mul_f32_e32 v88, v81, v81
	v_or3_b32 v140, v85, v78, v87
	v_pk_add_f32 v[78:79], v[74:75], s[42:43] op_sel_hi:[1,0] neg_lo:[0,1] neg_hi:[0,1]
	v_mul_f32_e32 v74, v77, v77
	v_fmac_f32_e32 v88, v80, v80
	v_fmac_f32_e32 v74, v76, v76
	v_fmac_f32_e32 v88, v91, v91
	v_fmac_f32_e32 v74, v79, v79
	v_fmac_f32_e32 v88, v90, v90
	v_fmac_f32_e32 v74, v78, v78
	v_cndmask_b32_e64 v75, v74, v88, s[4:5]
	v_cndmask_b32_e64 v74, v88, v74, s[4:5]
	v_mov_b32_e32 v88, 0x1f0
	v_pk_add_f32 v[72:73], v[72:73], s[44:45] op_sel_hi:[1,0] neg_lo:[0,1] neg_hi:[0,1]
	v_add_f32_dpp v89, v75, v74 quad_perm:[1,0,3,2] row_mask:0xf bank_mask:0xf bound_ctrl:1
	v_bitop3_b32 v74, v86, 16, v88 bitop3:0x6c
	v_or3_b32 v138, v85, v74, v87
	v_pk_add_f32 v[74:75], v[70:71], s[44:45] op_sel_hi:[1,0] neg_lo:[0,1] neg_hi:[0,1]
	v_bitop3_b32 v70, v86, 32, v88 bitop3:0x6c
	v_pk_add_f32 v[68:69], v[68:69], s[46:47] op_sel_hi:[1,0] neg_lo:[0,1] neg_hi:[0,1]
	v_mul_f32_e32 v92, v73, v73
	v_or3_b32 v135, v85, v70, v87
	v_pk_add_f32 v[70:71], v[66:67], s[46:47] op_sel_hi:[1,0] neg_lo:[0,1] neg_hi:[0,1]
	v_mul_f32_e32 v66, v69, v69
	v_fmac_f32_e32 v92, v72, v72
	v_fmac_f32_e32 v66, v68, v68
	v_fmac_f32_e32 v92, v75, v75
	v_fmac_f32_e32 v66, v71, v71
	v_fmac_f32_e32 v92, v74, v74
	v_fmac_f32_e32 v66, v70, v70
	v_cndmask_b32_e64 v67, v66, v92, s[4:5]
	v_cndmask_b32_e64 v66, v92, v66, s[4:5]
	v_pk_add_f32 v[64:65], v[64:65], s[48:49] op_sel_hi:[1,0] neg_lo:[0,1] neg_hi:[0,1]
	v_pk_add_f32 v[60:61], v[60:61], s[50:51] op_sel_hi:[1,0] neg_lo:[0,1] neg_hi:[0,1]
	v_add_f32_dpp v66, v67, v66 quad_perm:[1,0,3,2] row_mask:0xf bank_mask:0xf bound_ctrl:1
	v_cndmask_b32_e64 v67, v89, v66, s[6:7]
	v_cndmask_b32_e64 v66, v66, v89, s[6:7]
	v_mul_f32_e32 v92, v65, v65
	v_fmac_f32_e32 v92, v64, v64
	v_add_f32_dpp v89, v67, v66 quad_perm:[2,3,0,1] row_mask:0xf bank_mask:0xf bound_ctrl:1
	v_bitop3_b32 v66, v86, 48, v88 bitop3:0x6c
	v_or3_b32 v134, v85, v66, v87
	v_pk_add_f32 v[66:67], v[62:63], s[48:49] op_sel_hi:[1,0] neg_lo:[0,1] neg_hi:[0,1]
	v_bitop3_b32 v62, v86, 64, v88 bitop3:0x6c
	v_or3_b32 v120, v85, v62, v87
	v_pk_add_f32 v[62:63], v[58:59], s[50:51] op_sel_hi:[1,0] neg_lo:[0,1] neg_hi:[0,1]
	v_mul_f32_e32 v58, v61, v61
	v_fmac_f32_e32 v58, v60, v60
	v_fmac_f32_e32 v92, v67, v67
	v_fmac_f32_e32 v58, v63, v63
	v_fmac_f32_e32 v92, v66, v66
	v_fmac_f32_e32 v58, v62, v62
	v_cndmask_b32_e64 v59, v58, v92, s[4:5]
	v_cndmask_b32_e64 v58, v92, v58, s[4:5]
	v_pk_add_f32 v[56:57], v[56:57], s[34:35] op_sel_hi:[1,0] neg_lo:[0,1] neg_hi:[0,1]
	s_mov_b32 s25, 0x3e6d3387
	v_add_f32_dpp v92, v59, v58 quad_perm:[1,0,3,2] row_mask:0xf bank_mask:0xf bound_ctrl:1
	v_pk_add_f32 v[58:59], v[54:55], s[34:35] op_sel_hi:[1,0] neg_lo:[0,1] neg_hi:[0,1]
	v_pk_add_f32 v[54:55], v[50:51], s[0:1] op_sel_hi:[1,0] neg_lo:[0,1] neg_hi:[0,1]
	v_pk_add_f32 v[50:51], v[52:53], s[0:1] op_sel_hi:[1,0] neg_lo:[0,1] neg_hi:[0,1]
	v_mul_f32_e32 v93, v57, v57
	v_mul_f32_e32 v52, v51, v51
	v_fmac_f32_e32 v93, v56, v56
	v_fmac_f32_e32 v52, v50, v50
	v_fmac_f32_e32 v93, v59, v59
	v_fmac_f32_e32 v52, v55, v55
	v_fmac_f32_e32 v93, v58, v58
	v_fmac_f32_e32 v52, v54, v54
	v_cndmask_b32_e64 v53, v52, v93, s[4:5]
	v_cndmask_b32_e64 v52, v93, v52, s[4:5]
	s_mov_b32 s35, 0xf800000
	s_movk_i32 s0, 0x50
	v_add_f32_dpp v52, v53, v52 quad_perm:[1,0,3,2] row_mask:0xf bank_mask:0xf bound_ctrl:1
	v_cndmask_b32_e64 v53, v92, v52, s[6:7]
	v_cndmask_b32_e64 v52, v52, v92, s[6:7]
	s_mov_b32 s24, 0xbf3a00e3
	s_mov_b32 s22, 0x3f07dc22
	v_add_f32_dpp v52, v53, v52 quad_perm:[2,3,0,1] row_mask:0xf bank_mask:0xf bound_ctrl:1
	v_cndmask_b32_e64 v53, v89, v52, s[8:9]
	v_cndmask_b32_e64 v52, v52, v89, s[8:9]
	v_mov_b32_e32 v89, v53
	s_mov_b32 s34, 0xbe11a98e
	s_mov_b32 s40, 0x3e027906
	v_mov_b32_dpp v89, v89 row_shl:4 row_mask:0xf bank_mask:0x5
	s_mov_b32 s33, 5
	s_nop 0
	v_mov_b32_dpp v89, v53 row_shr:4 row_mask:0xf bank_mask:0xa
	v_add_f32_e32 v52, v52, v89
	v_bitop3_b32 v89, v86, s0, v88 bitop3:0x6c
	v_or3_b32 v121, v85, v89, v87
	v_add_f32_dpp v52, v52, v52 row_ror:8 row_mask:0xf bank_mask:0xf bound_ctrl:1
	v_mov_b32_e32 v53, v52
	s_nop 1
	v_permlane16_swap_b32_e32 v52, v53
	v_add_f32_e32 v52, v52, v53
	v_mov_b32_e32 v53, v52
	s_nop 1
	v_permlane32_swap_b32_e32 v52, v53
	v_add_f32_e32 v52, v52, v53
	v_fmamk_f32 v52, v52, 0x3b800000, v116
	v_mul_f32_e32 v53, 0x4f800000, v52
	v_cmp_gt_f32_e32 vcc, s35, v52
	s_nop 1
	v_cndmask_b32_e32 v52, v52, v53, vcc
	v_sqrt_f32_e32 v53, v52
	s_nop 0
	v_add_u32_e32 v89, -1, v53
	v_fma_f32 v92, -v89, v53, v52
	v_cmp_ge_f32_e64 s[0:1], 0, v92
	v_add_u32_e32 v92, 1, v53
	s_nop 0
	v_cndmask_b32_e64 v89, v53, v89, s[0:1]
	v_fma_f32 v53, -v92, v53, v52
	v_cmp_lt_f32_e64 s[0:1], 0, v53
	s_nop 1
	v_cndmask_b32_e64 v53, v89, v92, s[0:1]
	v_mul_f32_e32 v89, 0x37800000, v53
	v_cndmask_b32_e32 v53, v53, v89, vcc
	v_cmp_class_f32_e32 vcc, v52, v117
	s_nop 1
	v_cndmask_b32_e32 v52, v53, v52, vcc
	v_div_scale_f32 v53, s[0:1], v52, v52, 1.0
	v_rcp_f32_e32 v89, v53
	s_movk_i32 s0, 0x60
	v_bitop3_b32 v92, v86, s0, v88 bitop3:0x6c
	v_or3_b32 v118, v85, v92, v87
	v_fma_f32 v92, -v53, v89, 1.0
	v_fmac_f32_e32 v89, v92, v89
	v_div_scale_f32 v92, vcc, 1.0, v52, 1.0
	v_mul_f32_e32 v93, v92, v89
	v_fma_f32 v94, -v53, v93, v92
	v_fmac_f32_e32 v93, v94, v89
	v_fma_f32 v53, -v53, v93, v92
	v_div_fmas_f32 v53, v53, v89, v93
	v_div_fixup_f32 v52, v53, v52, 1.0
	s_waitcnt vmcnt(4)
	v_add_f32_e32 v89, v38, v39
	v_readlane_b32 s0, v52, 0
	s_nop 1
	v_pk_mul_f32 v[90:91], s[0:1], v[90:91] op_sel_hi:[0,1]
	v_pk_fma_f32 v[92:93], v[90:91], v[238:239], v[242:243]
	v_mov_b64_e32 v[90:91], s[24:25]
	v_fma_f32 v53, |v92|, s25, 1.0
	v_pk_mul_f32 v[98:99], v[92:93], v[92:93]
	v_rcp_f32_e32 v96, v53
	v_mul_f32_e32 v53, 0xbf38aa3b, v98
	v_exp_f32_e32 v98, v53
	v_fma_f32 v53, |v93|, s25, 1.0
	v_rcp_f32_e32 v97, v53
	s_mov_b32 s24, 0x3f35f0e3
	v_pk_mul_f32 v[80:81], s[0:1], v[80:81] op_sel_hi:[0,1]
	v_mul_f32_e32 v53, 0xbf38aa3b, v99
	v_pk_fma_f32 v[100:101], v[96:97], s[22:23], v[90:91] op_sel_hi:[1,0,0]
	v_pk_fma_f32 v[80:81], v[80:81], v[240:241], v[244:245]
	v_pk_fma_f32 v[100:101], v[96:97], v[100:101], s[24:25] op_sel_hi:[1,1,0]
	v_and_b32_e32 v95, 0x7fffffff, v93
	v_pk_fma_f32 v[100:101], v[96:97], v[100:101], s[34:35] op_sel_hi:[1,1,0]
	v_and_b32_e32 v94, 0x7fffffff, v92
	v_pk_fma_f32 v[100:101], v[96:97], v[100:101], s[40:41] op_sel_hi:[1,1,0]
	v_exp_f32_e32 v99, v53
	v_pk_mul_f32 v[96:97], v[96:97], v[100:101]
	v_fma_f32 v53, |v80|, s25, 1.0
	v_pk_mul_f32 v[94:95], v[94:95], v[96:97]
	v_rcp_f32_e32 v96, v53
	v_fma_f32 v53, |v81|, s25, 1.0
	v_rcp_f32_e32 v97, v53
	v_max_f32_e32 v92, 0, v92
	v_max_f32_e32 v93, 0, v93
	v_pk_fma_f32 v[92:93], v[98:99], v[94:95], v[92:93] neg_lo:[1,0,0] neg_hi:[1,0,0]
	v_pk_mul_f32 v[98:99], v[80:81], v[80:81]
	v_pk_fma_f32 v[100:101], v[96:97], s[22:23], v[90:91] op_sel_hi:[1,0,0]
	v_mul_f32_e32 v53, 0xbf38aa3b, v98
	v_exp_f32_e32 v98, v53
	v_pk_fma_f32 v[100:101], v[96:97], v[100:101], s[24:25] op_sel_hi:[1,1,0]
	v_mul_f32_e32 v53, 0xbf38aa3b, v99
	v_pk_fma_f32 v[100:101], v[96:97], v[100:101], s[34:35] op_sel_hi:[1,1,0]
	v_exp_f32_e32 v99, v53
	v_pk_fma_f32 v[100:101], v[96:97], v[100:101], s[40:41] op_sel_hi:[1,1,0]
	v_and_b32_e32 v95, 0x7fffffff, v81
	v_and_b32_e32 v94, 0x7fffffff, v80
	v_pk_mul_f32 v[96:97], v[96:97], v[100:101]
	v_readlane_b32 s0, v52, 1
	v_max_f32_e32 v80, 0, v80
	v_max_f32_e32 v81, 0, v81
	v_pk_mul_f32 v[94:95], v[94:95], v[96:97]
	v_pk_mul_f32 v[78:79], s[0:1], v[78:79] op_sel_hi:[0,1]
	v_pk_fma_f32 v[80:81], v[98:99], v[94:95], v[80:81] neg_lo:[1,0,0] neg_hi:[1,0,0]
	v_pk_fma_f32 v[78:79], v[78:79], v[238:239], v[242:243]
	v_cvt_pk_f16_f32 v92, v92, v93
	v_cvt_pk_f16_f32 v93, v80, v81
	v_fma_f32 v53, |v78|, s25, 1.0
	ds_write_b64 v140, v[92:93] offset:32768
	v_rcp_f32_e32 v92, v53
	v_fma_f32 v53, |v79|, s25, 1.0
	v_rcp_f32_e32 v93, v53
	v_pk_mul_f32 v[94:95], v[78:79], v[78:79]
	v_pk_mul_f32 v[76:77], s[0:1], v[76:77] op_sel_hi:[0,1]
	v_mul_f32_e32 v53, 0xbf38aa3b, v94
	v_pk_fma_f32 v[96:97], v[92:93], s[22:23], v[90:91] op_sel_hi:[1,0,0]
	v_exp_f32_e32 v94, v53
	v_pk_fma_f32 v[96:97], v[92:93], v[96:97], s[24:25] op_sel_hi:[1,1,0]
	v_mul_f32_e32 v53, 0xbf38aa3b, v95
	v_pk_fma_f32 v[96:97], v[92:93], v[96:97], s[34:35] op_sel_hi:[1,1,0]
	v_pk_fma_f32 v[76:77], v[76:77], v[240:241], v[244:245]
	v_pk_fma_f32 v[96:97], v[92:93], v[96:97], s[40:41] op_sel_hi:[1,1,0]
	v_and_b32_e32 v81, 0x7fffffff, v79
	v_and_b32_e32 v80, 0x7fffffff, v78
	v_exp_f32_e32 v95, v53
	v_pk_mul_f32 v[92:93], v[92:93], v[96:97]
	v_fma_f32 v53, |v76|, s25, 1.0
	v_pk_mul_f32 v[80:81], v[80:81], v[92:93]
	v_rcp_f32_e32 v92, v53
	v_fma_f32 v53, |v77|, s25, 1.0
	v_rcp_f32_e32 v93, v53
	v_max_f32_e32 v78, 0, v78
	v_max_f32_e32 v79, 0, v79
	v_pk_fma_f32 v[78:79], v[94:95], v[80:81], v[78:79] neg_lo:[1,0,0] neg_hi:[1,0,0]
	v_pk_mul_f32 v[94:95], v[76:77], v[76:77]
	v_pk_fma_f32 v[96:97], v[92:93], s[22:23], v[90:91] op_sel_hi:[1,0,0]
	v_mul_f32_e32 v53, 0xbf38aa3b, v94
	v_exp_f32_e32 v94, v53
	v_pk_fma_f32 v[96:97], v[92:93], v[96:97], s[24:25] op_sel_hi:[1,1,0]
	v_mul_f32_e32 v53, 0xbf38aa3b, v95
	v_pk_fma_f32 v[96:97], v[92:93], v[96:97], s[34:35] op_sel_hi:[1,1,0]
	v_exp_f32_e32 v95, v53
	v_pk_fma_f32 v[96:97], v[92:93], v[96:97], s[40:41] op_sel_hi:[1,1,0]
	v_and_b32_e32 v81, 0x7fffffff, v77
	v_and_b32_e32 v80, 0x7fffffff, v76
	v_pk_mul_f32 v[92:93], v[92:93], v[96:97]
	v_readlane_b32 s0, v52, 2
	v_max_f32_e32 v76, 0, v76
	v_max_f32_e32 v77, 0, v77
	v_pk_mul_f32 v[80:81], v[80:81], v[92:93]
	v_pk_mul_f32 v[74:75], s[0:1], v[74:75] op_sel_hi:[0,1]
	v_pk_fma_f32 v[76:77], v[94:95], v[80:81], v[76:77] neg_lo:[1,0,0] neg_hi:[1,0,0]
	v_pk_fma_f32 v[74:75], v[74:75], v[238:239], v[242:243]
	v_cvt_pk_f16_f32 v78, v78, v79
	v_cvt_pk_f16_f32 v79, v76, v77
	v_fma_f32 v53, |v74|, s25, 1.0
	ds_write_b64 v138, v[78:79] offset:33280
	v_rcp_f32_e32 v78, v53
	v_fma_f32 v53, |v75|, s25, 1.0
	v_rcp_f32_e32 v79, v53
	v_pk_mul_f32 v[80:81], v[74:75], v[74:75]
	v_pk_mul_f32 v[72:73], s[0:1], v[72:73] op_sel_hi:[0,1]
	v_mul_f32_e32 v53, 0xbf38aa3b, v80
	v_pk_fma_f32 v[92:93], v[78:79], s[22:23], v[90:91] op_sel_hi:[1,0,0]
	v_exp_f32_e32 v80, v53
	v_pk_fma_f32 v[92:93], v[78:79], v[92:93], s[24:25] op_sel_hi:[1,1,0]
	v_mul_f32_e32 v53, 0xbf38aa3b, v81
	v_pk_fma_f32 v[92:93], v[78:79], v[92:93], s[34:35] op_sel_hi:[1,1,0]
	v_pk_fma_f32 v[72:73], v[72:73], v[240:241], v[244:245]
	v_pk_fma_f32 v[92:93], v[78:79], v[92:93], s[40:41] op_sel_hi:[1,1,0]
	v_and_b32_e32 v77, 0x7fffffff, v75
	v_and_b32_e32 v76, 0x7fffffff, v74
	v_exp_f32_e32 v81, v53
	v_pk_mul_f32 v[78:79], v[78:79], v[92:93]
	v_fma_f32 v53, |v72|, s25, 1.0
	v_pk_mul_f32 v[76:77], v[76:77], v[78:79]
	v_rcp_f32_e32 v78, v53
	v_fma_f32 v53, |v73|, s25, 1.0
	v_rcp_f32_e32 v79, v53
	v_max_f32_e32 v74, 0, v74
	v_max_f32_e32 v75, 0, v75
	v_pk_fma_f32 v[74:75], v[80:81], v[76:77], v[74:75] neg_lo:[1,0,0] neg_hi:[1,0,0]
	v_pk_mul_f32 v[80:81], v[72:73], v[72:73]
	v_pk_fma_f32 v[92:93], v[78:79], s[22:23], v[90:91] op_sel_hi:[1,0,0]
	v_mul_f32_e32 v53, 0xbf38aa3b, v80
	v_exp_f32_e32 v80, v53
	v_pk_fma_f32 v[92:93], v[78:79], v[92:93], s[24:25] op_sel_hi:[1,1,0]
	v_mul_f32_e32 v53, 0xbf38aa3b, v81
	v_pk_fma_f32 v[92:93], v[78:79], v[92:93], s[34:35] op_sel_hi:[1,1,0]
	v_exp_f32_e32 v81, v53
	v_pk_fma_f32 v[92:93], v[78:79], v[92:93], s[40:41] op_sel_hi:[1,1,0]
	v_and_b32_e32 v77, 0x7fffffff, v73
	v_and_b32_e32 v76, 0x7fffffff, v72
	v_pk_mul_f32 v[78:79], v[78:79], v[92:93]
	v_readlane_b32 s0, v52, 3
	v_max_f32_e32 v72, 0, v72
	v_max_f32_e32 v73, 0, v73
	v_pk_mul_f32 v[76:77], v[76:77], v[78:79]
	v_pk_mul_f32 v[70:71], s[0:1], v[70:71] op_sel_hi:[0,1]
	v_pk_fma_f32 v[72:73], v[80:81], v[76:77], v[72:73] neg_lo:[1,0,0] neg_hi:[1,0,0]
	v_pk_fma_f32 v[70:71], v[70:71], v[238:239], v[242:243]
	v_cvt_pk_f16_f32 v74, v74, v75
	v_cvt_pk_f16_f32 v75, v72, v73
	v_fma_f32 v53, |v70|, s25, 1.0
	ds_write_b64 v135, v[74:75] offset:33792
	v_rcp_f32_e32 v74, v53
	v_fma_f32 v53, |v71|, s25, 1.0
	v_rcp_f32_e32 v75, v53
	v_pk_mul_f32 v[76:77], v[70:71], v[70:71]
	v_pk_mul_f32 v[68:69], s[0:1], v[68:69] op_sel_hi:[0,1]
	v_mul_f32_e32 v53, 0xbf38aa3b, v76
	v_pk_fma_f32 v[78:79], v[74:75], s[22:23], v[90:91] op_sel_hi:[1,0,0]
	v_exp_f32_e32 v76, v53
	v_pk_fma_f32 v[78:79], v[74:75], v[78:79], s[24:25] op_sel_hi:[1,1,0]
	v_mul_f32_e32 v53, 0xbf38aa3b, v77
	v_pk_fma_f32 v[78:79], v[74:75], v[78:79], s[34:35] op_sel_hi:[1,1,0]
	v_pk_fma_f32 v[68:69], v[68:69], v[240:241], v[244:245]
	v_pk_fma_f32 v[78:79], v[74:75], v[78:79], s[40:41] op_sel_hi:[1,1,0]
	v_and_b32_e32 v73, 0x7fffffff, v71
	v_and_b32_e32 v72, 0x7fffffff, v70
	v_exp_f32_e32 v77, v53
	v_pk_mul_f32 v[74:75], v[74:75], v[78:79]
	v_fma_f32 v53, |v68|, s25, 1.0
	v_pk_mul_f32 v[72:73], v[72:73], v[74:75]
	v_rcp_f32_e32 v74, v53
	v_fma_f32 v53, |v69|, s25, 1.0
	v_rcp_f32_e32 v75, v53
	v_max_f32_e32 v70, 0, v70
	v_max_f32_e32 v71, 0, v71
	v_pk_fma_f32 v[70:71], v[76:77], v[72:73], v[70:71] neg_lo:[1,0,0] neg_hi:[1,0,0]
	v_pk_mul_f32 v[76:77], v[68:69], v[68:69]
	v_pk_fma_f32 v[78:79], v[74:75], s[22:23], v[90:91] op_sel_hi:[1,0,0]
	v_mul_f32_e32 v53, 0xbf38aa3b, v76
	v_exp_f32_e32 v76, v53
	v_pk_fma_f32 v[78:79], v[74:75], v[78:79], s[24:25] op_sel_hi:[1,1,0]
	v_mul_f32_e32 v53, 0xbf38aa3b, v77
	v_pk_fma_f32 v[78:79], v[74:75], v[78:79], s[34:35] op_sel_hi:[1,1,0]
	v_exp_f32_e32 v77, v53
	v_pk_fma_f32 v[78:79], v[74:75], v[78:79], s[40:41] op_sel_hi:[1,1,0]
	v_and_b32_e32 v73, 0x7fffffff, v69
	v_and_b32_e32 v72, 0x7fffffff, v68
	v_pk_mul_f32 v[74:75], v[74:75], v[78:79]
	v_readlane_b32 s0, v52, 4
	v_max_f32_e32 v68, 0, v68
	v_max_f32_e32 v69, 0, v69
	v_pk_mul_f32 v[72:73], v[72:73], v[74:75]
	v_pk_mul_f32 v[66:67], s[0:1], v[66:67] op_sel_hi:[0,1]
	v_pk_fma_f32 v[68:69], v[76:77], v[72:73], v[68:69] neg_lo:[1,0,0] neg_hi:[1,0,0]
	v_pk_fma_f32 v[66:67], v[66:67], v[238:239], v[242:243]
	v_cvt_pk_f16_f32 v70, v70, v71
	v_cvt_pk_f16_f32 v71, v68, v69
	v_fma_f32 v53, |v66|, s25, 1.0
	ds_write_b64 v134, v[70:71] offset:34304
	v_rcp_f32_e32 v70, v53
	v_fma_f32 v53, |v67|, s25, 1.0
	v_rcp_f32_e32 v71, v53
	v_pk_mul_f32 v[72:73], v[66:67], v[66:67]
	v_pk_mul_f32 v[64:65], s[0:1], v[64:65] op_sel_hi:[0,1]
	v_mul_f32_e32 v53, 0xbf38aa3b, v72
	v_pk_fma_f32 v[74:75], v[70:71], s[22:23], v[90:91] op_sel_hi:[1,0,0]
	v_exp_f32_e32 v72, v53
	v_pk_fma_f32 v[74:75], v[70:71], v[74:75], s[24:25] op_sel_hi:[1,1,0]
	v_mul_f32_e32 v53, 0xbf38aa3b, v73
	v_pk_fma_f32 v[74:75], v[70:71], v[74:75], s[34:35] op_sel_hi:[1,1,0]
	v_pk_fma_f32 v[64:65], v[64:65], v[240:241], v[244:245]
	v_pk_fma_f32 v[74:75], v[70:71], v[74:75], s[40:41] op_sel_hi:[1,1,0]
	v_and_b32_e32 v69, 0x7fffffff, v67
	v_and_b32_e32 v68, 0x7fffffff, v66
	v_exp_f32_e32 v73, v53
	v_pk_mul_f32 v[70:71], v[70:71], v[74:75]
	v_fma_f32 v53, |v64|, s25, 1.0
	v_pk_mul_f32 v[68:69], v[68:69], v[70:71]
	v_rcp_f32_e32 v70, v53
	v_fma_f32 v53, |v65|, s25, 1.0
	v_rcp_f32_e32 v71, v53
	v_max_f32_e32 v66, 0, v66
	v_max_f32_e32 v67, 0, v67
	v_pk_fma_f32 v[66:67], v[72:73], v[68:69], v[66:67] neg_lo:[1,0,0] neg_hi:[1,0,0]
	v_pk_mul_f32 v[72:73], v[64:65], v[64:65]
	v_pk_fma_f32 v[74:75], v[70:71], s[22:23], v[90:91] op_sel_hi:[1,0,0]
	v_mul_f32_e32 v53, 0xbf38aa3b, v72
	v_exp_f32_e32 v72, v53
	v_pk_fma_f32 v[74:75], v[70:71], v[74:75], s[24:25] op_sel_hi:[1,1,0]
	v_mul_f32_e32 v53, 0xbf38aa3b, v73
	v_pk_fma_f32 v[74:75], v[70:71], v[74:75], s[34:35] op_sel_hi:[1,1,0]
	v_exp_f32_e32 v73, v53
	v_pk_fma_f32 v[74:75], v[70:71], v[74:75], s[40:41] op_sel_hi:[1,1,0]
	v_and_b32_e32 v69, 0x7fffffff, v65
	v_and_b32_e32 v68, 0x7fffffff, v64
	v_pk_mul_f32 v[70:71], v[70:71], v[74:75]
	v_readlane_b32 s0, v52, 5
	v_max_f32_e32 v64, 0, v64
	v_max_f32_e32 v65, 0, v65
	v_pk_mul_f32 v[68:69], v[68:69], v[70:71]
	v_pk_mul_f32 v[62:63], s[0:1], v[62:63] op_sel_hi:[0,1]
	v_pk_fma_f32 v[64:65], v[72:73], v[68:69], v[64:65] neg_lo:[1,0,0] neg_hi:[1,0,0]
	v_pk_fma_f32 v[62:63], v[62:63], v[238:239], v[242:243]
	v_cvt_pk_f16_f32 v66, v66, v67
	v_cvt_pk_f16_f32 v67, v64, v65
	v_fma_f32 v53, |v62|, s25, 1.0
	ds_write_b64 v120, v[66:67] offset:34816
	v_rcp_f32_e32 v66, v53
	v_fma_f32 v53, |v63|, s25, 1.0
	v_rcp_f32_e32 v67, v53
	v_pk_mul_f32 v[68:69], v[62:63], v[62:63]
	v_pk_mul_f32 v[60:61], s[0:1], v[60:61] op_sel_hi:[0,1]
	v_mul_f32_e32 v53, 0xbf38aa3b, v68
	v_pk_fma_f32 v[70:71], v[66:67], s[22:23], v[90:91] op_sel_hi:[1,0,0]
	v_exp_f32_e32 v68, v53
	v_pk_fma_f32 v[70:71], v[66:67], v[70:71], s[24:25] op_sel_hi:[1,1,0]
	v_mul_f32_e32 v53, 0xbf38aa3b, v69
	v_pk_fma_f32 v[70:71], v[66:67], v[70:71], s[34:35] op_sel_hi:[1,1,0]
	v_pk_fma_f32 v[60:61], v[60:61], v[240:241], v[244:245]
	v_pk_fma_f32 v[70:71], v[66:67], v[70:71], s[40:41] op_sel_hi:[1,1,0]
	v_and_b32_e32 v65, 0x7fffffff, v63
	v_and_b32_e32 v64, 0x7fffffff, v62
	v_exp_f32_e32 v69, v53
	v_pk_mul_f32 v[66:67], v[66:67], v[70:71]
	v_fma_f32 v53, |v60|, s25, 1.0
	v_pk_mul_f32 v[64:65], v[64:65], v[66:67]
	v_rcp_f32_e32 v66, v53
	v_fma_f32 v53, |v61|, s25, 1.0
	v_rcp_f32_e32 v67, v53
	v_max_f32_e32 v62, 0, v62
	v_max_f32_e32 v63, 0, v63
	v_pk_fma_f32 v[62:63], v[68:69], v[64:65], v[62:63] neg_lo:[1,0,0] neg_hi:[1,0,0]
	v_pk_mul_f32 v[68:69], v[60:61], v[60:61]
	v_pk_fma_f32 v[70:71], v[66:67], s[22:23], v[90:91] op_sel_hi:[1,0,0]
	v_mul_f32_e32 v53, 0xbf38aa3b, v68
	v_exp_f32_e32 v68, v53
	v_pk_fma_f32 v[70:71], v[66:67], v[70:71], s[24:25] op_sel_hi:[1,1,0]
	v_mul_f32_e32 v53, 0xbf38aa3b, v69
	v_pk_fma_f32 v[70:71], v[66:67], v[70:71], s[34:35] op_sel_hi:[1,1,0]
	v_exp_f32_e32 v69, v53
	v_pk_fma_f32 v[70:71], v[66:67], v[70:71], s[40:41] op_sel_hi:[1,1,0]
	v_and_b32_e32 v65, 0x7fffffff, v61
	v_and_b32_e32 v64, 0x7fffffff, v60
	v_pk_mul_f32 v[66:67], v[66:67], v[70:71]
	v_readlane_b32 s0, v52, 6
	v_max_f32_e32 v60, 0, v60
	v_max_f32_e32 v61, 0, v61
	v_pk_mul_f32 v[64:65], v[64:65], v[66:67]
	v_pk_mul_f32 v[58:59], s[0:1], v[58:59] op_sel_hi:[0,1]
	v_pk_fma_f32 v[60:61], v[68:69], v[64:65], v[60:61] neg_lo:[1,0,0] neg_hi:[1,0,0]
	v_pk_fma_f32 v[58:59], v[58:59], v[238:239], v[242:243]
	v_cvt_pk_f16_f32 v62, v62, v63
	v_cvt_pk_f16_f32 v63, v60, v61
	v_fma_f32 v53, |v58|, s25, 1.0
	ds_write_b64 v121, v[62:63] offset:35328
	v_rcp_f32_e32 v62, v53
	v_fma_f32 v53, |v59|, s25, 1.0
	v_rcp_f32_e32 v63, v53
	v_pk_mul_f32 v[64:65], v[58:59], v[58:59]
	v_pk_mul_f32 v[56:57], s[0:1], v[56:57] op_sel_hi:[0,1]
	v_mul_f32_e32 v53, 0xbf38aa3b, v64
	v_pk_fma_f32 v[66:67], v[62:63], s[22:23], v[90:91] op_sel_hi:[1,0,0]
	v_exp_f32_e32 v64, v53
	v_pk_fma_f32 v[66:67], v[62:63], v[66:67], s[24:25] op_sel_hi:[1,1,0]
	v_mul_f32_e32 v53, 0xbf38aa3b, v65
	v_pk_fma_f32 v[66:67], v[62:63], v[66:67], s[34:35] op_sel_hi:[1,1,0]
	v_pk_fma_f32 v[56:57], v[56:57], v[240:241], v[244:245]
	v_pk_fma_f32 v[66:67], v[62:63], v[66:67], s[40:41] op_sel_hi:[1,1,0]
	v_and_b32_e32 v61, 0x7fffffff, v59
	v_and_b32_e32 v60, 0x7fffffff, v58
	v_exp_f32_e32 v65, v53
	v_pk_mul_f32 v[62:63], v[62:63], v[66:67]
	v_fma_f32 v53, |v56|, s25, 1.0
	v_pk_mul_f32 v[60:61], v[60:61], v[62:63]
	v_rcp_f32_e32 v62, v53
	v_fma_f32 v53, |v57|, s25, 1.0
	v_rcp_f32_e32 v63, v53
	v_max_f32_e32 v58, 0, v58
	v_max_f32_e32 v59, 0, v59
	v_pk_fma_f32 v[58:59], v[64:65], v[60:61], v[58:59] neg_lo:[1,0,0] neg_hi:[1,0,0]
	v_pk_mul_f32 v[64:65], v[56:57], v[56:57]
	v_pk_fma_f32 v[66:67], v[62:63], s[22:23], v[90:91] op_sel_hi:[1,0,0]
	v_mul_f32_e32 v53, 0xbf38aa3b, v64
	v_exp_f32_e32 v64, v53
	v_pk_fma_f32 v[66:67], v[62:63], v[66:67], s[24:25] op_sel_hi:[1,1,0]
	v_mul_f32_e32 v53, 0xbf38aa3b, v65
	v_pk_fma_f32 v[66:67], v[62:63], v[66:67], s[34:35] op_sel_hi:[1,1,0]
	v_exp_f32_e32 v65, v53
	v_pk_fma_f32 v[66:67], v[62:63], v[66:67], s[40:41] op_sel_hi:[1,1,0]
	v_and_b32_e32 v61, 0x7fffffff, v57
	v_and_b32_e32 v60, 0x7fffffff, v56
	v_pk_mul_f32 v[62:63], v[62:63], v[66:67]
	v_readlane_b32 s0, v52, 7
	v_max_f32_e32 v56, 0, v56
	v_max_f32_e32 v57, 0, v57
	v_pk_mul_f32 v[60:61], v[60:61], v[62:63]
	v_pk_mul_f32 v[52:53], s[0:1], v[54:55] op_sel_hi:[0,1]
	v_pk_fma_f32 v[56:57], v[64:65], v[60:61], v[56:57] neg_lo:[1,0,0] neg_hi:[1,0,0]
	v_pk_fma_f32 v[52:53], v[52:53], v[238:239], v[242:243]
	v_cvt_pk_f16_f32 v58, v58, v59
	v_cvt_pk_f16_f32 v59, v56, v57
	v_fma_f32 v56, |v52|, s25, 1.0
	v_fma_f32 v57, |v53|, s25, 1.0
	v_rcp_f32_e32 v56, v56
	v_rcp_f32_e32 v57, v57
	ds_write_b64 v118, v[58:59] offset:35840
	v_pk_mul_f32 v[58:59], v[52:53], v[52:53]
	v_and_b32_e32 v55, 0x7fffffff, v53
	v_pk_fma_f32 v[60:61], v[56:57], s[22:23], v[90:91] op_sel_hi:[1,0,0]
	v_mul_f32_e32 v58, 0xbf38aa3b, v58
	v_pk_fma_f32 v[60:61], v[56:57], v[60:61], s[24:25] op_sel_hi:[1,1,0]
	v_mul_f32_e32 v59, 0xbf38aa3b, v59
	v_exp_f32_e32 v58, v58
	v_pk_fma_f32 v[60:61], v[56:57], v[60:61], s[34:35] op_sel_hi:[1,1,0]
	v_exp_f32_e32 v59, v59
	v_pk_fma_f32 v[60:61], v[56:57], v[60:61], s[40:41] op_sel_hi:[1,1,0]
	v_and_b32_e32 v54, 0x7fffffff, v52
	v_pk_mul_f32 v[56:57], v[56:57], v[60:61]
	v_max_f32_e32 v52, 0, v52
	v_max_f32_e32 v53, 0, v53
	v_pk_mul_f32 v[54:55], v[54:55], v[56:57]
	v_pk_mul_f32 v[50:51], s[0:1], v[50:51] op_sel_hi:[0,1]
	v_pk_fma_f32 v[52:53], v[58:59], v[54:55], v[52:53] neg_lo:[1,0,0] neg_hi:[1,0,0]
	v_pk_fma_f32 v[50:51], v[50:51], v[240:241], v[244:245]
	v_cvt_pk_f16_f32 v52, v52, v53
	v_fma_f32 v53, |v50|, s25, 1.0
	v_rcp_f32_e32 v56, v53
	v_fma_f32 v53, |v51|, s25, 1.0
	v_rcp_f32_e32 v57, v53
	v_pk_mul_f32 v[58:59], v[50:51], v[50:51]
	v_and_b32_e32 v55, 0x7fffffff, v51
	v_mul_f32_e32 v53, 0xbf38aa3b, v58
	v_pk_fma_f32 v[60:61], v[56:57], s[22:23], v[90:91] op_sel_hi:[1,0,0]
	v_exp_f32_e32 v58, v53
	v_pk_fma_f32 v[60:61], v[56:57], v[60:61], s[24:25] op_sel_hi:[1,1,0]
	v_mul_f32_e32 v53, 0xbf38aa3b, v59
	v_pk_fma_f32 v[60:61], v[56:57], v[60:61], s[34:35] op_sel_hi:[1,1,0]
	v_exp_f32_e32 v59, v53
	v_pk_fma_f32 v[60:61], v[56:57], v[60:61], s[40:41] op_sel_hi:[1,1,0]
	v_and_b32_e32 v54, 0x7fffffff, v50
	v_pk_mul_f32 v[56:57], v[56:57], v[60:61]
	v_max_f32_e32 v50, 0, v50
	v_max_f32_e32 v51, 0, v51
	v_pk_mul_f32 v[54:55], v[54:55], v[56:57]
	s_movk_i32 s0, 0x70
	v_pk_fma_f32 v[50:51], v[58:59], v[54:55], v[50:51] neg_lo:[1,0,0] neg_hi:[1,0,0]
	s_waitcnt vmcnt(0)
	v_add_f32_e32 v96, v24, v25
	v_cvt_pk_f16_f32 v53, v50, v51
	v_bitop3_b32 v50, v86, s0, v88 bitop3:0x6c
	s_movk_i32 s0, 0x4000
	v_add_co_u32_e32 v92, vcc, s0, v82
	s_movk_i32 s0, 0x5000
	s_nop 0
	v_addc_co_u32_e32 v93, vcc, 0, v83, vcc
	v_or3_b32 v144, v85, v50, v87
	v_add_co_u32_e32 v94, vcc, s0, v82
	ds_write_b64 v144, v[52:53] offset:36352
	s_nop 0
	v_addc_co_u32_e32 v95, vcc, 0, v83, vcc
	s_movk_i32 s56, 0x5000
	v_add_co_u32_e64 v234, s[58:59], s56, v82
	s_nop 1
	v_addc_co_u32_e64 v235, s[58:59], 0, v83, s[58:59]
	global_load_dwordx4 v[170:173], v[234:235], off offset:-4096 nt
	global_load_dwordx4 v[174:177], v[234:235], off offset:-3072 nt
	global_load_dwordx4 v[178:181], v[234:235], off offset:-2048 nt
	global_load_dwordx4 v[182:185], v[234:235], off offset:-1024 nt
	global_load_dwordx4 v[186:189], v[234:235], off nt
	global_load_dwordx4 v[190:193], v[234:235], off offset:1024 nt
	global_load_dwordx4 v[194:197], v[234:235], off offset:2048 nt
	global_load_dwordx4 v[198:201], v[234:235], off offset:3072 nt
	v_add_f32_e32 v92, v40, v41
	v_add_f32_e32 v89, v89, v92
	v_add_f32_e32 v92, v34, v35
	v_add_f32_e32 v93, v36, v37
	v_add_f32_e32 v92, v92, v93
	v_add_f32_e32 v93, v30, v31
	v_add_f32_e32 v94, v32, v33
	v_add_f32_e32 v93, v93, v94
	v_add_f32_e32 v94, v26, v27
	v_add_f32_e32 v95, v28, v29
	v_add_f32_e32 v94, v94, v95
	v_add_f32_e32 v95, v22, v23
	v_add_f32_e32 v95, v95, v96
	v_add_f32_e32 v96, v18, v19
	v_add_f32_e32 v97, v20, v21
	v_add_f32_e32 v96, v96, v97
	v_add_f32_e32 v97, v14, v15
	v_add_f32_e32 v98, v16, v17
	v_add_f32_e32 v97, v97, v98
	v_add_f32_e32 v98, v10, v11
	v_add_f32_e32 v99, v12, v13
	v_add_f32_e32 v98, v98, v99
	v_cndmask_b32_e64 v99, v92, v89, s[4:5]
	v_cndmask_b32_e64 v89, v89, v92, s[4:5]
	v_cndmask_b32_e64 v92, v94, v93, s[4:5]
	v_cndmask_b32_e64 v93, v93, v94, s[4:5]
	v_cndmask_b32_e64 v94, v95, v96, s[4:5]
	v_add_f32_dpp v89, v99, v89 quad_perm:[1,0,3,2] row_mask:0xf bank_mask:0xf bound_ctrl:1
	v_add_f32_dpp v92, v92, v93 quad_perm:[1,0,3,2] row_mask:0xf bank_mask:0xf bound_ctrl:1
	v_cndmask_b32_e64 v93, v96, v95, s[4:5]
	v_cndmask_b32_e64 v95, v97, v98, s[4:5]
	s_movk_i32 s1, 0x80
	v_add_f32_dpp v93, v93, v94 quad_perm:[1,0,3,2] row_mask:0xf bank_mask:0xf bound_ctrl:1
	v_cndmask_b32_e64 v94, v98, v97, s[4:5]
	s_movk_i32 s23, 0x90
	s_nop 0
	v_add_f32_dpp v94, v94, v95 quad_perm:[1,0,3,2] row_mask:0xf bank_mask:0xf bound_ctrl:1
	v_cndmask_b32_e64 v95, v89, v92, s[6:7]
	v_cndmask_b32_e64 v89, v92, v89, s[6:7]
	v_cndmask_b32_e64 v92, v93, v94, s[6:7]
	v_cndmask_b32_e64 v93, v94, v93, s[6:7]
	v_add_f32_dpp v89, v95, v89 quad_perm:[2,3,0,1] row_mask:0xf bank_mask:0xf bound_ctrl:1
	s_nop 0
	v_add_f32_dpp v92, v92, v93 quad_perm:[2,3,0,1] row_mask:0xf bank_mask:0xf bound_ctrl:1
	v_cndmask_b32_e64 v93, v89, v92, s[8:9]
	v_cndmask_b32_e64 v89, v92, v89, s[8:9]
	v_mov_b32_e32 v92, v93
	s_nop 1
	v_mov_b32_dpp v92, v92 row_shl:4 row_mask:0xf bank_mask:0x5
	s_nop 1
	v_mov_b32_dpp v92, v93 row_shr:4 row_mask:0xf bank_mask:0xa
	v_add_f32_e32 v89, v89, v92
	s_nop 1
	v_add_f32_dpp v89, v89, v89 row_ror:8 row_mask:0xf bank_mask:0xf bound_ctrl:1
	v_mov_b32_e32 v92, v89
	s_nop 1
	v_permlane16_swap_b32_e32 v89, v92
	v_add_f32_e32 v89, v89, v92
	v_mov_b32_e32 v92, v89
	s_nop 1
	v_permlane32_swap_b32_e32 v89, v92
	v_add_f32_e32 v89, v89, v92
	v_mul_f32_e32 v89, 0x3b800000, v89
	v_bitop3_b32 v92, v86, s1, v88 bitop3:0x6c
	v_readlane_b32 s44, v89, 0
	v_readlane_b32 s46, v89, 1
	v_readlane_b32 s48, v89, 2
	v_pk_add_f32 v[40:41], v[40:41], s[44:45] op_sel_hi:[1,0] neg_lo:[0,1] neg_hi:[0,1]
	v_pk_add_f32 v[36:37], v[36:37], s[46:47] op_sel_hi:[1,0] neg_lo:[0,1] neg_hi:[0,1]
	v_readlane_b32 s50, v89, 3
	v_readlane_b32 s52, v89, 4
	v_readlane_b32 s54, v89, 5
	v_readlane_b32 s42, v89, 6
	v_readlane_b32 s0, v89, 7
	v_mul_f32_e32 v89, v41, v41
	v_or3_b32 v145, v85, v92, v87
	v_pk_add_f32 v[92:93], v[34:35], s[46:47] op_sel_hi:[1,0] neg_lo:[0,1] neg_hi:[0,1]
	v_mul_f32_e32 v34, v37, v37
	v_pk_add_f32 v[38:39], v[38:39], s[44:45] op_sel_hi:[1,0] neg_lo:[0,1] neg_hi:[0,1]
	v_fmac_f32_e32 v89, v40, v40
	v_fmac_f32_e32 v34, v36, v36
	v_fmac_f32_e32 v89, v39, v39
	v_fmac_f32_e32 v34, v93, v93
	v_fmac_f32_e32 v89, v38, v38
	v_fmac_f32_e32 v34, v92, v92
	v_cndmask_b32_e64 v35, v34, v89, s[4:5]
	v_cndmask_b32_e64 v34, v89, v34, s[4:5]
	s_movk_i32 s1, 0xa0
	v_pk_add_f32 v[32:33], v[32:33], s[48:49] op_sel_hi:[1,0] neg_lo:[0,1] neg_hi:[0,1]
	v_add_f32_dpp v89, v35, v34 quad_perm:[1,0,3,2] row_mask:0xf bank_mask:0xf bound_ctrl:1
	v_bitop3_b32 v34, v86, s23, v88 bitop3:0x6c
	v_or3_b32 v139, v85, v34, v87
	v_pk_add_f32 v[34:35], v[30:31], s[48:49] op_sel_hi:[1,0] neg_lo:[0,1] neg_hi:[0,1]
	v_bitop3_b32 v30, v86, s1, v88 bitop3:0x6c
	v_pk_add_f32 v[28:29], v[28:29], s[50:51] op_sel_hi:[1,0] neg_lo:[0,1] neg_hi:[0,1]
	v_mul_f32_e32 v94, v33, v33
	v_or3_b32 v137, v85, v30, v87
	v_pk_add_f32 v[30:31], v[26:27], s[50:51] op_sel_hi:[1,0] neg_lo:[0,1] neg_hi:[0,1]
	v_mul_f32_e32 v26, v29, v29
	v_fmac_f32_e32 v94, v32, v32
	v_fmac_f32_e32 v26, v28, v28
	v_fmac_f32_e32 v94, v35, v35
	v_fmac_f32_e32 v26, v31, v31
	v_fmac_f32_e32 v94, v34, v34
	v_fmac_f32_e32 v26, v30, v30
	v_cndmask_b32_e64 v27, v26, v94, s[4:5]
	v_cndmask_b32_e64 v26, v94, v26, s[4:5]
	s_movk_i32 s1, 0xb0
	v_pk_add_f32 v[24:25], v[24:25], s[52:53] op_sel_hi:[1,0] neg_lo:[0,1] neg_hi:[0,1]
	v_add_f32_dpp v26, v27, v26 quad_perm:[1,0,3,2] row_mask:0xf bank_mask:0xf bound_ctrl:1
	v_cndmask_b32_e64 v27, v89, v26, s[6:7]
	v_cndmask_b32_e64 v26, v26, v89, s[6:7]
	v_pk_add_f32 v[20:21], v[20:21], s[54:55] op_sel_hi:[1,0] neg_lo:[0,1] neg_hi:[0,1]
	v_mul_f32_e32 v94, v25, v25
	v_add_f32_dpp v89, v27, v26 quad_perm:[2,3,0,1] row_mask:0xf bank_mask:0xf bound_ctrl:1
	v_bitop3_b32 v26, v86, s1, v88 bitop3:0x6c
	s_movk_i32 s1, 0xc0
	v_or3_b32 v136, v85, v26, v87
	v_pk_add_f32 v[26:27], v[22:23], s[52:53] op_sel_hi:[1,0] neg_lo:[0,1] neg_hi:[0,1]
	v_bitop3_b32 v22, v86, s1, v88 bitop3:0x6c
	v_or3_b32 v123, v85, v22, v87
	v_pk_add_f32 v[22:23], v[18:19], s[54:55] op_sel_hi:[1,0] neg_lo:[0,1] neg_hi:[0,1]
	v_mul_f32_e32 v18, v21, v21
	v_fmac_f32_e32 v94, v24, v24
	v_fmac_f32_e32 v18, v20, v20
	v_fmac_f32_e32 v94, v27, v27
	v_fmac_f32_e32 v18, v23, v23
	v_fmac_f32_e32 v94, v26, v26
	v_fmac_f32_e32 v18, v22, v22
	v_cndmask_b32_e64 v19, v18, v94, s[4:5]
	v_cndmask_b32_e64 v18, v94, v18, s[4:5]
	v_pk_add_f32 v[16:17], v[16:17], s[42:43] op_sel_hi:[1,0] neg_lo:[0,1] neg_hi:[0,1]
	s_nop 0
	v_add_f32_dpp v94, v19, v18 quad_perm:[1,0,3,2] row_mask:0xf bank_mask:0xf bound_ctrl:1
	v_pk_add_f32 v[18:19], v[14:15], s[42:43] op_sel_hi:[1,0] neg_lo:[0,1] neg_hi:[0,1]
	v_pk_add_f32 v[14:15], v[10:11], s[0:1] op_sel_hi:[1,0] neg_lo:[0,1] neg_hi:[0,1]
	v_pk_add_f32 v[10:11], v[12:13], s[0:1] op_sel_hi:[1,0] neg_lo:[0,1] neg_hi:[0,1]
	v_mul_f32_e32 v95, v17, v17
	v_mul_f32_e32 v12, v11, v11
	v_fmac_f32_e32 v95, v16, v16
	v_fmac_f32_e32 v12, v10, v10
	v_fmac_f32_e32 v95, v19, v19
	v_fmac_f32_e32 v12, v15, v15
	v_fmac_f32_e32 v95, v18, v18
	v_fmac_f32_e32 v12, v14, v14
	v_cndmask_b32_e64 v13, v12, v95, s[4:5]
	v_cndmask_b32_e64 v12, v95, v12, s[4:5]
	s_movk_i32 s0, 0xd0
	s_nop 0
	v_add_f32_dpp v12, v13, v12 quad_perm:[1,0,3,2] row_mask:0xf bank_mask:0xf bound_ctrl:1
	v_cndmask_b32_e64 v13, v94, v12, s[6:7]
	v_cndmask_b32_e64 v12, v12, v94, s[6:7]
	s_nop 1
	v_add_f32_dpp v12, v13, v12 quad_perm:[2,3,0,1] row_mask:0xf bank_mask:0xf bound_ctrl:1
	v_cndmask_b32_e64 v13, v89, v12, s[8:9]
	v_cndmask_b32_e64 v12, v12, v89, s[8:9]
	v_mov_b32_e32 v89, v13
	s_nop 1
	v_mov_b32_dpp v89, v89 row_shl:4 row_mask:0xf bank_mask:0x5
	s_nop 1
	v_mov_b32_dpp v89, v13 row_shr:4 row_mask:0xf bank_mask:0xa
	v_add_f32_e32 v12, v12, v89
	v_bitop3_b32 v89, v86, s0, v88 bitop3:0x6c
	v_or3_b32 v133, v85, v89, v87
	v_add_f32_dpp v12, v12, v12 row_ror:8 row_mask:0xf bank_mask:0xf bound_ctrl:1
	v_mov_b32_e32 v13, v12
	s_nop 1
	v_permlane16_swap_b32_e32 v12, v13
	v_add_f32_e32 v12, v12, v13
	v_mov_b32_e32 v13, v12
	s_nop 1
	v_permlane32_swap_b32_e32 v12, v13
	v_add_f32_e32 v12, v12, v13
	v_fmamk_f32 v12, v12, 0x3b800000, v116
	v_mul_f32_e32 v13, 0x4f800000, v12
	v_cmp_gt_f32_e32 vcc, s35, v12
	s_nop 1
	v_cndmask_b32_e32 v12, v12, v13, vcc
	v_sqrt_f32_e32 v13, v12
	s_nop 0
	v_add_u32_e32 v89, -1, v13
	v_fma_f32 v94, -v89, v13, v12
	v_cmp_ge_f32_e64 s[0:1], 0, v94
	v_add_u32_e32 v94, 1, v13
	s_nop 0
	v_cndmask_b32_e64 v89, v13, v89, s[0:1]
	v_fma_f32 v13, -v94, v13, v12
	v_cmp_lt_f32_e64 s[0:1], 0, v13
	s_nop 1
	v_cndmask_b32_e64 v13, v89, v94, s[0:1]
	v_mul_f32_e32 v89, 0x37800000, v13
	v_cndmask_b32_e32 v13, v13, v89, vcc
	v_cmp_class_f32_e32 vcc, v12, v117
	s_nop 1
	v_cndmask_b32_e32 v12, v13, v12, vcc
	v_div_scale_f32 v13, s[0:1], v12, v12, 1.0
	v_rcp_f32_e32 v89, v13
	s_movk_i32 s0, 0xe0
	v_bitop3_b32 v94, v86, s0, v88 bitop3:0x6c
	v_or3_b32 v119, v85, v94, v87
	v_fma_f32 v94, -v13, v89, 1.0
	v_fmac_f32_e32 v89, v94, v89
	v_div_scale_f32 v94, vcc, 1.0, v12, 1.0
	v_mul_f32_e32 v95, v94, v89
	v_fma_f32 v96, -v13, v95, v94
	v_fmac_f32_e32 v95, v96, v89
	v_fma_f32 v13, -v13, v95, v94
	v_div_fmas_f32 v13, v13, v89, v95
	v_div_fixup_f32 v12, v13, v12, 1.0
	s_nop 0
	v_readlane_b32 s0, v12, 0
	s_nop 1
	v_pk_mul_f32 v[38:39], s[0:1], v[38:39] op_sel_hi:[0,1]
	v_pk_fma_f32 v[38:39], v[38:39], v[238:239], v[242:243]
	v_pk_mul_f32 v[40:41], s[0:1], v[40:41] op_sel_hi:[0,1]
	v_fma_f32 v13, |v38|, s25, 1.0
	v_rcp_f32_e32 v96, v13
	v_fma_f32 v13, |v39|, s25, 1.0
	v_rcp_f32_e32 v97, v13
	v_pk_mul_f32 v[98:99], v[38:39], v[38:39]
	v_pk_fma_f32 v[40:41], v[40:41], v[240:241], v[244:245]
	v_mul_f32_e32 v13, 0xbf38aa3b, v98
	v_pk_fma_f32 v[100:101], v[96:97], s[22:23], v[90:91] op_sel_hi:[1,0,0]
	v_exp_f32_e32 v98, v13
	v_pk_fma_f32 v[100:101], v[96:97], v[100:101], s[24:25] op_sel_hi:[1,1,0]
	v_mul_f32_e32 v13, 0xbf38aa3b, v99
	v_pk_fma_f32 v[100:101], v[96:97], v[100:101], s[34:35] op_sel_hi:[1,1,0]
	v_and_b32_e32 v95, 0x7fffffff, v39
	v_pk_fma_f32 v[100:101], v[96:97], v[100:101], s[40:41] op_sel_hi:[1,1,0]
	v_and_b32_e32 v94, 0x7fffffff, v38
	v_exp_f32_e32 v99, v13
	v_pk_mul_f32 v[96:97], v[96:97], v[100:101]
	v_fma_f32 v13, |v40|, s25, 1.0
	v_pk_mul_f32 v[94:95], v[94:95], v[96:97]
	v_rcp_f32_e32 v96, v13
	v_fma_f32 v13, |v41|, s25, 1.0
	v_rcp_f32_e32 v97, v13
	v_max_f32_e32 v38, 0, v38
	v_max_f32_e32 v39, 0, v39
	v_pk_fma_f32 v[38:39], v[98:99], v[94:95], v[38:39] neg_lo:[1,0,0] neg_hi:[1,0,0]
	v_pk_mul_f32 v[98:99], v[40:41], v[40:41]
	v_pk_fma_f32 v[100:101], v[96:97], s[22:23], v[90:91] op_sel_hi:[1,0,0]
	v_mul_f32_e32 v13, 0xbf38aa3b, v98
	v_exp_f32_e32 v98, v13
	v_pk_fma_f32 v[100:101], v[96:97], v[100:101], s[24:25] op_sel_hi:[1,1,0]
	v_mul_f32_e32 v13, 0xbf38aa3b, v99
	v_pk_fma_f32 v[100:101], v[96:97], v[100:101], s[34:35] op_sel_hi:[1,1,0]
	v_exp_f32_e32 v99, v13
	v_pk_fma_f32 v[100:101], v[96:97], v[100:101], s[40:41] op_sel_hi:[1,1,0]
	v_and_b32_e32 v95, 0x7fffffff, v41
	v_and_b32_e32 v94, 0x7fffffff, v40
	v_pk_mul_f32 v[96:97], v[96:97], v[100:101]
	v_max_f32_e32 v40, 0, v40
	v_max_f32_e32 v41, 0, v41
	v_pk_mul_f32 v[94:95], v[94:95], v[96:97]
	v_cvt_pk_f16_f32 v38, v38, v39
	v_pk_fma_f32 v[40:41], v[98:99], v[94:95], v[40:41] neg_lo:[1,0,0] neg_hi:[1,0,0]
	v_readlane_b32 s0, v12, 1
	v_cvt_pk_f16_f32 v39, v40, v41
	ds_write_b64 v145, v[38:39] offset:36864
	v_pk_mul_f32 v[38:39], s[0:1], v[92:93] op_sel_hi:[0,1]
	v_pk_fma_f32 v[38:39], v[38:39], v[238:239], v[242:243]
	v_pk_mul_f32 v[36:37], s[0:1], v[36:37] op_sel_hi:[0,1]
	v_fma_f32 v13, |v38|, s25, 1.0
	v_rcp_f32_e32 v92, v13
	v_fma_f32 v13, |v39|, s25, 1.0
	v_rcp_f32_e32 v93, v13
	v_pk_mul_f32 v[94:95], v[38:39], v[38:39]
	v_pk_fma_f32 v[36:37], v[36:37], v[240:241], v[244:245]
	v_mul_f32_e32 v13, 0xbf38aa3b, v94
	v_pk_fma_f32 v[96:97], v[92:93], s[22:23], v[90:91] op_sel_hi:[1,0,0]
	v_exp_f32_e32 v94, v13
	v_pk_fma_f32 v[96:97], v[92:93], v[96:97], s[24:25] op_sel_hi:[1,1,0]
	v_mul_f32_e32 v13, 0xbf38aa3b, v95
	v_pk_fma_f32 v[96:97], v[92:93], v[96:97], s[34:35] op_sel_hi:[1,1,0]
	v_and_b32_e32 v41, 0x7fffffff, v39
	v_pk_fma_f32 v[96:97], v[92:93], v[96:97], s[40:41] op_sel_hi:[1,1,0]
	v_and_b32_e32 v40, 0x7fffffff, v38
	v_exp_f32_e32 v95, v13
	v_pk_mul_f32 v[92:93], v[92:93], v[96:97]
	v_fma_f32 v13, |v36|, s25, 1.0
	v_pk_mul_f32 v[40:41], v[40:41], v[92:93]
	v_rcp_f32_e32 v92, v13
	v_fma_f32 v13, |v37|, s25, 1.0
	v_rcp_f32_e32 v93, v13
	v_max_f32_e32 v38, 0, v38
	v_max_f32_e32 v39, 0, v39
	v_pk_fma_f32 v[38:39], v[94:95], v[40:41], v[38:39] neg_lo:[1,0,0] neg_hi:[1,0,0]
	v_pk_mul_f32 v[94:95], v[36:37], v[36:37]
	v_pk_fma_f32 v[96:97], v[92:93], s[22:23], v[90:91] op_sel_hi:[1,0,0]
	v_mul_f32_e32 v13, 0xbf38aa3b, v94
	v_exp_f32_e32 v94, v13
	v_pk_fma_f32 v[96:97], v[92:93], v[96:97], s[24:25] op_sel_hi:[1,1,0]
	v_mul_f32_e32 v13, 0xbf38aa3b, v95
	v_pk_fma_f32 v[96:97], v[92:93], v[96:97], s[34:35] op_sel_hi:[1,1,0]
	v_exp_f32_e32 v95, v13
	v_pk_fma_f32 v[96:97], v[92:93], v[96:97], s[40:41] op_sel_hi:[1,1,0]
	v_and_b32_e32 v41, 0x7fffffff, v37
	v_and_b32_e32 v40, 0x7fffffff, v36
	v_pk_mul_f32 v[92:93], v[92:93], v[96:97]
	v_readlane_b32 s0, v12, 2
	v_max_f32_e32 v36, 0, v36
	v_max_f32_e32 v37, 0, v37
	v_pk_mul_f32 v[40:41], v[40:41], v[92:93]
	v_pk_mul_f32 v[34:35], s[0:1], v[34:35] op_sel_hi:[0,1]
	v_pk_fma_f32 v[36:37], v[94:95], v[40:41], v[36:37] neg_lo:[1,0,0] neg_hi:[1,0,0]
	v_pk_fma_f32 v[34:35], v[34:35], v[238:239], v[242:243]
	v_cvt_pk_f16_f32 v38, v38, v39
	v_cvt_pk_f16_f32 v39, v36, v37
	v_fma_f32 v13, |v34|, s25, 1.0
	ds_write_b64 v139, v[38:39] offset:37376
	v_rcp_f32_e32 v38, v13
	v_fma_f32 v13, |v35|, s25, 1.0
	v_rcp_f32_e32 v39, v13
	v_pk_mul_f32 v[40:41], v[34:35], v[34:35]
	v_pk_mul_f32 v[32:33], s[0:1], v[32:33] op_sel_hi:[0,1]
	v_mul_f32_e32 v13, 0xbf38aa3b, v40
	v_pk_fma_f32 v[92:93], v[38:39], s[22:23], v[90:91] op_sel_hi:[1,0,0]
	v_exp_f32_e32 v40, v13
	v_pk_fma_f32 v[92:93], v[38:39], v[92:93], s[24:25] op_sel_hi:[1,1,0]
	v_mul_f32_e32 v13, 0xbf38aa3b, v41
	v_pk_fma_f32 v[92:93], v[38:39], v[92:93], s[34:35] op_sel_hi:[1,1,0]
	v_pk_fma_f32 v[32:33], v[32:33], v[240:241], v[244:245]
	v_pk_fma_f32 v[92:93], v[38:39], v[92:93], s[40:41] op_sel_hi:[1,1,0]
	v_and_b32_e32 v37, 0x7fffffff, v35
	v_and_b32_e32 v36, 0x7fffffff, v34
	v_exp_f32_e32 v41, v13
	v_pk_mul_f32 v[38:39], v[38:39], v[92:93]
	v_fma_f32 v13, |v32|, s25, 1.0
	v_pk_mul_f32 v[36:37], v[36:37], v[38:39]
	v_rcp_f32_e32 v38, v13
	v_fma_f32 v13, |v33|, s25, 1.0
	v_rcp_f32_e32 v39, v13
	v_max_f32_e32 v34, 0, v34
	v_max_f32_e32 v35, 0, v35
	v_pk_fma_f32 v[34:35], v[40:41], v[36:37], v[34:35] neg_lo:[1,0,0] neg_hi:[1,0,0]
	v_pk_mul_f32 v[40:41], v[32:33], v[32:33]
	v_pk_fma_f32 v[92:93], v[38:39], s[22:23], v[90:91] op_sel_hi:[1,0,0]
	v_mul_f32_e32 v13, 0xbf38aa3b, v40
	v_exp_f32_e32 v40, v13
	v_pk_fma_f32 v[92:93], v[38:39], v[92:93], s[24:25] op_sel_hi:[1,1,0]
	v_mul_f32_e32 v13, 0xbf38aa3b, v41
	v_pk_fma_f32 v[92:93], v[38:39], v[92:93], s[34:35] op_sel_hi:[1,1,0]
	v_exp_f32_e32 v41, v13
	v_pk_fma_f32 v[92:93], v[38:39], v[92:93], s[40:41] op_sel_hi:[1,1,0]
	v_and_b32_e32 v37, 0x7fffffff, v33
	v_and_b32_e32 v36, 0x7fffffff, v32
	v_pk_mul_f32 v[38:39], v[38:39], v[92:93]
	v_readlane_b32 s0, v12, 3
	v_max_f32_e32 v32, 0, v32
	v_max_f32_e32 v33, 0, v33
	v_pk_mul_f32 v[36:37], v[36:37], v[38:39]
	v_pk_mul_f32 v[30:31], s[0:1], v[30:31] op_sel_hi:[0,1]
	v_pk_fma_f32 v[32:33], v[40:41], v[36:37], v[32:33] neg_lo:[1,0,0] neg_hi:[1,0,0]
	v_pk_fma_f32 v[30:31], v[30:31], v[238:239], v[242:243]
	v_cvt_pk_f16_f32 v34, v34, v35
	v_cvt_pk_f16_f32 v35, v32, v33
	v_fma_f32 v13, |v30|, s25, 1.0
	ds_write_b64 v137, v[34:35] offset:37888
	v_rcp_f32_e32 v34, v13
	v_fma_f32 v13, |v31|, s25, 1.0
	v_rcp_f32_e32 v35, v13
	v_pk_mul_f32 v[36:37], v[30:31], v[30:31]
	v_pk_mul_f32 v[28:29], s[0:1], v[28:29] op_sel_hi:[0,1]
	v_mul_f32_e32 v13, 0xbf38aa3b, v36
	v_pk_fma_f32 v[38:39], v[34:35], s[22:23], v[90:91] op_sel_hi:[1,0,0]
	v_exp_f32_e32 v36, v13
	v_pk_fma_f32 v[38:39], v[34:35], v[38:39], s[24:25] op_sel_hi:[1,1,0]
	v_mul_f32_e32 v13, 0xbf38aa3b, v37
	v_pk_fma_f32 v[38:39], v[34:35], v[38:39], s[34:35] op_sel_hi:[1,1,0]
	v_pk_fma_f32 v[28:29], v[28:29], v[240:241], v[244:245]
	v_pk_fma_f32 v[38:39], v[34:35], v[38:39], s[40:41] op_sel_hi:[1,1,0]
	v_and_b32_e32 v33, 0x7fffffff, v31
	v_and_b32_e32 v32, 0x7fffffff, v30
	v_exp_f32_e32 v37, v13
	v_pk_mul_f32 v[34:35], v[34:35], v[38:39]
	v_fma_f32 v13, |v28|, s25, 1.0
	v_pk_mul_f32 v[32:33], v[32:33], v[34:35]
	v_rcp_f32_e32 v34, v13
	v_fma_f32 v13, |v29|, s25, 1.0
	v_rcp_f32_e32 v35, v13
	v_max_f32_e32 v30, 0, v30
	v_max_f32_e32 v31, 0, v31
	v_pk_fma_f32 v[30:31], v[36:37], v[32:33], v[30:31] neg_lo:[1,0,0] neg_hi:[1,0,0]
	v_pk_mul_f32 v[36:37], v[28:29], v[28:29]
	v_pk_fma_f32 v[38:39], v[34:35], s[22:23], v[90:91] op_sel_hi:[1,0,0]
	v_mul_f32_e32 v13, 0xbf38aa3b, v36
	v_exp_f32_e32 v36, v13
	v_pk_fma_f32 v[38:39], v[34:35], v[38:39], s[24:25] op_sel_hi:[1,1,0]
	v_mul_f32_e32 v13, 0xbf38aa3b, v37
	v_pk_fma_f32 v[38:39], v[34:35], v[38:39], s[34:35] op_sel_hi:[1,1,0]
	v_exp_f32_e32 v37, v13
	v_pk_fma_f32 v[38:39], v[34:35], v[38:39], s[40:41] op_sel_hi:[1,1,0]
	v_and_b32_e32 v33, 0x7fffffff, v29
	v_and_b32_e32 v32, 0x7fffffff, v28
	v_pk_mul_f32 v[34:35], v[34:35], v[38:39]
	v_readlane_b32 s0, v12, 4
	v_max_f32_e32 v28, 0, v28
	v_max_f32_e32 v29, 0, v29
	v_pk_mul_f32 v[32:33], v[32:33], v[34:35]
	v_pk_mul_f32 v[26:27], s[0:1], v[26:27] op_sel_hi:[0,1]
	v_pk_fma_f32 v[28:29], v[36:37], v[32:33], v[28:29] neg_lo:[1,0,0] neg_hi:[1,0,0]
	v_pk_fma_f32 v[26:27], v[26:27], v[238:239], v[242:243]
	v_cvt_pk_f16_f32 v30, v30, v31
	v_cvt_pk_f16_f32 v31, v28, v29
	v_fma_f32 v13, |v26|, s25, 1.0
	ds_write_b64 v136, v[30:31] offset:38400
	v_rcp_f32_e32 v30, v13
	v_fma_f32 v13, |v27|, s25, 1.0
	v_rcp_f32_e32 v31, v13
	v_pk_mul_f32 v[32:33], v[26:27], v[26:27]
	v_pk_mul_f32 v[24:25], s[0:1], v[24:25] op_sel_hi:[0,1]
	v_mul_f32_e32 v13, 0xbf38aa3b, v32
	v_pk_fma_f32 v[34:35], v[30:31], s[22:23], v[90:91] op_sel_hi:[1,0,0]
	v_exp_f32_e32 v32, v13
	v_pk_fma_f32 v[34:35], v[30:31], v[34:35], s[24:25] op_sel_hi:[1,1,0]
	v_mul_f32_e32 v13, 0xbf38aa3b, v33
	v_pk_fma_f32 v[34:35], v[30:31], v[34:35], s[34:35] op_sel_hi:[1,1,0]
	v_pk_fma_f32 v[24:25], v[24:25], v[240:241], v[244:245]
	v_pk_fma_f32 v[34:35], v[30:31], v[34:35], s[40:41] op_sel_hi:[1,1,0]
	v_and_b32_e32 v29, 0x7fffffff, v27
	v_and_b32_e32 v28, 0x7fffffff, v26
	v_exp_f32_e32 v33, v13
	v_pk_mul_f32 v[30:31], v[30:31], v[34:35]
	v_fma_f32 v13, |v24|, s25, 1.0
	v_pk_mul_f32 v[28:29], v[28:29], v[30:31]
	v_rcp_f32_e32 v30, v13
	v_fma_f32 v13, |v25|, s25, 1.0
	v_rcp_f32_e32 v31, v13
	v_max_f32_e32 v26, 0, v26
	v_max_f32_e32 v27, 0, v27
	v_pk_fma_f32 v[26:27], v[32:33], v[28:29], v[26:27] neg_lo:[1,0,0] neg_hi:[1,0,0]
	v_pk_mul_f32 v[32:33], v[24:25], v[24:25]
	v_pk_fma_f32 v[34:35], v[30:31], s[22:23], v[90:91] op_sel_hi:[1,0,0]
	v_mul_f32_e32 v13, 0xbf38aa3b, v32
	v_exp_f32_e32 v32, v13
	v_pk_fma_f32 v[34:35], v[30:31], v[34:35], s[24:25] op_sel_hi:[1,1,0]
	v_mul_f32_e32 v13, 0xbf38aa3b, v33
	v_pk_fma_f32 v[34:35], v[30:31], v[34:35], s[34:35] op_sel_hi:[1,1,0]
	v_exp_f32_e32 v33, v13
	v_pk_fma_f32 v[34:35], v[30:31], v[34:35], s[40:41] op_sel_hi:[1,1,0]
	v_and_b32_e32 v29, 0x7fffffff, v25
	v_and_b32_e32 v28, 0x7fffffff, v24
	v_pk_mul_f32 v[30:31], v[30:31], v[34:35]
	v_readlane_b32 s0, v12, 5
	v_max_f32_e32 v24, 0, v24
	v_max_f32_e32 v25, 0, v25
	v_pk_mul_f32 v[28:29], v[28:29], v[30:31]
	v_pk_mul_f32 v[22:23], s[0:1], v[22:23] op_sel_hi:[0,1]
	v_pk_fma_f32 v[24:25], v[32:33], v[28:29], v[24:25] neg_lo:[1,0,0] neg_hi:[1,0,0]
	v_pk_fma_f32 v[22:23], v[22:23], v[238:239], v[242:243]
	v_cvt_pk_f16_f32 v26, v26, v27
	v_cvt_pk_f16_f32 v27, v24, v25
	v_fma_f32 v13, |v22|, s25, 1.0
	ds_write_b64 v123, v[26:27] offset:38912
	v_rcp_f32_e32 v26, v13
	v_fma_f32 v13, |v23|, s25, 1.0
	v_rcp_f32_e32 v27, v13
	v_pk_mul_f32 v[28:29], v[22:23], v[22:23]
	v_pk_mul_f32 v[20:21], s[0:1], v[20:21] op_sel_hi:[0,1]
	v_mul_f32_e32 v13, 0xbf38aa3b, v28
	v_pk_fma_f32 v[30:31], v[26:27], s[22:23], v[90:91] op_sel_hi:[1,0,0]
	v_exp_f32_e32 v28, v13
	v_pk_fma_f32 v[30:31], v[26:27], v[30:31], s[24:25] op_sel_hi:[1,1,0]
	v_mul_f32_e32 v13, 0xbf38aa3b, v29
	v_pk_fma_f32 v[30:31], v[26:27], v[30:31], s[34:35] op_sel_hi:[1,1,0]
	v_pk_fma_f32 v[20:21], v[20:21], v[240:241], v[244:245]
	v_pk_fma_f32 v[30:31], v[26:27], v[30:31], s[40:41] op_sel_hi:[1,1,0]
	s_waitcnt vmcnt(7)
	v_add_f32_e32 v92, v170, v171
	v_add_f32_e32 v93, v172, v173
	v_and_b32_e32 v25, 0x7fffffff, v23
	v_and_b32_e32 v24, 0x7fffffff, v22
	v_exp_f32_e32 v29, v13
	v_pk_mul_f32 v[26:27], v[26:27], v[30:31]
	v_fma_f32 v13, |v20|, s25, 1.0
	v_add_f32_e32 v92, v92, v93
	s_waitcnt vmcnt(6)
	v_add_f32_e32 v93, v174, v175
	v_add_f32_e32 v94, v176, v177
	v_pk_mul_f32 v[24:25], v[24:25], v[26:27]
	v_rcp_f32_e32 v26, v13
	v_fma_f32 v13, |v21|, s25, 1.0
	v_add_f32_e32 v93, v93, v94
	s_waitcnt vmcnt(5)
	v_add_f32_e32 v94, v178, v179
	v_add_f32_e32 v95, v180, v181
	v_rcp_f32_e32 v27, v13
	v_add_f32_e32 v94, v94, v95
	s_waitcnt vmcnt(4)
	v_add_f32_e32 v95, v182, v183
	v_add_f32_e32 v96, v184, v185
	v_add_f32_e32 v95, v95, v96
	s_waitcnt vmcnt(3)
	v_add_f32_e32 v96, v186, v187
	v_add_f32_e32 v97, v188, v189
	v_max_f32_e32 v22, 0, v22
	v_max_f32_e32 v23, 0, v23
	v_add_f32_e32 v96, v96, v97
	s_waitcnt vmcnt(2)
	v_add_f32_e32 v97, v190, v191
	v_add_f32_e32 v98, v192, v193
	v_pk_fma_f32 v[22:23], v[28:29], v[24:25], v[22:23] neg_lo:[1,0,0] neg_hi:[1,0,0]
	v_pk_mul_f32 v[28:29], v[20:21], v[20:21]
	v_add_f32_e32 v97, v97, v98
	s_waitcnt vmcnt(1)
	v_add_f32_e32 v98, v194, v195
	v_add_f32_e32 v99, v196, v197
	v_mul_f32_e32 v13, 0xbf38aa3b, v28
	v_pk_fma_f32 v[30:31], v[26:27], s[22:23], v[90:91] op_sel_hi:[1,0,0]
	v_add_f32_e32 v98, v98, v99
	s_waitcnt vmcnt(0)
	v_add_f32_e32 v99, v198, v199
	v_add_f32_e32 v100, v200, v201
	v_exp_f32_e32 v28, v13
	v_pk_fma_f32 v[30:31], v[26:27], v[30:31], s[24:25] op_sel_hi:[1,1,0]
	v_mul_f32_e32 v13, 0xbf38aa3b, v29
	v_add_f32_e32 v99, v99, v100
	v_cndmask_b32_e64 v100, v93, v92, s[4:5]
	v_cndmask_b32_e64 v92, v92, v93, s[4:5]
	v_cndmask_b32_e64 v93, v95, v94, s[4:5]
	v_cndmask_b32_e64 v94, v94, v95, s[4:5]
	v_pk_fma_f32 v[30:31], v[26:27], v[30:31], s[34:35] op_sel_hi:[1,1,0]
	v_exp_f32_e32 v29, v13
	v_add_f32_dpp v93, v93, v94 quad_perm:[1,0,3,2] row_mask:0xf bank_mask:0xf bound_ctrl:1
	v_cndmask_b32_e64 v94, v97, v96, s[4:5]
	v_cndmask_b32_e64 v95, v96, v97, s[4:5]
	v_pk_fma_f32 v[30:31], v[26:27], v[30:31], s[40:41] op_sel_hi:[1,1,0]
	v_cndmask_b32_e64 v96, v98, v99, s[4:5]
	v_add_f32_dpp v94, v94, v95 quad_perm:[1,0,3,2] row_mask:0xf bank_mask:0xf bound_ctrl:1
	v_cndmask_b32_e64 v95, v99, v98, s[4:5]
	v_and_b32_e32 v25, 0x7fffffff, v21
	v_and_b32_e32 v24, 0x7fffffff, v20
	v_pk_mul_f32 v[26:27], v[26:27], v[30:31]
	v_readlane_b32 s0, v12, 6
	v_add_f32_dpp v92, v100, v92 quad_perm:[1,0,3,2] row_mask:0xf bank_mask:0xf bound_ctrl:1
	v_add_f32_dpp v95, v95, v96 quad_perm:[1,0,3,2] row_mask:0xf bank_mask:0xf bound_ctrl:1
	v_max_f32_e32 v20, 0, v20
	v_max_f32_e32 v21, 0, v21
	v_pk_mul_f32 v[24:25], v[24:25], v[26:27]
	v_pk_mul_f32 v[18:19], s[0:1], v[18:19] op_sel_hi:[0,1]
	v_cndmask_b32_e64 v96, v92, v93, s[6:7]
	v_cndmask_b32_e64 v92, v93, v92, s[6:7]
	v_cndmask_b32_e64 v93, v94, v95, s[6:7]
	v_cndmask_b32_e64 v94, v95, v94, s[6:7]
	v_pk_fma_f32 v[20:21], v[28:29], v[24:25], v[20:21] neg_lo:[1,0,0] neg_hi:[1,0,0]
	v_pk_fma_f32 v[18:19], v[18:19], v[238:239], v[242:243]
	v_add_f32_dpp v92, v96, v92 quad_perm:[2,3,0,1] row_mask:0xf bank_mask:0xf bound_ctrl:1
	v_add_f32_dpp v93, v93, v94 quad_perm:[2,3,0,1] row_mask:0xf bank_mask:0xf bound_ctrl:1
	v_cvt_pk_f16_f32 v22, v22, v23
	v_cvt_pk_f16_f32 v23, v20, v21
	v_fma_f32 v13, |v18|, s25, 1.0
	v_cndmask_b32_e64 v94, v92, v93, s[8:9]
	ds_write_b64 v133, v[22:23] offset:39424
	v_rcp_f32_e32 v22, v13
	v_fma_f32 v13, |v19|, s25, 1.0
	v_cndmask_b32_e64 v92, v93, v92, s[8:9]
	v_mov_b32_e32 v93, v94
	v_rcp_f32_e32 v23, v13
	v_pk_mul_f32 v[24:25], v[18:19], v[18:19]
	v_mov_b32_dpp v93, v93 row_shl:4 row_mask:0xf bank_mask:0x5
	v_mul_f32_e32 v13, 0xbf38aa3b, v24
	v_pk_fma_f32 v[26:27], v[22:23], s[22:23], v[90:91] op_sel_hi:[1,0,0]
	v_mov_b32_dpp v93, v94 row_shr:4 row_mask:0xf bank_mask:0xa
	v_add_f32_e32 v92, v92, v93
	v_pk_fma_f32 v[26:27], v[22:23], v[26:27], s[24:25] op_sel_hi:[1,1,0]
	v_pk_mul_f32 v[16:17], s[0:1], v[16:17] op_sel_hi:[0,1]
	v_add_f32_dpp v92, v92, v92 row_ror:8 row_mask:0xf bank_mask:0xf bound_ctrl:1
	v_mov_b32_e32 v93, v92
	s_nop 1
	v_permlane16_swap_b32_e32 v92, v93
	v_pk_fma_f32 v[26:27], v[22:23], v[26:27], s[34:35] op_sel_hi:[1,1,0]
	v_add_f32_e32 v92, v92, v93
	v_exp_f32_e32 v24, v13
	v_pk_fma_f32 v[26:27], v[22:23], v[26:27], s[40:41] op_sel_hi:[1,1,0]
	v_mul_f32_e32 v13, 0xbf38aa3b, v25
	v_pk_fma_f32 v[16:17], v[16:17], v[240:241], v[244:245]
	v_mov_b32_e32 v93, v92
	v_and_b32_e32 v21, 0x7fffffff, v19
	v_and_b32_e32 v20, 0x7fffffff, v18
	v_exp_f32_e32 v25, v13
	v_pk_mul_f32 v[22:23], v[22:23], v[26:27]
	v_fma_f32 v13, |v16|, s25, 1.0
	v_permlane32_swap_b32_e32 v92, v93
	v_pk_mul_f32 v[20:21], v[20:21], v[22:23]
	v_rcp_f32_e32 v22, v13
	v_fma_f32 v13, |v17|, s25, 1.0
	v_add_f32_e32 v92, v92, v93
	v_rcp_f32_e32 v23, v13
	v_mul_f32_e32 v92, 0x3b800000, v92
	v_max_f32_e32 v18, 0, v18
	v_max_f32_e32 v19, 0, v19
	v_readlane_b32 s42, v92, 0
	v_readlane_b32 s44, v92, 1
	v_readlane_b32 s46, v92, 2
	v_readlane_b32 s48, v92, 3
	v_pk_fma_f32 v[18:19], v[24:25], v[20:21], v[18:19] neg_lo:[1,0,0] neg_hi:[1,0,0]
	v_pk_mul_f32 v[24:25], v[16:17], v[16:17]
	v_pk_add_f32 v[160:161], v[172:173], s[42:43] op_sel_hi:[1, 0] neg_lo:[0, 1] neg_hi:[0, 1]
	v_pk_add_f32 v[110:111], v[176:177], s[44:45] op_sel_hi:[1, 0] neg_lo:[0, 1] neg_hi:[0, 1]
	v_pk_add_f32 v[104:105], v[180:181], s[46:47] op_sel_hi:[1, 0] neg_lo:[0, 1] neg_hi:[0, 1]
	v_pk_add_f32 v[100:101], v[184:185], s[48:49] op_sel_hi:[1, 0] neg_lo:[0, 1] neg_hi:[0, 1]
	v_mul_f32_e32 v13, 0xbf38aa3b, v24
	v_pk_add_f32 v[158:159], v[170:171], s[42:43] op_sel_hi:[1, 0] neg_lo:[0, 1] neg_hi:[0, 1]
	v_mul_f32_e32 v78, v161, v161
	v_pk_add_f32 v[162:163], v[174:175], s[44:45] op_sel_hi:[1, 0] neg_lo:[0, 1] neg_hi:[0, 1]
	v_mul_f32_e32 v74, v111, v111
	v_pk_add_f32 v[108:109], v[178:179], s[46:47] op_sel_hi:[1, 0] neg_lo:[0, 1] neg_hi:[0, 1]
	v_mul_f32_e32 v70, v105, v105
	v_pk_add_f32 v[102:103], v[182:183], s[48:49] op_sel_hi:[1, 0] neg_lo:[0, 1] neg_hi:[0, 1]
	v_mul_f32_e32 v66, v101, v101
	v_exp_f32_e32 v24, v13
	v_pk_fma_f32 v[26:27], v[22:23], s[22:23], v[90:91] op_sel_hi:[1,0,0]
	v_mul_f32_e32 v13, 0xbf38aa3b, v25
	v_readlane_b32 s0, v12, 7
	v_fmac_f32_e32 v78, v160, v160
	v_fmac_f32_e32 v74, v110, v110
	v_fmac_f32_e32 v70, v104, v104
	v_fmac_f32_e32 v66, v100, v100
	v_pk_fma_f32 v[26:27], v[22:23], v[26:27], s[24:25] op_sel_hi:[1,1,0]
	v_exp_f32_e32 v25, v13
	v_pk_mul_f32 v[12:13], s[0:1], v[14:15] op_sel_hi:[0,1]
	v_pk_mul_f32 v[10:11], s[0:1], v[10:11] op_sel_hi:[0,1]
	s_movk_i32 s0, 0x6000
	v_fmac_f32_e32 v78, v159, v159
	v_fmac_f32_e32 v74, v163, v163
	v_fmac_f32_e32 v70, v109, v109
	v_fmac_f32_e32 v66, v103, v103
	v_pk_fma_f32 v[26:27], v[22:23], v[26:27], s[34:35] op_sel_hi:[1,1,0]
	v_add_co_u32_e32 v154, vcc, s0, v82
	v_fmac_f32_e32 v78, v158, v158
	v_fmac_f32_e32 v74, v162, v162
	v_fmac_f32_e32 v70, v108, v108
	v_fmac_f32_e32 v66, v102, v102
	v_pk_fma_f32 v[26:27], v[22:23], v[26:27], s[40:41] op_sel_hi:[1,1,0]
	v_addc_co_u32_e32 v155, vcc, 0, v83, vcc
	s_movk_i32 s0, 0x7000
	v_cndmask_b32_e64 v75, v74, v78, s[4:5]
	v_cndmask_b32_e64 v74, v78, v74, s[4:5]
	v_cndmask_b32_e64 v67, v66, v70, s[4:5]
	v_cndmask_b32_e64 v66, v70, v66, s[4:5]
	v_and_b32_e32 v21, 0x7fffffff, v17
	v_and_b32_e32 v20, 0x7fffffff, v16
	v_pk_mul_f32 v[22:23], v[22:23], v[26:27]
	v_add_co_u32_e32 v156, vcc, s0, v82
	v_readlane_b32 s50, v92, 4
	v_readlane_b32 s52, v92, 5
	v_readlane_b32 s54, v92, 6
	v_readlane_b32 s0, v92, 7
	v_add_f32_dpp v74, v75, v74 quad_perm:[1,0,3,2] row_mask:0xf bank_mask:0xf bound_ctrl:1
	v_add_f32_dpp v66, v67, v66 quad_perm:[1,0,3,2] row_mask:0xf bank_mask:0xf bound_ctrl:1
	v_max_f32_e32 v16, 0, v16
	v_max_f32_e32 v17, 0, v17
	v_pk_mul_f32 v[20:21], v[20:21], v[22:23]
	v_cndmask_b32_e64 v67, v74, v66, s[6:7]
	v_cndmask_b32_e64 v66, v66, v74, s[6:7]
	v_pk_add_f32 v[96:97], v[188:189], s[50:51] op_sel_hi:[1, 0] neg_lo:[0, 1] neg_hi:[0, 1]
	v_pk_add_f32 v[92:93], v[192:193], s[52:53] op_sel_hi:[1, 0] neg_lo:[0, 1] neg_hi:[0, 1]
	v_pk_add_f32 v[78:79], v[196:197], s[54:55] op_sel_hi:[1, 0] neg_lo:[0, 1] neg_hi:[0, 1]
	v_pk_add_f32 v[74:75], v[200:201], s[0:1] op_sel_hi:[1, 0] neg_lo:[0, 1] neg_hi:[0, 1]
	v_pk_fma_f32 v[16:17], v[24:25], v[20:21], v[16:17] neg_lo:[1,0,0] neg_hi:[1,0,0]
	v_pk_fma_f32 v[12:13], v[12:13], v[238:239], v[242:243]
	v_pk_add_f32 v[98:99], v[186:187], s[50:51] op_sel_hi:[1, 0] neg_lo:[0, 1] neg_hi:[0, 1]
	v_mul_f32_e32 v62, v97, v97
	v_pk_add_f32 v[94:95], v[190:191], s[52:53] op_sel_hi:[1, 0] neg_lo:[0, 1] neg_hi:[0, 1]
	v_mul_f32_e32 v58, v93, v93
	v_pk_add_f32 v[80:81], v[194:195], s[54:55] op_sel_hi:[1, 0] neg_lo:[0, 1] neg_hi:[0, 1]
	v_mul_f32_e32 v54, v79, v79
	v_pk_add_f32 v[76:77], v[198:199], s[0:1] op_sel_hi:[1, 0] neg_lo:[0, 1] neg_hi:[0, 1]
	v_mul_f32_e32 v50, v75, v75
	v_cvt_pk_f16_f32 v18, v18, v19
	v_cvt_pk_f16_f32 v19, v16, v17
	v_fma_f32 v16, |v12|, s25, 1.0
	v_fma_f32 v17, |v13|, s25, 1.0
	v_fmac_f32_e32 v62, v96, v96
	v_fmac_f32_e32 v58, v92, v92
	v_fmac_f32_e32 v54, v78, v78
	v_fmac_f32_e32 v50, v74, v74
	v_rcp_f32_e32 v16, v16
	v_rcp_f32_e32 v17, v17
	v_fmac_f32_e32 v62, v99, v99
	v_fmac_f32_e32 v58, v95, v95
	v_fmac_f32_e32 v54, v81, v81
	v_fmac_f32_e32 v50, v77, v77
	v_fmac_f32_e32 v62, v98, v98
	v_fmac_f32_e32 v58, v94, v94
	v_fmac_f32_e32 v54, v80, v80
	v_fmac_f32_e32 v50, v76, v76
	v_cndmask_b32_e64 v59, v58, v62, s[4:5]
	v_cndmask_b32_e64 v58, v62, v58, s[4:5]
	v_cndmask_b32_e64 v51, v50, v54, s[4:5]
	v_cndmask_b32_e64 v50, v54, v50, s[4:5]
	v_add_f32_dpp v58, v59, v58 quad_perm:[1,0,3,2] row_mask:0xf bank_mask:0xf bound_ctrl:1
	ds_write_b64 v119, v[18:19] offset:39936
	v_add_f32_dpp v50, v51, v50 quad_perm:[1,0,3,2] row_mask:0xf bank_mask:0xf bound_ctrl:1
	v_pk_mul_f32 v[18:19], v[12:13], v[12:13]
	v_pk_fma_f32 v[20:21], v[16:17], s[22:23], v[90:91] op_sel_hi:[1,0,0]
	v_cndmask_b32_e64 v51, v58, v50, s[6:7]
	v_cndmask_b32_e64 v50, v50, v58, s[6:7]
	v_mul_f32_e32 v18, 0xbf38aa3b, v18
	v_pk_fma_f32 v[20:21], v[16:17], v[20:21], s[24:25] op_sel_hi:[1,1,0]
	v_mul_f32_e32 v19, 0xbf38aa3b, v19
	v_add_f32_dpp v66, v67, v66 quad_perm:[2,3,0,1] row_mask:0xf bank_mask:0xf bound_ctrl:1
	v_add_f32_dpp v50, v51, v50 quad_perm:[2,3,0,1] row_mask:0xf bank_mask:0xf bound_ctrl:1
	v_exp_f32_e32 v18, v18
	v_pk_fma_f32 v[20:21], v[16:17], v[20:21], s[34:35] op_sel_hi:[1,1,0]
	v_exp_f32_e32 v19, v19
	v_cndmask_b32_e64 v51, v66, v50, s[8:9]
	v_pk_fma_f32 v[20:21], v[16:17], v[20:21], s[40:41] op_sel_hi:[1,1,0]
	v_mov_b32_e32 v52, v51
	v_and_b32_e32 v15, 0x7fffffff, v13
	v_and_b32_e32 v14, 0x7fffffff, v12
	v_pk_mul_f32 v[16:17], v[16:17], v[20:21]
	v_mov_b32_dpp v52, v52 row_shl:4 row_mask:0xf bank_mask:0x5
	v_max_f32_e32 v12, 0, v12
	v_max_f32_e32 v13, 0, v13
	v_pk_mul_f32 v[14:15], v[14:15], v[16:17]
	v_cndmask_b32_e64 v50, v50, v66, s[8:9]
	v_mov_b32_dpp v52, v51 row_shr:4 row_mask:0xf bank_mask:0xa
	v_pk_fma_f32 v[12:13], v[18:19], v[14:15], v[12:13] neg_lo:[1,0,0] neg_hi:[1,0,0]
	v_pk_fma_f32 v[10:11], v[10:11], v[240:241], v[244:245]
	v_add_f32_e32 v50, v50, v52
	v_cvt_pk_f16_f32 v12, v12, v13
	v_fma_f32 v13, |v10|, s25, 1.0
	v_add_f32_dpp v50, v50, v50 row_ror:8 row_mask:0xf bank_mask:0xf bound_ctrl:1
	v_rcp_f32_e32 v16, v13
	v_fma_f32 v13, |v11|, s25, 1.0
	v_mov_b32_e32 v51, v50
	v_rcp_f32_e32 v17, v13
	s_nop 0
	v_permlane16_swap_b32_e32 v50, v51
	v_add_f32_e32 v50, v50, v51
	v_mov_b32_e32 v51, v50
	v_pk_mul_f32 v[18:19], v[10:11], v[10:11]
	s_nop 0
	v_permlane32_swap_b32_e32 v50, v51
	v_mul_f32_e32 v13, 0xbf38aa3b, v18
	v_pk_fma_f32 v[20:21], v[16:17], s[22:23], v[90:91] op_sel_hi:[1,0,0]
	v_add_f32_e32 v50, v50, v51
	v_exp_f32_e32 v18, v13
	v_pk_fma_f32 v[20:21], v[16:17], v[20:21], s[24:25] op_sel_hi:[1,1,0]
	v_mul_f32_e32 v13, 0xbf38aa3b, v19
	v_addc_co_u32_e32 v157, vcc, 0, v83, vcc
	v_fmamk_f32 v50, v50, 0x3b800000, v116
	v_pk_fma_f32 v[20:21], v[16:17], v[20:21], s[34:35] op_sel_hi:[1,1,0]
	v_exp_f32_e32 v19, v13
	v_mul_f32_e32 v51, 0x4f800000, v50
	v_cmp_gt_f32_e32 vcc, s35, v50
	v_pk_fma_f32 v[20:21], v[16:17], v[20:21], s[40:41] op_sel_hi:[1,1,0]
	v_and_b32_e32 v15, 0x7fffffff, v11
	v_cndmask_b32_e32 v50, v50, v51, vcc
	v_and_b32_e32 v14, 0x7fffffff, v10
	v_pk_mul_f32 v[16:17], v[16:17], v[20:21]
	v_sqrt_f32_e32 v51, v50
	v_max_f32_e32 v10, 0, v10
	v_max_f32_e32 v11, 0, v11
	v_pk_mul_f32 v[14:15], v[14:15], v[16:17]
	v_add_u32_e32 v52, -1, v51
	v_pk_fma_f32 v[10:11], v[18:19], v[14:15], v[10:11] neg_lo:[1,0,0] neg_hi:[1,0,0]
	v_fma_f32 v53, -v52, v51, v50
	v_cvt_pk_f16_f32 v13, v10, v11
	v_bitop3_b32 v10, v86, s41, v88 bitop3:0x6c
	v_or3_b32 v146, v85, v10, v87
	v_lshlrev_b32_e32 v10, 4, v141
	v_and_or_b32 v147, v10, s41, v84
	v_lshlrev_b32_e32 v10, 4, v142
	v_and_or_b32 v148, v10, s41, v84
	v_lshlrev_b32_e32 v10, 4, v143
	v_cmp_ge_f32_e64 s[0:1], 0, v53
	v_add_u32_e32 v53, 1, v51
	v_and_or_b32 v149, v10, s41, v84
	v_bitop3_b32 v10, v125, v0, 15 bitop3:0x78
	v_cndmask_b32_e64 v52, v51, v52, s[0:1]
	v_fma_f32 v51, -v53, v51, v50
	v_lshl_or_b32 v150, v10, 4, v84
	v_bitop3_b32 v10, v125, v107, 4 bitop3:0x36
	v_cmp_lt_f32_e64 s[0:1], 0, v51
	v_lshl_or_b32 v151, v10, 4, v84
	v_bitop3_b32 v10, v125, v107, 8 bitop3:0x36
	v_cndmask_b32_e64 v51, v52, v53, s[0:1]
	v_lshl_or_b32 v152, v10, 4, v84
	v_bitop3_b32 v10, v125, v107, 12 bitop3:0x36
	v_mul_f32_e32 v52, 0x37800000, v51
	ds_write_b64 v146, v[12:13] offset:40448
	v_lshl_or_b32 v153, v10, 4, v84
	v_cndmask_b32_e32 v51, v51, v52, vcc
	v_cmp_class_f32_e32 vcc, v50, v117
	ds_read_b128 v[38:41], v115 offset:32768
	ds_read_b128 v[34:37], v147 offset:32768
	ds_read_b128 v[30:33], v148 offset:32768
	ds_read_b128 v[26:29], v149 offset:32768
	ds_read_b128 v[22:25], v150 offset:33024
	ds_read_b128 v[18:21], v151 offset:33024
	ds_read_b128 v[14:17], v152 offset:33024
	ds_read_b128 v[10:13], v153 offset:33024
	s_movk_i32 s57, 0x7000
	s_nop 1
	v_add_co_u32_e64 v236, s[60:61], s57, v82
	s_nop 1
	v_addc_co_u32_e64 v237, s[60:61], 0, v83, s[60:61]
	s_nop 1
	global_load_dwordx4 v[206:209], v[236:237], off offset:-3072 nt
	global_load_dwordx4 v[210:213], v[236:237], off offset:-2048 nt
	global_load_dwordx4 v[214:217], v[236:237], off offset:-1024 nt
	global_load_dwordx4 v[202:205], v[236:237], off offset:-4096 nt
	global_load_dwordx4 v[218:221], v[236:237], off nt
	v_cndmask_b32_e32 v154, v51, v50, vcc
	v_div_scale_f32 v155, s[0:1], v154, v154, 1.0
	v_rcp_f32_e32 v164, v155
	global_load_dwordx4 v[222:225], v[236:237], off offset:1024 nt
	global_load_dwordx4 v[226:229], v[236:237], off offset:2048 nt
	global_load_dwordx4 v[230:233], v[236:237], off offset:3072 nt
	v_fma_f32 v156, -v155, v164, 1.0
	v_fmac_f32_e32 v164, v156, v164
	v_div_scale_f32 v156, vcc, 1.0, v154, 1.0
	v_mul_f32_e32 v157, v156, v164
	v_fma_f32 v165, -v155, v157, v156
	v_fmac_f32_e32 v157, v165, v164
	v_fma_f32 v155, -v155, v157, v156
	v_div_fmas_f32 v155, v155, v164, v157
	v_div_fixup_f32 v154, v155, v154, 1.0
	s_nop 0
	v_readlane_b32 s0, v154, 0
	s_nop 1
	v_pk_mul_f32 v[156:157], s[0:1], v[158:159] op_sel_hi:[0,1]
	v_pk_fma_f32 v[156:157], v[156:157], v[238:239], v[242:243]
	s_nop 0
	v_fma_f32 v155, |v156|, s25, 1.0
	v_rcp_f32_e32 v164, v155
	v_fma_f32 v155, |v157|, s25, 1.0
	v_rcp_f32_e32 v165, v155
	v_pk_mul_f32 v[166:167], v[156:157], v[156:157]
	v_and_b32_e32 v159, 0x7fffffff, v157
	v_mul_f32_e32 v155, 0xbf38aa3b, v166
	v_pk_fma_f32 v[168:169], v[164:165], s[22:23], v[90:91] op_sel_hi:[1,0,0]
	v_exp_f32_e32 v166, v155
	v_pk_fma_f32 v[168:169], v[164:165], v[168:169], s[24:25] op_sel_hi:[1,1,0]
	v_mul_f32_e32 v155, 0xbf38aa3b, v167
	v_pk_fma_f32 v[168:169], v[164:165], v[168:169], s[34:35] op_sel_hi:[1,1,0]
	v_exp_f32_e32 v167, v155
	v_pk_fma_f32 v[168:169], v[164:165], v[168:169], s[40:41] op_sel_hi:[1,1,0]
	v_and_b32_e32 v158, 0x7fffffff, v156
	v_pk_mul_f32 v[164:165], v[164:165], v[168:169]
	v_max_f32_e32 v156, 0, v156
	v_max_f32_e32 v157, 0, v157
	v_pk_mul_f32 v[158:159], v[158:159], v[164:165]
	s_nop 0
	v_pk_fma_f32 v[156:157], v[166:167], v[158:159], v[156:157] neg_lo:[1,0,0] neg_hi:[1,0,0]
	v_pk_mul_f32 v[158:159], s[0:1], v[160:161] op_sel_hi:[0,1]
	v_pk_fma_f32 v[158:159], v[158:159], v[240:241], v[244:245]
	v_cvt_pk_f16_f32 v156, v156, v157
	v_fma_f32 v155, |v158|, s25, 1.0
	v_rcp_f32_e32 v164, v155
	v_fma_f32 v155, |v159|, s25, 1.0
	v_rcp_f32_e32 v165, v155
	v_pk_mul_f32 v[166:167], v[158:159], v[158:159]
	v_and_b32_e32 v161, 0x7fffffff, v159
	v_mul_f32_e32 v155, 0xbf38aa3b, v166
	v_pk_fma_f32 v[168:169], v[164:165], s[22:23], v[90:91] op_sel_hi:[1,0,0]
	v_exp_f32_e32 v166, v155
	v_pk_fma_f32 v[168:169], v[164:165], v[168:169], s[24:25] op_sel_hi:[1,1,0]
	v_mul_f32_e32 v155, 0xbf38aa3b, v167
	v_pk_fma_f32 v[168:169], v[164:165], v[168:169], s[34:35] op_sel_hi:[1,1,0]
	v_exp_f32_e32 v167, v155
	v_pk_fma_f32 v[168:169], v[164:165], v[168:169], s[40:41] op_sel_hi:[1,1,0]
	v_and_b32_e32 v160, 0x7fffffff, v158
	v_pk_mul_f32 v[164:165], v[164:165], v[168:169]
	v_max_f32_e32 v158, 0, v158
	v_max_f32_e32 v159, 0, v159
	v_pk_mul_f32 v[160:161], v[160:161], v[164:165]
	v_readlane_b32 s0, v154, 1
	v_pk_fma_f32 v[158:159], v[166:167], v[160:161], v[158:159] neg_lo:[1,0,0] neg_hi:[1,0,0]
	s_nop 0
	v_cvt_pk_f16_f32 v157, v158, v159
	ds_write_b64 v140, v[156:157] offset:32768
	v_pk_mul_f32 v[156:157], s[0:1], v[162:163] op_sel_hi:[0,1]
	v_pk_fma_f32 v[156:157], v[156:157], v[238:239], v[242:243]
	v_pk_mul_f32 v[110:111], s[0:1], v[110:111] op_sel_hi:[0,1]
	v_fma_f32 v140, |v156|, s25, 1.0
	v_rcp_f32_e32 v160, v140
	v_fma_f32 v140, |v157|, s25, 1.0
	v_rcp_f32_e32 v161, v140
	v_pk_mul_f32 v[162:163], v[156:157], v[156:157]
	v_pk_fma_f32 v[110:111], v[110:111], v[240:241], v[244:245]
	v_mul_f32_e32 v140, 0xbf38aa3b, v162
	v_pk_fma_f32 v[164:165], v[160:161], s[22:23], v[90:91] op_sel_hi:[1,0,0]
	v_exp_f32_e32 v162, v140
	v_pk_fma_f32 v[164:165], v[160:161], v[164:165], s[24:25] op_sel_hi:[1,1,0]
	v_mul_f32_e32 v140, 0xbf38aa3b, v163
	v_pk_fma_f32 v[164:165], v[160:161], v[164:165], s[34:35] op_sel_hi:[1,1,0]
	v_and_b32_e32 v159, 0x7fffffff, v157
	v_pk_fma_f32 v[164:165], v[160:161], v[164:165], s[40:41] op_sel_hi:[1,1,0]
	v_and_b32_e32 v158, 0x7fffffff, v156
	v_exp_f32_e32 v163, v140
	v_pk_mul_f32 v[160:161], v[160:161], v[164:165]
	v_fma_f32 v140, |v110|, s25, 1.0
	v_pk_mul_f32 v[158:159], v[158:159], v[160:161]
	v_rcp_f32_e32 v160, v140
	v_fma_f32 v140, |v111|, s25, 1.0
	v_rcp_f32_e32 v161, v140
	v_max_f32_e32 v156, 0, v156
	v_max_f32_e32 v157, 0, v157
	v_pk_fma_f32 v[156:157], v[162:163], v[158:159], v[156:157] neg_lo:[1,0,0] neg_hi:[1,0,0]
	v_pk_mul_f32 v[162:163], v[110:111], v[110:111]
	v_pk_fma_f32 v[164:165], v[160:161], s[22:23], v[90:91] op_sel_hi:[1,0,0]
	v_mul_f32_e32 v140, 0xbf38aa3b, v162
	v_exp_f32_e32 v162, v140
	v_pk_fma_f32 v[164:165], v[160:161], v[164:165], s[24:25] op_sel_hi:[1,1,0]
	v_mul_f32_e32 v140, 0xbf38aa3b, v163
	v_pk_fma_f32 v[164:165], v[160:161], v[164:165], s[34:35] op_sel_hi:[1,1,0]
	v_exp_f32_e32 v163, v140
	v_pk_fma_f32 v[164:165], v[160:161], v[164:165], s[40:41] op_sel_hi:[1,1,0]
	v_and_b32_e32 v159, 0x7fffffff, v111
	v_and_b32_e32 v158, 0x7fffffff, v110
	v_pk_mul_f32 v[160:161], v[160:161], v[164:165]
	v_max_f32_e32 v110, 0, v110
	v_max_f32_e32 v111, 0, v111
	v_pk_mul_f32 v[158:159], v[158:159], v[160:161]
	v_readlane_b32 s0, v154, 2
	v_pk_fma_f32 v[110:111], v[162:163], v[158:159], v[110:111] neg_lo:[1,0,0] neg_hi:[1,0,0]
	v_cvt_pk_f16_f32 v156, v156, v157
	v_pk_mul_f32 v[108:109], s[0:1], v[108:109] op_sel_hi:[0,1]
	v_cvt_pk_f16_f32 v157, v110, v111
	v_pk_fma_f32 v[108:109], v[108:109], v[238:239], v[242:243]
	ds_write_b64 v138, v[156:157] offset:33280
	v_fma_f32 v138, |v108|, s25, 1.0
	v_rcp_f32_e32 v156, v138
	v_fma_f32 v138, |v109|, s25, 1.0
	v_rcp_f32_e32 v157, v138
	v_pk_mul_f32 v[158:159], v[108:109], v[108:109]
	v_and_b32_e32 v111, 0x7fffffff, v109
	v_mul_f32_e32 v138, 0xbf38aa3b, v158
	v_pk_fma_f32 v[160:161], v[156:157], s[22:23], v[90:91] op_sel_hi:[1,0,0]
	v_exp_f32_e32 v158, v138
	v_pk_fma_f32 v[160:161], v[156:157], v[160:161], s[24:25] op_sel_hi:[1,1,0]
	v_mul_f32_e32 v138, 0xbf38aa3b, v159
	v_pk_fma_f32 v[160:161], v[156:157], v[160:161], s[34:35] op_sel_hi:[1,1,0]
	v_exp_f32_e32 v159, v138
	v_pk_fma_f32 v[160:161], v[156:157], v[160:161], s[40:41] op_sel_hi:[1,1,0]
	v_and_b32_e32 v110, 0x7fffffff, v108
	v_pk_mul_f32 v[156:157], v[156:157], v[160:161]
	v_max_f32_e32 v108, 0, v108
	v_max_f32_e32 v109, 0, v109
	v_pk_mul_f32 v[110:111], v[110:111], v[156:157]
	v_pk_mul_f32 v[104:105], s[0:1], v[104:105] op_sel_hi:[0,1]
	v_pk_fma_f32 v[108:109], v[158:159], v[110:111], v[108:109] neg_lo:[1,0,0] neg_hi:[1,0,0]
	v_pk_fma_f32 v[104:105], v[104:105], v[240:241], v[244:245]
	v_cvt_pk_f16_f32 v108, v108, v109
	v_fma_f32 v109, |v104|, s25, 1.0
	v_rcp_f32_e32 v156, v109
	v_fma_f32 v109, |v105|, s25, 1.0
	v_rcp_f32_e32 v157, v109
	v_pk_mul_f32 v[158:159], v[104:105], v[104:105]
	v_and_b32_e32 v111, 0x7fffffff, v105
	v_mul_f32_e32 v109, 0xbf38aa3b, v158
	v_pk_fma_f32 v[160:161], v[156:157], s[22:23], v[90:91] op_sel_hi:[1,0,0]
	v_exp_f32_e32 v158, v109
	v_pk_fma_f32 v[160:161], v[156:157], v[160:161], s[24:25] op_sel_hi:[1,1,0]
	v_mul_f32_e32 v109, 0xbf38aa3b, v159
	v_pk_fma_f32 v[160:161], v[156:157], v[160:161], s[34:35] op_sel_hi:[1,1,0]
	v_exp_f32_e32 v159, v109
	v_pk_fma_f32 v[160:161], v[156:157], v[160:161], s[40:41] op_sel_hi:[1,1,0]
	v_and_b32_e32 v110, 0x7fffffff, v104
	v_pk_mul_f32 v[156:157], v[156:157], v[160:161]
	v_max_f32_e32 v104, 0, v104
	v_max_f32_e32 v105, 0, v105
	v_pk_mul_f32 v[110:111], v[110:111], v[156:157]
	v_readlane_b32 s0, v154, 3
	v_pk_fma_f32 v[104:105], v[158:159], v[110:111], v[104:105] neg_lo:[1,0,0] neg_hi:[1,0,0]
	s_nop 0
	v_pk_mul_f32 v[102:103], s[0:1], v[102:103] op_sel_hi:[0,1]
	v_cvt_pk_f16_f32 v109, v104, v105
	v_pk_fma_f32 v[102:103], v[102:103], v[238:239], v[242:243]
	ds_write_b64 v135, v[108:109] offset:33792
	v_fma_f32 v108, |v102|, s25, 1.0
	v_fma_f32 v109, |v103|, s25, 1.0
	v_rcp_f32_e32 v108, v108
	v_rcp_f32_e32 v109, v109
	v_pk_mul_f32 v[110:111], v[102:103], v[102:103]
	v_and_b32_e32 v105, 0x7fffffff, v103
	v_mul_f32_e32 v110, 0xbf38aa3b, v110
	v_pk_fma_f32 v[156:157], v[108:109], s[22:23], v[90:91] op_sel_hi:[1,0,0]
	v_mul_f32_e32 v111, 0xbf38aa3b, v111
	v_pk_fma_f32 v[156:157], v[108:109], v[156:157], s[24:25] op_sel_hi:[1,1,0]
	v_exp_f32_e32 v110, v110
	v_pk_fma_f32 v[156:157], v[108:109], v[156:157], s[34:35] op_sel_hi:[1,1,0]
	v_exp_f32_e32 v111, v111
	v_pk_fma_f32 v[156:157], v[108:109], v[156:157], s[40:41] op_sel_hi:[1,1,0]
	v_and_b32_e32 v104, 0x7fffffff, v102
	v_pk_mul_f32 v[108:109], v[108:109], v[156:157]
	v_max_f32_e32 v102, 0, v102
	v_max_f32_e32 v103, 0, v103
	v_pk_mul_f32 v[104:105], v[104:105], v[108:109]
	v_pk_mul_f32 v[100:101], s[0:1], v[100:101] op_sel_hi:[0,1]
	v_pk_fma_f32 v[102:103], v[110:111], v[104:105], v[102:103] neg_lo:[1,0,0] neg_hi:[1,0,0]
	v_pk_fma_f32 v[100:101], v[100:101], v[240:241], v[244:245]
	v_cvt_pk_f16_f32 v102, v102, v103
	v_fma_f32 v103, |v100|, s25, 1.0
	v_rcp_f32_e32 v108, v103
	v_fma_f32 v103, |v101|, s25, 1.0
	v_rcp_f32_e32 v109, v103
	v_pk_mul_f32 v[110:111], v[100:101], v[100:101]
	v_and_b32_e32 v105, 0x7fffffff, v101
	v_mul_f32_e32 v103, 0xbf38aa3b, v110
	v_pk_fma_f32 v[156:157], v[108:109], s[22:23], v[90:91] op_sel_hi:[1,0,0]
	v_exp_f32_e32 v110, v103
	v_pk_fma_f32 v[156:157], v[108:109], v[156:157], s[24:25] op_sel_hi:[1,1,0]
	v_mul_f32_e32 v103, 0xbf38aa3b, v111
	v_pk_fma_f32 v[156:157], v[108:109], v[156:157], s[34:35] op_sel_hi:[1,1,0]
	v_exp_f32_e32 v111, v103
	v_pk_fma_f32 v[156:157], v[108:109], v[156:157], s[40:41] op_sel_hi:[1,1,0]
	v_and_b32_e32 v104, 0x7fffffff, v100
	v_pk_mul_f32 v[108:109], v[108:109], v[156:157]
	v_max_f32_e32 v100, 0, v100
	v_max_f32_e32 v101, 0, v101
	v_pk_mul_f32 v[104:105], v[104:105], v[108:109]
	v_readlane_b32 s0, v154, 4
	v_pk_fma_f32 v[100:101], v[110:111], v[104:105], v[100:101] neg_lo:[1,0,0] neg_hi:[1,0,0]
	s_nop 0
	v_pk_mul_f32 v[98:99], s[0:1], v[98:99] op_sel_hi:[0,1]
	v_cvt_pk_f16_f32 v103, v100, v101
	v_pk_fma_f32 v[98:99], v[98:99], v[238:239], v[242:243]
	ds_write_b64 v134, v[102:103] offset:34304
	v_fma_f32 v102, |v98|, s25, 1.0
	v_fma_f32 v103, |v99|, s25, 1.0
	v_rcp_f32_e32 v102, v102
	v_rcp_f32_e32 v103, v103
	v_pk_mul_f32 v[104:105], v[98:99], v[98:99]
	v_and_b32_e32 v101, 0x7fffffff, v99
	v_mul_f32_e32 v104, 0xbf38aa3b, v104
	v_pk_fma_f32 v[108:109], v[102:103], s[22:23], v[90:91] op_sel_hi:[1,0,0]
	v_mul_f32_e32 v105, 0xbf38aa3b, v105
	v_pk_fma_f32 v[108:109], v[102:103], v[108:109], s[24:25] op_sel_hi:[1,1,0]
	v_exp_f32_e32 v104, v104
	v_pk_fma_f32 v[108:109], v[102:103], v[108:109], s[34:35] op_sel_hi:[1,1,0]
	v_exp_f32_e32 v105, v105
	v_pk_fma_f32 v[108:109], v[102:103], v[108:109], s[40:41] op_sel_hi:[1,1,0]
	v_and_b32_e32 v100, 0x7fffffff, v98
	v_pk_mul_f32 v[102:103], v[102:103], v[108:109]
	v_max_f32_e32 v98, 0, v98
	v_max_f32_e32 v99, 0, v99
	v_pk_mul_f32 v[100:101], v[100:101], v[102:103]
	v_pk_mul_f32 v[96:97], s[0:1], v[96:97] op_sel_hi:[0,1]
	v_pk_fma_f32 v[98:99], v[104:105], v[100:101], v[98:99] neg_lo:[1,0,0] neg_hi:[1,0,0]
	v_pk_fma_f32 v[96:97], v[96:97], v[240:241], v[244:245]
	v_cvt_pk_f16_f32 v98, v98, v99
	v_fma_f32 v99, |v96|, s25, 1.0
	v_rcp_f32_e32 v102, v99
	v_fma_f32 v99, |v97|, s25, 1.0
	v_rcp_f32_e32 v103, v99
	v_pk_mul_f32 v[104:105], v[96:97], v[96:97]
	v_and_b32_e32 v101, 0x7fffffff, v97
	v_mul_f32_e32 v99, 0xbf38aa3b, v104
	v_pk_fma_f32 v[108:109], v[102:103], s[22:23], v[90:91] op_sel_hi:[1,0,0]
	v_exp_f32_e32 v104, v99
	v_pk_fma_f32 v[108:109], v[102:103], v[108:109], s[24:25] op_sel_hi:[1,1,0]
	v_mul_f32_e32 v99, 0xbf38aa3b, v105
	v_pk_fma_f32 v[108:109], v[102:103], v[108:109], s[34:35] op_sel_hi:[1,1,0]
	v_exp_f32_e32 v105, v99
	v_pk_fma_f32 v[108:109], v[102:103], v[108:109], s[40:41] op_sel_hi:[1,1,0]
	v_and_b32_e32 v100, 0x7fffffff, v96
	v_pk_mul_f32 v[102:103], v[102:103], v[108:109]
	v_max_f32_e32 v96, 0, v96
	v_max_f32_e32 v97, 0, v97
	v_pk_mul_f32 v[100:101], v[100:101], v[102:103]
	v_readlane_b32 s0, v154, 5
	v_pk_fma_f32 v[96:97], v[104:105], v[100:101], v[96:97] neg_lo:[1,0,0] neg_hi:[1,0,0]
	v_mov_b32_e32 v104, 0
	v_pk_mul_f32 v[94:95], s[0:1], v[94:95] op_sel_hi:[0,1]
	v_cvt_pk_f16_f32 v99, v96, v97
	v_pk_fma_f32 v[94:95], v[94:95], v[238:239], v[242:243]
	ds_write_b64 v120, v[98:99] offset:34816
	v_fma_f32 v98, |v94|, s25, 1.0
	v_fma_f32 v99, |v95|, s25, 1.0
	v_rcp_f32_e32 v98, v98
	v_rcp_f32_e32 v99, v99
	v_pk_mul_f32 v[100:101], v[94:95], v[94:95]
	v_and_b32_e32 v97, 0x7fffffff, v95
	v_mul_f32_e32 v100, 0xbf38aa3b, v100
	v_pk_fma_f32 v[102:103], v[98:99], s[22:23], v[90:91] op_sel_hi:[1,0,0]
	v_mul_f32_e32 v101, 0xbf38aa3b, v101
	v_pk_fma_f32 v[102:103], v[98:99], v[102:103], s[24:25] op_sel_hi:[1,1,0]
	v_exp_f32_e32 v100, v100
	v_pk_fma_f32 v[102:103], v[98:99], v[102:103], s[34:35] op_sel_hi:[1,1,0]
	v_exp_f32_e32 v101, v101
	v_pk_fma_f32 v[102:103], v[98:99], v[102:103], s[40:41] op_sel_hi:[1,1,0]
	v_and_b32_e32 v96, 0x7fffffff, v94
	v_pk_mul_f32 v[98:99], v[98:99], v[102:103]
	v_max_f32_e32 v94, 0, v94
	v_max_f32_e32 v95, 0, v95
	v_pk_mul_f32 v[96:97], v[96:97], v[98:99]
	v_pk_mul_f32 v[92:93], s[0:1], v[92:93] op_sel_hi:[0,1]
	v_pk_fma_f32 v[94:95], v[100:101], v[96:97], v[94:95] neg_lo:[1,0,0] neg_hi:[1,0,0]
	v_pk_fma_f32 v[92:93], v[92:93], v[240:241], v[244:245]
	v_cvt_pk_f16_f32 v94, v94, v95
	v_fma_f32 v95, |v92|, s25, 1.0
	v_rcp_f32_e32 v98, v95
	v_fma_f32 v95, |v93|, s25, 1.0
	v_rcp_f32_e32 v99, v95
	v_pk_mul_f32 v[100:101], v[92:93], v[92:93]
	v_and_b32_e32 v97, 0x7fffffff, v93
	v_mul_f32_e32 v95, 0xbf38aa3b, v100
	v_pk_fma_f32 v[102:103], v[98:99], s[22:23], v[90:91] op_sel_hi:[1,0,0]
	v_exp_f32_e32 v100, v95
	v_pk_fma_f32 v[102:103], v[98:99], v[102:103], s[24:25] op_sel_hi:[1,1,0]
	v_mul_f32_e32 v95, 0xbf38aa3b, v101
	v_pk_fma_f32 v[102:103], v[98:99], v[102:103], s[34:35] op_sel_hi:[1,1,0]
	v_exp_f32_e32 v101, v95
	v_pk_fma_f32 v[102:103], v[98:99], v[102:103], s[40:41] op_sel_hi:[1,1,0]
	v_and_b32_e32 v96, 0x7fffffff, v92
	v_pk_mul_f32 v[98:99], v[98:99], v[102:103]
	v_max_f32_e32 v92, 0, v92
	v_max_f32_e32 v93, 0, v93
	v_pk_mul_f32 v[96:97], v[96:97], v[98:99]
	v_readlane_b32 s0, v154, 6
	v_pk_fma_f32 v[92:93], v[100:101], v[96:97], v[92:93] neg_lo:[1,0,0] neg_hi:[1,0,0]
	s_waitcnt vmcnt(1)
	v_add_f32_e32 v100, v228, v229
	v_pk_mul_f32 v[80:81], s[0:1], v[80:81] op_sel_hi:[0,1]
	v_cvt_pk_f16_f32 v95, v92, v93
	v_pk_fma_f32 v[80:81], v[80:81], v[238:239], v[242:243]
	ds_write_b64 v121, v[94:95] offset:35328
	v_fma_f32 v94, |v80|, s25, 1.0
	v_fma_f32 v95, |v81|, s25, 1.0
	v_rcp_f32_e32 v94, v94
	v_rcp_f32_e32 v95, v95
	v_pk_mul_f32 v[96:97], v[80:81], v[80:81]
	v_and_b32_e32 v93, 0x7fffffff, v81
	v_mul_f32_e32 v96, 0xbf38aa3b, v96
	v_pk_fma_f32 v[98:99], v[94:95], s[22:23], v[90:91] op_sel_hi:[1,0,0]
	v_mul_f32_e32 v97, 0xbf38aa3b, v97
	v_pk_fma_f32 v[98:99], v[94:95], v[98:99], s[24:25] op_sel_hi:[1,1,0]
	v_exp_f32_e32 v96, v96
	v_pk_fma_f32 v[98:99], v[94:95], v[98:99], s[34:35] op_sel_hi:[1,1,0]
	v_exp_f32_e32 v97, v97
	v_pk_fma_f32 v[98:99], v[94:95], v[98:99], s[40:41] op_sel_hi:[1,1,0]
	v_and_b32_e32 v92, 0x7fffffff, v80
	v_pk_mul_f32 v[94:95], v[94:95], v[98:99]
	v_max_f32_e32 v80, 0, v80
	v_max_f32_e32 v81, 0, v81
	v_pk_mul_f32 v[92:93], v[92:93], v[94:95]
	v_pk_mul_f32 v[78:79], s[0:1], v[78:79] op_sel_hi:[0,1]
	v_pk_fma_f32 v[80:81], v[96:97], v[92:93], v[80:81] neg_lo:[1,0,0] neg_hi:[1,0,0]
	v_pk_fma_f32 v[78:79], v[78:79], v[240:241], v[244:245]
	v_cvt_pk_f16_f32 v80, v80, v81
	v_fma_f32 v81, |v78|, s25, 1.0
	v_rcp_f32_e32 v94, v81
	v_fma_f32 v81, |v79|, s25, 1.0
	v_rcp_f32_e32 v95, v81
	v_pk_mul_f32 v[96:97], v[78:79], v[78:79]
	v_and_b32_e32 v93, 0x7fffffff, v79
	v_mul_f32_e32 v81, 0xbf38aa3b, v96
	v_pk_fma_f32 v[98:99], v[94:95], s[22:23], v[90:91] op_sel_hi:[1,0,0]
	v_exp_f32_e32 v96, v81
	v_pk_fma_f32 v[98:99], v[94:95], v[98:99], s[24:25] op_sel_hi:[1,1,0]
	v_mul_f32_e32 v81, 0xbf38aa3b, v97
	v_pk_fma_f32 v[98:99], v[94:95], v[98:99], s[34:35] op_sel_hi:[1,1,0]
	v_exp_f32_e32 v97, v81
	v_pk_fma_f32 v[98:99], v[94:95], v[98:99], s[40:41] op_sel_hi:[1,1,0]
	v_and_b32_e32 v92, 0x7fffffff, v78
	v_pk_mul_f32 v[94:95], v[94:95], v[98:99]
	v_max_f32_e32 v78, 0, v78
	v_max_f32_e32 v79, 0, v79
	v_pk_mul_f32 v[92:93], v[92:93], v[94:95]
	v_readlane_b32 s0, v154, 7
	v_pk_fma_f32 v[78:79], v[96:97], v[92:93], v[78:79] neg_lo:[1,0,0] neg_hi:[1,0,0]
	v_add_f32_e32 v97, v224, v225
	v_pk_mul_f32 v[76:77], s[0:1], v[76:77] op_sel_hi:[0,1]
	v_cvt_pk_f16_f32 v81, v78, v79
	v_pk_fma_f32 v[76:77], v[76:77], v[238:239], v[242:243]
	ds_write_b64 v118, v[80:81] offset:35840
	v_fma_f32 v80, |v76|, s25, 1.0
	v_fma_f32 v81, |v77|, s25, 1.0
	v_rcp_f32_e32 v80, v80
	v_rcp_f32_e32 v81, v81
	v_pk_mul_f32 v[92:93], v[76:77], v[76:77]
	v_and_b32_e32 v79, 0x7fffffff, v77
	v_mul_f32_e32 v92, 0xbf38aa3b, v92
	v_pk_fma_f32 v[94:95], v[80:81], s[22:23], v[90:91] op_sel_hi:[1,0,0]
	v_mul_f32_e32 v93, 0xbf38aa3b, v93
	v_pk_fma_f32 v[94:95], v[80:81], v[94:95], s[24:25] op_sel_hi:[1,1,0]
	v_exp_f32_e32 v92, v92
	v_pk_fma_f32 v[94:95], v[80:81], v[94:95], s[34:35] op_sel_hi:[1,1,0]
	v_exp_f32_e32 v93, v93
	v_pk_fma_f32 v[94:95], v[80:81], v[94:95], s[40:41] op_sel_hi:[1,1,0]
	v_and_b32_e32 v78, 0x7fffffff, v76
	v_pk_mul_f32 v[80:81], v[80:81], v[94:95]
	v_max_f32_e32 v76, 0, v76
	v_max_f32_e32 v77, 0, v77
	v_pk_mul_f32 v[78:79], v[78:79], v[80:81]
	v_pk_mul_f32 v[74:75], s[0:1], v[74:75] op_sel_hi:[0,1]
	v_pk_fma_f32 v[76:77], v[92:93], v[78:79], v[76:77] neg_lo:[1,0,0] neg_hi:[1,0,0]
	v_pk_fma_f32 v[92:93], v[74:75], v[240:241], v[244:245]
	v_cvt_pk_f16_f32 v80, v76, v77
	v_fma_f32 v74, |v92|, s25, 1.0
	v_fma_f32 v75, |v93|, s25, 1.0
	v_rcp_f32_e32 v74, v74
	v_rcp_f32_e32 v75, v75
	v_pk_mul_f32 v[76:77], v[92:93], v[92:93]
	s_waitcnt vmcnt(0)
	v_add_f32_e32 v101, v232, v233
	v_mul_f32_e32 v76, 0xbf38aa3b, v76
	v_pk_fma_f32 v[78:79], v[74:75], s[22:23], v[90:91] op_sel_hi:[1,0,0]
	v_exp_f32_e32 v96, v76
	v_pk_fma_f32 v[78:79], v[74:75], v[78:79], s[24:25] op_sel_hi:[1,1,0]
	v_add_f32_e32 v76, v208, v209
	v_pk_fma_f32 v[78:79], v[74:75], v[78:79], s[34:35] op_sel_hi:[1,1,0]
	v_mul_f32_e32 v81, 0xbf38aa3b, v77
	v_pk_fma_f32 v[78:79], v[74:75], v[78:79], s[40:41] op_sel_hi:[1,1,0]
	v_add_f32_e32 v77, v212, v213
	v_pk_mul_f32 v[98:99], v[74:75], v[78:79]
	v_add_f32_e32 v74, v202, v203
	v_add_f32_e32 v75, v204, v205
	v_add_f32_e32 v74, v74, v75
	v_add_f32_e32 v75, v206, v207
	v_add_f32_e32 v75, v75, v76
	v_add_f32_e32 v76, v210, v211
	v_add_f32_e32 v76, v76, v77
	v_add_f32_e32 v77, v214, v215
	v_add_f32_e32 v78, v216, v217
	v_add_f32_e32 v77, v77, v78
	v_add_f32_e32 v78, v218, v219
	v_add_f32_e32 v79, v220, v221
	v_add_f32_e32 v78, v78, v79
	v_add_f32_e32 v79, v222, v223
	v_add_f32_e32 v79, v79, v97
	v_add_f32_e32 v97, v226, v227
	v_add_f32_e32 v97, v97, v100
	v_add_f32_e32 v100, v230, v231
	v_add_f32_e32 v100, v100, v101
	v_cndmask_b32_e64 v101, v75, v74, s[4:5]
	v_cndmask_b32_e64 v74, v74, v75, s[4:5]
	v_cndmask_b32_e64 v75, v77, v76, s[4:5]
	v_cndmask_b32_e64 v76, v76, v77, s[4:5]
	v_cndmask_b32_e64 v77, v78, v79, s[4:5]
	v_add_f32_dpp v74, v101, v74 quad_perm:[1,0,3,2] row_mask:0xf bank_mask:0xf bound_ctrl:1
	v_add_f32_dpp v75, v75, v76 quad_perm:[1,0,3,2] row_mask:0xf bank_mask:0xf bound_ctrl:1
	v_cndmask_b32_e64 v76, v79, v78, s[4:5]
	v_cndmask_b32_e64 v78, v97, v100, s[4:5]
	v_and_b32_e32 v95, 0x7fffffff, v93
	v_add_f32_dpp v76, v76, v77 quad_perm:[1,0,3,2] row_mask:0xf bank_mask:0xf bound_ctrl:1
	v_cndmask_b32_e64 v77, v100, v97, s[4:5]
	v_exp_f32_e32 v97, v81
	v_and_b32_e32 v94, 0x7fffffff, v92
	v_add_f32_dpp v77, v77, v78 quad_perm:[1,0,3,2] row_mask:0xf bank_mask:0xf bound_ctrl:1
	v_cndmask_b32_e64 v78, v74, v75, s[6:7]
	v_cndmask_b32_e64 v74, v75, v74, s[6:7]
	v_cndmask_b32_e64 v75, v76, v77, s[6:7]
	v_cndmask_b32_e64 v76, v77, v76, s[6:7]
	v_add_f32_dpp v74, v78, v74 quad_perm:[2,3,0,1] row_mask:0xf bank_mask:0xf bound_ctrl:1
	v_max_f32_e32 v92, 0, v92
	v_add_f32_dpp v75, v75, v76 quad_perm:[2,3,0,1] row_mask:0xf bank_mask:0xf bound_ctrl:1
	v_cndmask_b32_e64 v76, v74, v75, s[8:9]
	v_cndmask_b32_e64 v74, v75, v74, s[8:9]
	v_mov_b32_e32 v75, v76
	v_max_f32_e32 v93, 0, v93
	s_waitcnt lgkmcnt(14)
	v_dot2c_f32_f16_e32 v104, v38, v38
	v_mov_b32_dpp v75, v75 row_shl:4 row_mask:0xf bank_mask:0x5
	v_mov_b32_e32 v105, 0
	v_dot2c_f32_f16_e32 v104, v39, v39
	v_mov_b32_dpp v75, v76 row_shr:4 row_mask:0xf bank_mask:0xa
	v_add_f32_e32 v74, v74, v75
	v_dot2c_f32_f16_e32 v104, v40, v40
	v_dot2c_f32_f16_e32 v104, v41, v41
	v_add_f32_dpp v74, v74, v74 row_ror:8 row_mask:0xf bank_mask:0xf bound_ctrl:1
	v_mov_b32_e32 v75, v74
	s_nop 1
	v_permlane16_swap_b32_e32 v74, v75
	v_add_f32_e32 v74, v74, v75
	v_mov_b32_e32 v75, v74
	s_nop 1
	v_permlane32_swap_b32_e32 v74, v75
	v_add_f32_e32 v74, v74, v75
	v_mul_f32_e32 v74, 0x3b800000, v74
	s_waitcnt lgkmcnt(13)
	v_dot2c_f32_f16_e32 v104, v34, v34
	v_readlane_b32 s42, v74, 0
	v_readlane_b32 s44, v74, 1
	v_readlane_b32 s46, v74, 2
	v_pk_add_f32 v[102:103], v[204:205], s[42:43] op_sel_hi:[1, 0] neg_lo:[0, 1] neg_hi:[0, 1]
	v_pk_add_f32 v[78:79], v[208:209], s[44:45] op_sel_hi:[1, 0] neg_lo:[0, 1] neg_hi:[0, 1]
	v_pk_add_f32 v[100:101], v[202:203], s[42:43] op_sel_hi:[1, 0] neg_lo:[0, 1] neg_hi:[0, 1]
	v_mul_f32_e32 v70, v103, v103
	v_mul_f32_e32 v71, v79, v79
	v_fmac_f32_e32 v70, v102, v102
	v_pk_add_f32 v[86:87], v[206:207], s[44:45] op_sel_hi:[1, 0] neg_lo:[0, 1] neg_hi:[0, 1]
	v_fmac_f32_e32 v71, v78, v78
	v_fmac_f32_e32 v70, v101, v101
	v_fmac_f32_e32 v71, v87, v87
	v_fmac_f32_e32 v70, v100, v100
	v_fmac_f32_e32 v71, v86, v86
	v_readlane_b32 s48, v74, 3
	v_cndmask_b32_e64 v72, v71, v70, s[4:5]
	v_cndmask_b32_e64 v70, v70, v71, s[4:5]
	v_readlane_b32 s50, v74, 4
	v_readlane_b32 s52, v74, 5
	v_readlane_b32 s54, v74, 6
	v_readlane_b32 s0, v74, 7
	v_add_f32_dpp v88, v72, v70 quad_perm:[1,0,3,2] row_mask:0xf bank_mask:0xf bound_ctrl:1
	v_pk_add_f32 v[74:75], v[212:213], s[46:47] op_sel_hi:[1, 0] neg_lo:[0, 1] neg_hi:[0, 1]
	v_pk_add_f32 v[70:71], v[216:217], s[48:49] op_sel_hi:[1, 0] neg_lo:[0, 1] neg_hi:[0, 1]
	v_pk_add_f32 v[76:77], v[210:211], s[46:47] op_sel_hi:[1, 0] neg_lo:[0, 1] neg_hi:[0, 1]
	v_mul_f32_e32 v82, v75, v75
	v_pk_add_f32 v[72:73], v[214:215], s[48:49] op_sel_hi:[1, 0] neg_lo:[0, 1] neg_hi:[0, 1]
	v_mul_f32_e32 v66, v71, v71
	v_fmac_f32_e32 v82, v74, v74
	v_fmac_f32_e32 v66, v70, v70
	v_fmac_f32_e32 v82, v77, v77
	v_fmac_f32_e32 v66, v73, v73
	v_fmac_f32_e32 v82, v76, v76
	v_fmac_f32_e32 v66, v72, v72
	v_cndmask_b32_e64 v67, v66, v82, s[4:5]
	v_cndmask_b32_e64 v66, v82, v66, s[4:5]
	v_pk_add_f32 v[68:69], v[218:219], s[50:51] op_sel_hi:[1, 0] neg_lo:[0, 1] neg_hi:[0, 1]
	v_pk_add_f32 v[62:63], v[222:223], s[52:53] op_sel_hi:[1, 0] neg_lo:[0, 1] neg_hi:[0, 1]
	v_add_f32_dpp v66, v67, v66 quad_perm:[1,0,3,2] row_mask:0xf bank_mask:0xf bound_ctrl:1
	v_cndmask_b32_e64 v67, v88, v66, s[6:7]
	v_cndmask_b32_e64 v66, v66, v88, s[6:7]
	v_pk_add_f32 v[56:57], v[228:229], s[54:55] op_sel_hi:[1, 0] neg_lo:[0, 1] neg_hi:[0, 1]
	v_dot2c_f32_f16_e32 v104, v35, v35
	v_add_f32_dpp v82, v67, v66 quad_perm:[2,3,0,1] row_mask:0xf bank_mask:0xf bound_ctrl:1
	v_pk_add_f32 v[66:67], v[220:221], s[50:51] op_sel_hi:[1, 0] neg_lo:[0, 1] neg_hi:[0, 1]
	v_pk_add_f32 v[60:61], v[224:225], s[52:53] op_sel_hi:[1, 0] neg_lo:[0, 1] neg_hi:[0, 1]
	v_mul_f32_e32 v58, v67, v67
	v_mul_f32_e32 v59, v61, v61
	v_fmac_f32_e32 v58, v66, v66
	v_fmac_f32_e32 v59, v60, v60
	v_fmac_f32_e32 v58, v69, v69
	v_fmac_f32_e32 v59, v63, v63
	v_fmac_f32_e32 v58, v68, v68
	v_fmac_f32_e32 v59, v62, v62
	v_cndmask_b32_e64 v64, v59, v58, s[4:5]
	v_cndmask_b32_e64 v58, v58, v59, s[4:5]
	v_mul_f32_e32 v65, v57, v57
	v_fmac_f32_e32 v65, v56, v56
	v_add_f32_dpp v64, v64, v58 quad_perm:[1,0,3,2] row_mask:0xf bank_mask:0xf bound_ctrl:1
	v_pk_add_f32 v[58:59], v[226:227], s[54:55] op_sel_hi:[1, 0] neg_lo:[0, 1] neg_hi:[0, 1]
	v_pk_add_f32 v[54:55], v[230:231], s[0:1] op_sel_hi:[1, 0] neg_lo:[0, 1] neg_hi:[0, 1]
	v_pk_add_f32 v[50:51], v[232:233], s[0:1] op_sel_hi:[1, 0] neg_lo:[0, 1] neg_hi:[0, 1]
	v_fmac_f32_e32 v65, v59, v59
	v_mul_f32_e32 v52, v51, v51
	v_fmac_f32_e32 v52, v50, v50
	v_fmac_f32_e32 v52, v55, v55
	v_fmac_f32_e32 v65, v58, v58
	v_fmac_f32_e32 v52, v54, v54
	v_cndmask_b32_e64 v53, v52, v65, s[4:5]
	v_cndmask_b32_e64 v52, v65, v52, s[4:5]
	v_dot2c_f32_f16_e32 v104, v36, v36
	v_dot2c_f32_f16_e32 v104, v37, v37
	v_add_f32_dpp v52, v53, v52 quad_perm:[1,0,3,2] row_mask:0xf bank_mask:0xf bound_ctrl:1
	v_cndmask_b32_e64 v53, v64, v52, s[6:7]
	v_cndmask_b32_e64 v52, v52, v64, s[6:7]
	s_waitcnt lgkmcnt(12)
	v_dot2c_f32_f16_e32 v104, v30, v30
	v_dot2c_f32_f16_e32 v104, v31, v31
	v_add_f32_dpp v52, v53, v52 quad_perm:[2,3,0,1] row_mask:0xf bank_mask:0xf bound_ctrl:1
	v_cndmask_b32_e64 v53, v82, v52, s[8:9]
	v_mov_b32_e32 v64, v53
	v_cndmask_b32_e64 v52, v52, v82, s[8:9]
	v_dot2c_f32_f16_e32 v104, v32, v32
	v_mov_b32_dpp v64, v64 row_shl:4 row_mask:0xf bank_mask:0x5
	v_dot2c_f32_f16_e32 v104, v33, v33
	s_waitcnt lgkmcnt(11)
	v_dot2c_f32_f16_e32 v104, v26, v26
	v_mov_b32_dpp v64, v53 row_shr:4 row_mask:0xf bank_mask:0xa
	v_add_f32_e32 v52, v52, v64
	v_dot2c_f32_f16_e32 v104, v27, v27
	v_dot2c_f32_f16_e32 v104, v28, v28
	v_add_f32_dpp v52, v52, v52 row_ror:8 row_mask:0xf bank_mask:0xf bound_ctrl:1
	v_mov_b32_e32 v53, v52
	s_nop 1
	v_permlane16_swap_b32_e32 v52, v53
	v_add_f32_e32 v52, v52, v53
	v_mov_b32_e32 v53, v52
	s_nop 1
	v_permlane32_swap_b32_e32 v52, v53
	v_add_f32_e32 v52, v52, v53
	v_fmac_f32_e32 v116, 0x3b800000, v52
	v_mul_f32_e32 v52, 0x4f800000, v116
	v_cmp_gt_f32_e32 vcc, s35, v116
	v_dot2c_f32_f16_e32 v104, v29, v29
	s_waitcnt lgkmcnt(10)
	v_dot2c_f32_f16_e32 v104, v22, v22
	v_cndmask_b32_e32 v64, v116, v52, vcc
	v_sqrt_f32_e32 v65, v64
	v_pk_mul_f32 v[52:53], v[94:95], v[98:99]
	v_and_b32_e32 v94, 48, v0
	v_pk_fma_f32 v[52:53], v[96:97], v[52:53], v[92:93] neg_lo:[1,0,0] neg_hi:[1,0,0]
	v_add_u32_e32 v81, -1, v65
	v_fma_f32 v82, -v81, v65, v64
	v_cmp_ge_f32_e64 s[0:1], 0, v82
	v_add_u32_e32 v82, 1, v65
	v_add_u32_e32 v95, 0x19860, v94
	v_cndmask_b32_e64 v81, v65, v81, s[0:1]
	v_fma_f32 v65, -v82, v65, v64
	v_cmp_lt_f32_e64 s[0:1], 0, v65
	v_dot2c_f32_f16_e32 v104, v23, v23
	v_dot2c_f32_f16_e32 v104, v24, v24
	v_cndmask_b32_e64 v65, v81, v82, s[0:1]
	v_mul_f32_e32 v81, 0x37800000, v65
	v_cndmask_b32_e32 v65, v65, v81, vcc
	v_cmp_class_f32_e32 vcc, v64, v117
	v_cvt_pk_f16_f32 v81, v52, v53
	ds_write_b64 v144, v[80:81] offset:36352
	v_cndmask_b32_e32 v64, v65, v64, vcc
	v_div_scale_f32 v65, s[0:1], v64, v64, 1.0
	v_rcp_f32_e32 v82, v65
	v_dot2c_f32_f16_e32 v104, v25, v25
	s_waitcnt lgkmcnt(10)
	v_dot2c_f32_f16_e32 v104, v18, v18
	v_dot2c_f32_f16_e32 v104, v19, v19
	v_fma_f32 v52, -v65, v82, 1.0
	v_fmac_f32_e32 v82, v52, v82
	v_div_scale_f32 v52, vcc, 1.0, v64, 1.0
	v_mul_f32_e32 v53, v52, v82
	v_fma_f32 v80, -v65, v53, v52
	v_fmac_f32_e32 v53, v80, v82
	v_fma_f32 v52, -v65, v53, v52
	v_div_fmas_f32 v52, v52, v82, v53
	v_div_fixup_f32 v52, v52, v64, 1.0
	v_dot2c_f32_f16_e32 v104, v20, v20
	v_readlane_b32 s0, v52, 0
	v_dot2c_f32_f16_e32 v104, v21, v21
	s_waitcnt lgkmcnt(9)
	v_dot2c_f32_f16_e32 v104, v14, v14
	v_pk_mul_f32 v[64:65], s[0:1], v[100:101] op_sel_hi:[0,1]
	v_pk_fma_f32 v[64:65], v[64:65], v[238:239], v[242:243]
	v_dot2c_f32_f16_e32 v104, v15, v15
	v_fma_f32 v53, |v64|, s25, 1.0
	v_rcp_f32_e32 v82, v53
	v_fma_f32 v53, |v65|, s25, 1.0
	v_rcp_f32_e32 v83, v53
	v_pk_mul_f32 v[84:85], v[64:65], v[64:65]
	v_and_b32_e32 v81, 0x7fffffff, v65
	v_mul_f32_e32 v53, 0xbf38aa3b, v84
	v_pk_fma_f32 v[88:89], v[82:83], s[22:23], v[90:91] op_sel_hi:[1,0,0]
	v_exp_f32_e32 v84, v53
	v_pk_fma_f32 v[88:89], v[82:83], v[88:89], s[24:25] op_sel_hi:[1,1,0]
	v_mul_f32_e32 v53, 0xbf38aa3b, v85
	v_pk_fma_f32 v[88:89], v[82:83], v[88:89], s[34:35] op_sel_hi:[1,1,0]
	v_exp_f32_e32 v85, v53
	v_pk_fma_f32 v[88:89], v[82:83], v[88:89], s[40:41] op_sel_hi:[1,1,0]
	v_and_b32_e32 v80, 0x7fffffff, v64
	v_pk_mul_f32 v[82:83], v[82:83], v[88:89]
	v_max_f32_e32 v64, 0, v64
	v_max_f32_e32 v65, 0, v65
	v_pk_mul_f32 v[80:81], v[80:81], v[82:83]
	v_dot2c_f32_f16_e32 v104, v16, v16
	v_pk_fma_f32 v[64:65], v[84:85], v[80:81], v[64:65] neg_lo:[1,0,0] neg_hi:[1,0,0]
	v_pk_mul_f32 v[80:81], s[0:1], v[102:103] op_sel_hi:[0,1]
	v_pk_fma_f32 v[80:81], v[80:81], v[240:241], v[244:245]
	v_cvt_pk_f16_f32 v64, v64, v65
	v_fma_f32 v53, |v80|, s25, 1.0
	v_rcp_f32_e32 v84, v53
	v_fma_f32 v53, |v81|, s25, 1.0
	v_rcp_f32_e32 v85, v53
	v_pk_mul_f32 v[88:89], v[80:81], v[80:81]
	v_and_b32_e32 v83, 0x7fffffff, v81
	v_mul_f32_e32 v53, 0xbf38aa3b, v88
	v_pk_fma_f32 v[92:93], v[84:85], s[22:23], v[90:91] op_sel_hi:[1,0,0]
	v_exp_f32_e32 v88, v53
	v_pk_fma_f32 v[92:93], v[84:85], v[92:93], s[24:25] op_sel_hi:[1,1,0]
	v_mul_f32_e32 v53, 0xbf38aa3b, v89
	v_pk_fma_f32 v[92:93], v[84:85], v[92:93], s[34:35] op_sel_hi:[1,1,0]
	v_exp_f32_e32 v89, v53
	v_pk_fma_f32 v[92:93], v[84:85], v[92:93], s[40:41] op_sel_hi:[1,1,0]
	v_and_b32_e32 v82, 0x7fffffff, v80
	v_pk_mul_f32 v[84:85], v[84:85], v[92:93]
	v_max_f32_e32 v80, 0, v80
	v_max_f32_e32 v81, 0, v81
	v_pk_mul_f32 v[82:83], v[82:83], v[84:85]
	v_readlane_b32 s0, v52, 1
	v_pk_fma_f32 v[80:81], v[88:89], v[82:83], v[80:81] neg_lo:[1,0,0] neg_hi:[1,0,0]
	v_dot2c_f32_f16_e32 v104, v17, v17
	v_cvt_pk_f16_f32 v65, v80, v81
	ds_write_b64 v145, v[64:65] offset:36864
	v_pk_mul_f32 v[64:65], s[0:1], v[86:87] op_sel_hi:[0,1]
	v_pk_fma_f32 v[64:65], v[64:65], v[238:239], v[242:243]
	v_pk_mul_f32 v[78:79], s[0:1], v[78:79] op_sel_hi:[0,1]
	v_fma_f32 v53, |v64|, s25, 1.0
	v_rcp_f32_e32 v82, v53
	v_fma_f32 v53, |v65|, s25, 1.0
	v_rcp_f32_e32 v83, v53
	v_pk_mul_f32 v[84:85], v[64:65], v[64:65]
	v_pk_fma_f32 v[78:79], v[78:79], v[240:241], v[244:245]
	v_mul_f32_e32 v53, 0xbf38aa3b, v84
	v_pk_fma_f32 v[86:87], v[82:83], s[22:23], v[90:91] op_sel_hi:[1,0,0]
	v_exp_f32_e32 v84, v53
	v_pk_fma_f32 v[86:87], v[82:83], v[86:87], s[24:25] op_sel_hi:[1,1,0]
	v_mul_f32_e32 v53, 0xbf38aa3b, v85
	v_pk_fma_f32 v[86:87], v[82:83], v[86:87], s[34:35] op_sel_hi:[1,1,0]
	v_and_b32_e32 v81, 0x7fffffff, v65
	v_pk_fma_f32 v[86:87], v[82:83], v[86:87], s[40:41] op_sel_hi:[1,1,0]
	v_and_b32_e32 v80, 0x7fffffff, v64
	v_exp_f32_e32 v85, v53
	v_pk_mul_f32 v[82:83], v[82:83], v[86:87]
	v_fma_f32 v53, |v78|, s25, 1.0
	v_pk_mul_f32 v[80:81], v[80:81], v[82:83]
	v_rcp_f32_e32 v82, v53
	v_fma_f32 v53, |v79|, s25, 1.0
	v_rcp_f32_e32 v83, v53
	v_max_f32_e32 v64, 0, v64
	v_max_f32_e32 v65, 0, v65
	v_pk_fma_f32 v[64:65], v[84:85], v[80:81], v[64:65] neg_lo:[1,0,0] neg_hi:[1,0,0]
	v_pk_mul_f32 v[84:85], v[78:79], v[78:79]
	v_pk_fma_f32 v[86:87], v[82:83], s[22:23], v[90:91] op_sel_hi:[1,0,0]
	v_mul_f32_e32 v53, 0xbf38aa3b, v84
	v_exp_f32_e32 v84, v53
	v_pk_fma_f32 v[86:87], v[82:83], v[86:87], s[24:25] op_sel_hi:[1,1,0]
	v_mul_f32_e32 v53, 0xbf38aa3b, v85
	v_pk_fma_f32 v[86:87], v[82:83], v[86:87], s[34:35] op_sel_hi:[1,1,0]
	v_exp_f32_e32 v85, v53
	v_pk_fma_f32 v[86:87], v[82:83], v[86:87], s[40:41] op_sel_hi:[1,1,0]
	v_and_b32_e32 v81, 0x7fffffff, v79
	v_and_b32_e32 v80, 0x7fffffff, v78
	v_pk_mul_f32 v[82:83], v[82:83], v[86:87]
	v_max_f32_e32 v78, 0, v78
	v_max_f32_e32 v79, 0, v79
	v_pk_mul_f32 v[80:81], v[80:81], v[82:83]
	v_cvt_pk_f16_f32 v64, v64, v65
	v_pk_fma_f32 v[78:79], v[84:85], v[80:81], v[78:79] neg_lo:[1,0,0] neg_hi:[1,0,0]
	v_readlane_b32 s0, v52, 2
	v_cvt_pk_f16_f32 v65, v78, v79
	ds_write_b64 v139, v[64:65] offset:37376
	v_pk_mul_f32 v[64:65], s[0:1], v[76:77] op_sel_hi:[0,1]
	v_pk_fma_f32 v[64:65], v[64:65], v[238:239], v[242:243]
	v_pk_mul_f32 v[74:75], s[0:1], v[74:75] op_sel_hi:[0,1]
	v_fma_f32 v53, |v64|, s25, 1.0
	v_rcp_f32_e32 v78, v53
	v_fma_f32 v53, |v65|, s25, 1.0
	v_rcp_f32_e32 v79, v53
	v_pk_mul_f32 v[80:81], v[64:65], v[64:65]
	v_pk_fma_f32 v[74:75], v[74:75], v[240:241], v[244:245]
	v_mul_f32_e32 v53, 0xbf38aa3b, v80
	v_pk_fma_f32 v[82:83], v[78:79], s[22:23], v[90:91] op_sel_hi:[1,0,0]
	v_exp_f32_e32 v80, v53
	v_pk_fma_f32 v[82:83], v[78:79], v[82:83], s[24:25] op_sel_hi:[1,1,0]
	v_mul_f32_e32 v53, 0xbf38aa3b, v81
	v_pk_fma_f32 v[82:83], v[78:79], v[82:83], s[34:35] op_sel_hi:[1,1,0]
	v_and_b32_e32 v77, 0x7fffffff, v65
	v_pk_fma_f32 v[82:83], v[78:79], v[82:83], s[40:41] op_sel_hi:[1,1,0]
	v_and_b32_e32 v76, 0x7fffffff, v64
	v_exp_f32_e32 v81, v53
	v_pk_mul_f32 v[78:79], v[78:79], v[82:83]
	v_fma_f32 v53, |v74|, s25, 1.0
	v_pk_mul_f32 v[76:77], v[76:77], v[78:79]
	v_rcp_f32_e32 v78, v53
	v_fma_f32 v53, |v75|, s25, 1.0
	v_rcp_f32_e32 v79, v53
	v_max_f32_e32 v64, 0, v64
	v_max_f32_e32 v65, 0, v65
	v_pk_fma_f32 v[64:65], v[80:81], v[76:77], v[64:65] neg_lo:[1,0,0] neg_hi:[1,0,0]
	v_pk_mul_f32 v[80:81], v[74:75], v[74:75]
	v_pk_fma_f32 v[82:83], v[78:79], s[22:23], v[90:91] op_sel_hi:[1,0,0]
	v_mul_f32_e32 v53, 0xbf38aa3b, v80
	v_exp_f32_e32 v80, v53
	v_pk_fma_f32 v[82:83], v[78:79], v[82:83], s[24:25] op_sel_hi:[1,1,0]
	v_mul_f32_e32 v53, 0xbf38aa3b, v81
	v_pk_fma_f32 v[82:83], v[78:79], v[82:83], s[34:35] op_sel_hi:[1,1,0]
	v_exp_f32_e32 v81, v53
	v_pk_fma_f32 v[82:83], v[78:79], v[82:83], s[40:41] op_sel_hi:[1,1,0]
	v_and_b32_e32 v77, 0x7fffffff, v75
	v_and_b32_e32 v76, 0x7fffffff, v74
	v_pk_mul_f32 v[78:79], v[78:79], v[82:83]
	v_max_f32_e32 v74, 0, v74
	v_max_f32_e32 v75, 0, v75
	v_pk_mul_f32 v[76:77], v[76:77], v[78:79]
	v_cvt_pk_f16_f32 v64, v64, v65
	v_pk_fma_f32 v[74:75], v[80:81], v[76:77], v[74:75] neg_lo:[1,0,0] neg_hi:[1,0,0]
	v_readlane_b32 s0, v52, 3
	v_cvt_pk_f16_f32 v65, v74, v75
	ds_write_b64 v137, v[64:65] offset:37888
	v_pk_mul_f32 v[64:65], s[0:1], v[72:73] op_sel_hi:[0,1]
	v_pk_fma_f32 v[64:65], v[64:65], v[238:239], v[242:243]
	v_pk_mul_f32 v[70:71], s[0:1], v[70:71] op_sel_hi:[0,1]
	v_fma_f32 v53, |v64|, s25, 1.0
	v_rcp_f32_e32 v74, v53
	v_fma_f32 v53, |v65|, s25, 1.0
	v_rcp_f32_e32 v75, v53
	v_pk_mul_f32 v[76:77], v[64:65], v[64:65]
	v_pk_fma_f32 v[70:71], v[70:71], v[240:241], v[244:245]
	v_mul_f32_e32 v53, 0xbf38aa3b, v76
	v_pk_fma_f32 v[78:79], v[74:75], s[22:23], v[90:91] op_sel_hi:[1,0,0]
	v_exp_f32_e32 v76, v53
	v_pk_fma_f32 v[78:79], v[74:75], v[78:79], s[24:25] op_sel_hi:[1,1,0]
	v_mul_f32_e32 v53, 0xbf38aa3b, v77
	v_pk_fma_f32 v[78:79], v[74:75], v[78:79], s[34:35] op_sel_hi:[1,1,0]
	v_and_b32_e32 v73, 0x7fffffff, v65
	v_pk_fma_f32 v[78:79], v[74:75], v[78:79], s[40:41] op_sel_hi:[1,1,0]
	v_and_b32_e32 v72, 0x7fffffff, v64
	v_exp_f32_e32 v77, v53
	v_pk_mul_f32 v[74:75], v[74:75], v[78:79]
	v_fma_f32 v53, |v70|, s25, 1.0
	v_pk_mul_f32 v[72:73], v[72:73], v[74:75]
	v_rcp_f32_e32 v74, v53
	v_fma_f32 v53, |v71|, s25, 1.0
	v_rcp_f32_e32 v75, v53
	v_max_f32_e32 v64, 0, v64
	v_max_f32_e32 v65, 0, v65
	v_pk_fma_f32 v[64:65], v[76:77], v[72:73], v[64:65] neg_lo:[1,0,0] neg_hi:[1,0,0]
	v_pk_mul_f32 v[76:77], v[70:71], v[70:71]
	v_pk_fma_f32 v[78:79], v[74:75], s[22:23], v[90:91] op_sel_hi:[1,0,0]
	v_mul_f32_e32 v53, 0xbf38aa3b, v76
	v_exp_f32_e32 v76, v53
	v_pk_fma_f32 v[78:79], v[74:75], v[78:79], s[24:25] op_sel_hi:[1,1,0]
	v_mul_f32_e32 v53, 0xbf38aa3b, v77
	v_pk_fma_f32 v[78:79], v[74:75], v[78:79], s[34:35] op_sel_hi:[1,1,0]
	v_exp_f32_e32 v77, v53
	v_pk_fma_f32 v[78:79], v[74:75], v[78:79], s[40:41] op_sel_hi:[1,1,0]
	v_and_b32_e32 v73, 0x7fffffff, v71
	v_and_b32_e32 v72, 0x7fffffff, v70
	v_pk_mul_f32 v[74:75], v[74:75], v[78:79]
	v_max_f32_e32 v70, 0, v70
	v_max_f32_e32 v71, 0, v71
	v_pk_mul_f32 v[72:73], v[72:73], v[74:75]
	v_cvt_pk_f16_f32 v64, v64, v65
	v_pk_fma_f32 v[70:71], v[76:77], v[72:73], v[70:71] neg_lo:[1,0,0] neg_hi:[1,0,0]
	v_readlane_b32 s0, v52, 4
	v_cvt_pk_f16_f32 v65, v70, v71
	ds_write_b64 v136, v[64:65] offset:38400
	v_pk_mul_f32 v[64:65], s[0:1], v[68:69] op_sel_hi:[0,1]
	v_pk_fma_f32 v[64:65], v[64:65], v[238:239], v[242:243]
	v_pk_mul_f32 v[66:67], s[0:1], v[66:67] op_sel_hi:[0,1]
	v_fma_f32 v53, |v64|, s25, 1.0
	v_rcp_f32_e32 v70, v53
	v_fma_f32 v53, |v65|, s25, 1.0
	v_rcp_f32_e32 v71, v53
	v_pk_mul_f32 v[72:73], v[64:65], v[64:65]
	v_pk_fma_f32 v[66:67], v[66:67], v[240:241], v[244:245]
	v_mul_f32_e32 v53, 0xbf38aa3b, v72
	v_pk_fma_f32 v[74:75], v[70:71], s[22:23], v[90:91] op_sel_hi:[1,0,0]
	v_exp_f32_e32 v72, v53
	v_pk_fma_f32 v[74:75], v[70:71], v[74:75], s[24:25] op_sel_hi:[1,1,0]
	v_mul_f32_e32 v53, 0xbf38aa3b, v73
	v_pk_fma_f32 v[74:75], v[70:71], v[74:75], s[34:35] op_sel_hi:[1,1,0]
	v_and_b32_e32 v69, 0x7fffffff, v65
	v_pk_fma_f32 v[74:75], v[70:71], v[74:75], s[40:41] op_sel_hi:[1,1,0]
	v_and_b32_e32 v68, 0x7fffffff, v64
	v_exp_f32_e32 v73, v53
	v_pk_mul_f32 v[70:71], v[70:71], v[74:75]
	v_fma_f32 v53, |v66|, s25, 1.0
	v_pk_mul_f32 v[68:69], v[68:69], v[70:71]
	v_rcp_f32_e32 v70, v53
	v_fma_f32 v53, |v67|, s25, 1.0
	v_rcp_f32_e32 v71, v53
	v_max_f32_e32 v64, 0, v64
	v_max_f32_e32 v65, 0, v65
	v_pk_fma_f32 v[64:65], v[72:73], v[68:69], v[64:65] neg_lo:[1,0,0] neg_hi:[1,0,0]
	v_pk_mul_f32 v[72:73], v[66:67], v[66:67]
	v_pk_fma_f32 v[74:75], v[70:71], s[22:23], v[90:91] op_sel_hi:[1,0,0]
	v_mul_f32_e32 v53, 0xbf38aa3b, v72
	v_exp_f32_e32 v72, v53
	v_pk_fma_f32 v[74:75], v[70:71], v[74:75], s[24:25] op_sel_hi:[1,1,0]
	v_mul_f32_e32 v53, 0xbf38aa3b, v73
	v_pk_fma_f32 v[74:75], v[70:71], v[74:75], s[34:35] op_sel_hi:[1,1,0]
	v_exp_f32_e32 v73, v53
	v_pk_fma_f32 v[74:75], v[70:71], v[74:75], s[40:41] op_sel_hi:[1,1,0]
	v_readlane_b32 s0, v52, 5
	v_and_b32_e32 v69, 0x7fffffff, v67
	v_and_b32_e32 v68, 0x7fffffff, v66
	v_pk_mul_f32 v[70:71], v[70:71], v[74:75]
	v_pk_mul_f32 v[62:63], s[0:1], v[62:63] op_sel_hi:[0,1]
	v_max_f32_e32 v66, 0, v66
	v_max_f32_e32 v67, 0, v67
	v_pk_mul_f32 v[68:69], v[68:69], v[70:71]
	v_pk_fma_f32 v[62:63], v[62:63], v[238:239], v[242:243]
	v_pk_fma_f32 v[66:67], v[72:73], v[68:69], v[66:67] neg_lo:[1,0,0] neg_hi:[1,0,0]
	v_fma_f32 v53, |v62|, s25, 1.0
	v_cvt_pk_f16_f32 v64, v64, v65
	v_cvt_pk_f16_f32 v65, v66, v67
	v_rcp_f32_e32 v66, v53
	v_fma_f32 v53, |v63|, s25, 1.0
	v_rcp_f32_e32 v67, v53
	v_pk_mul_f32 v[68:69], v[62:63], v[62:63]
	v_pk_mul_f32 v[60:61], s[0:1], v[60:61] op_sel_hi:[0,1]
	v_mul_f32_e32 v53, 0xbf38aa3b, v68
	v_pk_fma_f32 v[70:71], v[66:67], s[22:23], v[90:91] op_sel_hi:[1,0,0]
	v_exp_f32_e32 v68, v53
	v_pk_fma_f32 v[70:71], v[66:67], v[70:71], s[24:25] op_sel_hi:[1,1,0]
	v_mul_f32_e32 v53, 0xbf38aa3b, v69
	v_pk_fma_f32 v[70:71], v[66:67], v[70:71], s[34:35] op_sel_hi:[1,1,0]
	v_pk_fma_f32 v[60:61], v[60:61], v[240:241], v[244:245]
	v_pk_fma_f32 v[70:71], v[66:67], v[70:71], s[40:41] op_sel_hi:[1,1,0]
	ds_write_b64 v123, v[64:65] offset:38912
	v_and_b32_e32 v65, 0x7fffffff, v63
	v_and_b32_e32 v64, 0x7fffffff, v62
	v_exp_f32_e32 v69, v53
	v_pk_mul_f32 v[66:67], v[66:67], v[70:71]
	v_fma_f32 v53, |v60|, s25, 1.0
	v_pk_mul_f32 v[64:65], v[64:65], v[66:67]
	v_rcp_f32_e32 v66, v53
	v_fma_f32 v53, |v61|, s25, 1.0
	v_rcp_f32_e32 v67, v53
	v_max_f32_e32 v62, 0, v62
	v_max_f32_e32 v63, 0, v63
	v_pk_fma_f32 v[62:63], v[68:69], v[64:65], v[62:63] neg_lo:[1,0,0] neg_hi:[1,0,0]
	v_pk_mul_f32 v[68:69], v[60:61], v[60:61]
	v_pk_fma_f32 v[70:71], v[66:67], s[22:23], v[90:91] op_sel_hi:[1,0,0]
	v_mul_f32_e32 v53, 0xbf38aa3b, v68
	v_exp_f32_e32 v68, v53
	v_pk_fma_f32 v[70:71], v[66:67], v[70:71], s[24:25] op_sel_hi:[1,1,0]
	v_mul_f32_e32 v53, 0xbf38aa3b, v69
	v_pk_fma_f32 v[70:71], v[66:67], v[70:71], s[34:35] op_sel_hi:[1,1,0]
	v_exp_f32_e32 v69, v53
	v_pk_fma_f32 v[70:71], v[66:67], v[70:71], s[40:41] op_sel_hi:[1,1,0]
	v_and_b32_e32 v65, 0x7fffffff, v61
	v_and_b32_e32 v64, 0x7fffffff, v60
	v_pk_mul_f32 v[66:67], v[66:67], v[70:71]
	v_readlane_b32 s0, v52, 6
	v_max_f32_e32 v60, 0, v60
	v_max_f32_e32 v61, 0, v61
	v_pk_mul_f32 v[64:65], v[64:65], v[66:67]
	v_pk_mul_f32 v[58:59], s[0:1], v[58:59] op_sel_hi:[0,1]
	v_pk_fma_f32 v[60:61], v[68:69], v[64:65], v[60:61] neg_lo:[1,0,0] neg_hi:[1,0,0]
	v_pk_fma_f32 v[58:59], v[58:59], v[238:239], v[242:243]
	v_cvt_pk_f16_f32 v62, v62, v63
	v_cvt_pk_f16_f32 v63, v60, v61
	v_fma_f32 v53, |v58|, s25, 1.0
	ds_write_b64 v133, v[62:63] offset:39424
	v_rcp_f32_e32 v62, v53
	v_fma_f32 v53, |v59|, s25, 1.0
	v_rcp_f32_e32 v63, v53
	v_pk_mul_f32 v[64:65], v[58:59], v[58:59]
	v_pk_mul_f32 v[56:57], s[0:1], v[56:57] op_sel_hi:[0,1]
	v_mul_f32_e32 v53, 0xbf38aa3b, v64
	v_pk_fma_f32 v[66:67], v[62:63], s[22:23], v[90:91] op_sel_hi:[1,0,0]
	v_exp_f32_e32 v64, v53
	v_pk_fma_f32 v[66:67], v[62:63], v[66:67], s[24:25] op_sel_hi:[1,1,0]
	v_mul_f32_e32 v53, 0xbf38aa3b, v65
	v_pk_fma_f32 v[66:67], v[62:63], v[66:67], s[34:35] op_sel_hi:[1,1,0]
	v_exp_f32_e32 v65, v53
	v_pk_fma_f32 v[66:67], v[62:63], v[66:67], s[40:41] op_sel_hi:[1,1,0]
	v_pk_fma_f32 v[56:57], v[56:57], v[240:241], v[244:245]
	v_and_b32_e32 v61, 0x7fffffff, v59
	v_and_b32_e32 v60, 0x7fffffff, v58
	v_pk_mul_f32 v[62:63], v[62:63], v[66:67]
	v_fma_f32 v53, |v56|, s25, 1.0
	v_pk_mul_f32 v[60:61], v[60:61], v[62:63]
	v_rcp_f32_e32 v62, v53
	v_fma_f32 v53, |v57|, s25, 1.0
	v_max_f32_e32 v58, 0, v58
	v_max_f32_e32 v59, 0, v59
	v_rcp_f32_e32 v63, v53
	v_pk_fma_f32 v[58:59], v[64:65], v[60:61], v[58:59] neg_lo:[1,0,0] neg_hi:[1,0,0]
	v_pk_mul_f32 v[64:65], v[56:57], v[56:57]
	v_readlane_b32 s0, v52, 7
	v_mul_f32_e32 v53, 0xbf38aa3b, v64
	v_exp_f32_e32 v64, v53
	v_mul_f32_e32 v53, 0xbf38aa3b, v65
	v_pk_fma_f32 v[66:67], v[62:63], s[22:23], v[90:91] op_sel_hi:[1,0,0]
	v_exp_f32_e32 v65, v53
	v_pk_mul_f32 v[52:53], s[0:1], v[54:55] op_sel_hi:[0,1]
	v_pk_fma_f32 v[66:67], v[62:63], v[66:67], s[24:25] op_sel_hi:[1,1,0]
	v_pk_fma_f32 v[42:43], v[52:53], v[238:239], v[242:243]
	v_pk_fma_f32 v[66:67], v[62:63], v[66:67], s[34:35] op_sel_hi:[1,1,0]
	v_fma_f32 v52, |v42|, s25, 1.0
	v_fma_f32 v53, |v43|, s25, 1.0
	v_pk_fma_f32 v[66:67], v[62:63], v[66:67], s[40:41] op_sel_hi:[1,1,0]
	v_rcp_f32_e32 v52, v52
	v_rcp_f32_e32 v53, v53
	v_and_b32_e32 v61, 0x7fffffff, v57
	v_and_b32_e32 v60, 0x7fffffff, v56
	v_pk_mul_f32 v[62:63], v[62:63], v[66:67]
	v_max_f32_e32 v56, 0, v56
	v_max_f32_e32 v57, 0, v57
	v_pk_mul_f32 v[60:61], v[60:61], v[62:63]
	v_cvt_pk_f16_f32 v58, v58, v59
	v_pk_fma_f32 v[56:57], v[64:65], v[60:61], v[56:57] neg_lo:[1,0,0] neg_hi:[1,0,0]
	v_pk_mul_f32 v[54:55], v[42:43], v[42:43]
	v_cvt_pk_f16_f32 v59, v56, v57
	v_pk_fma_f32 v[56:57], v[52:53], s[22:23], v[90:91] op_sel_hi:[1,0,0]
	v_mul_f32_e32 v54, 0xbf38aa3b, v54
	v_pk_fma_f32 v[56:57], v[52:53], v[56:57], s[24:25] op_sel_hi:[1,1,0]
	v_mul_f32_e32 v55, 0xbf38aa3b, v55
	v_exp_f32_e32 v54, v54
	v_pk_fma_f32 v[56:57], v[52:53], v[56:57], s[34:35] op_sel_hi:[1,1,0]
	v_exp_f32_e32 v55, v55
	v_pk_fma_f32 v[56:57], v[52:53], v[56:57], s[40:41] op_sel_hi:[1,1,0]
	v_and_b32_e32 v47, 0x7fffffff, v43
	v_and_b32_e32 v46, 0x7fffffff, v42
	v_pk_mul_f32 v[52:53], v[52:53], v[56:57]
	v_max_f32_e32 v42, 0, v42
	v_max_f32_e32 v43, 0, v43
	v_pk_mul_f32 v[46:47], v[46:47], v[52:53]
	ds_write_b64 v119, v[58:59] offset:39936
	v_pk_fma_f32 v[42:43], v[54:55], v[46:47], v[42:43] neg_lo:[1,0,0] neg_hi:[1,0,0]
	v_pk_mul_f32 v[46:47], s[0:1], v[50:51] op_sel_hi:[0,1]
	v_pk_fma_f32 v[44:45], v[46:47], v[240:241], v[244:245]
	v_cvt_pk_f16_f32 v42, v42, v43
	v_fma_f32 v43, |v44|, s25, 1.0
	v_rcp_f32_e32 v48, v43
	v_fma_f32 v43, |v45|, s25, 1.0
	v_rcp_f32_e32 v49, v43
	v_pk_mul_f32 v[50:51], v[44:45], v[44:45]
	v_and_b32_e32 v47, 0x7fffffff, v45
	v_mul_f32_e32 v43, 0xbf38aa3b, v50
	v_pk_fma_f32 v[52:53], v[48:49], s[22:23], v[90:91] op_sel_hi:[1,0,0]
	v_exp_f32_e32 v50, v43
	v_pk_fma_f32 v[52:53], v[48:49], v[52:53], s[24:25] op_sel_hi:[1,1,0]
	v_mul_f32_e32 v43, 0xbf38aa3b, v51
	v_pk_fma_f32 v[52:53], v[48:49], v[52:53], s[34:35] op_sel_hi:[1,1,0]
	v_exp_f32_e32 v51, v43
	v_pk_fma_f32 v[52:53], v[48:49], v[52:53], s[40:41] op_sel_hi:[1,1,0]
	v_and_b32_e32 v46, 0x7fffffff, v44
	v_pk_mul_f32 v[48:49], v[48:49], v[52:53]
	v_max_f32_e32 v44, 0, v44
	v_max_f32_e32 v45, 0, v45
	v_pk_mul_f32 v[46:47], v[46:47], v[48:49]
	s_waitcnt lgkmcnt(14)
	v_dot2c_f32_f16_e32 v104, v10, v10
	v_pk_fma_f32 v[44:45], v[50:51], v[46:47], v[44:45] neg_lo:[1,0,0] neg_hi:[1,0,0]
	v_dot2c_f32_f16_e32 v104, v11, v11
	v_cvt_pk_f16_f32 v43, v44, v45
	ds_write_b64 v146, v[42:43] offset:40448
	ds_read_b128 v[70:73], v115 offset:32768
	ds_read_b128 v[66:69], v147 offset:32768
	ds_read_b128 v[62:65], v148 offset:32768
	ds_read_b128 v[58:61], v149 offset:32768
	ds_read_b128 v[54:57], v150 offset:33024
	ds_read_b128 v[50:53], v151 offset:33024
	ds_read_b128 v[46:49], v152 offset:33024
	ds_read_b128 v[42:45], v153 offset:33024
	ds_read_b128 v[74:77], v95
	ds_read_b128 v[78:81], v95 offset:64
	ds_read_b128 v[82:85], v95 offset:128
	ds_read_b128 v[86:89], v95 offset:192
	ds_read_b128 v[90:93], v95 offset:256
	ds_read_b128 v[96:99], v95 offset:320
	s_waitcnt lgkmcnt(5)
	v_dot2c_f32_f16_e32 v105, v38, v74
	v_dot2c_f32_f16_e32 v105, v39, v75
	ds_read_b128 v[100:103], v95 offset:384
	ds_read_b128 v[108:111], v95 offset:448
	v_mov_b32_e32 v95, 0
	v_dot2c_f32_f16_e32 v105, v40, v76
	v_dot2c_f32_f16_e32 v95, v70, v70
	v_dot2c_f32_f16_e32 v105, v41, v77
	v_mov_b32_e32 v115, 0
	v_dot2c_f32_f16_e32 v95, v71, v71
	s_waitcnt lgkmcnt(6)
	v_dot2c_f32_f16_e32 v105, v34, v78
	v_dot2c_f32_f16_e32 v115, v70, v74
	v_dot2c_f32_f16_e32 v95, v72, v72
	v_dot2c_f32_f16_e32 v105, v35, v79
	v_dot2c_f32_f16_e32 v115, v71, v75
	v_dot2c_f32_f16_e32 v95, v73, v73
	v_dot2c_f32_f16_e32 v105, v36, v80
	v_dot2c_f32_f16_e32 v115, v72, v76
	v_dot2c_f32_f16_e32 v95, v66, v66
	v_dot2c_f32_f16_e32 v105, v37, v81
	v_dot2c_f32_f16_e32 v115, v73, v77
	v_dot2c_f32_f16_e32 v95, v67, v67
	s_waitcnt lgkmcnt(5)
	v_dot2c_f32_f16_e32 v105, v30, v82
	v_dot2c_f32_f16_e32 v115, v66, v78
	v_dot2c_f32_f16_e32 v95, v68, v68
	v_dot2c_f32_f16_e32 v105, v31, v83
	v_dot2c_f32_f16_e32 v115, v67, v79
	v_dot2c_f32_f16_e32 v95, v69, v69
	v_dot2c_f32_f16_e32 v105, v32, v84
	v_dot2c_f32_f16_e32 v115, v68, v80
	v_dot2c_f32_f16_e32 v95, v62, v62
	v_dot2c_f32_f16_e32 v105, v33, v85
	v_dot2c_f32_f16_e32 v115, v69, v81
	v_dot2c_f32_f16_e32 v95, v63, v63
	s_waitcnt lgkmcnt(4)
	v_dot2c_f32_f16_e32 v105, v26, v86
	v_dot2c_f32_f16_e32 v115, v62, v82
	v_dot2c_f32_f16_e32 v95, v64, v64
	v_dot2c_f32_f16_e32 v105, v27, v87
	v_dot2c_f32_f16_e32 v115, v63, v83
	v_dot2c_f32_f16_e32 v95, v65, v65
	v_dot2c_f32_f16_e32 v105, v28, v88
	v_dot2c_f32_f16_e32 v115, v64, v84
	v_dot2c_f32_f16_e32 v95, v58, v58
	v_dot2c_f32_f16_e32 v105, v29, v89
	v_dot2c_f32_f16_e32 v115, v65, v85
	v_dot2c_f32_f16_e32 v95, v59, v59
	s_waitcnt lgkmcnt(3)
	v_dot2c_f32_f16_e32 v105, v22, v90
	v_dot2c_f32_f16_e32 v115, v58, v86
	v_dot2c_f32_f16_e32 v95, v60, v60
	v_dot2c_f32_f16_e32 v105, v23, v91
	v_dot2c_f32_f16_e32 v115, v59, v87
	v_dot2c_f32_f16_e32 v95, v61, v61
	v_dot2c_f32_f16_e32 v105, v24, v92
	v_dot2c_f32_f16_e32 v115, v60, v88
	v_dot2c_f32_f16_e32 v95, v54, v54
	v_dot2c_f32_f16_e32 v105, v25, v93
	v_dot2c_f32_f16_e32 v115, v61, v89
	v_dot2c_f32_f16_e32 v95, v55, v55
	s_waitcnt lgkmcnt(2)
	v_dot2c_f32_f16_e32 v105, v18, v96
	v_dot2c_f32_f16_e32 v115, v54, v90
	v_dot2c_f32_f16_e32 v95, v56, v56
	v_dot2c_f32_f16_e32 v105, v19, v97
	v_dot2c_f32_f16_e32 v115, v55, v91
	v_dot2c_f32_f16_e32 v95, v57, v57
	v_dot2c_f32_f16_e32 v105, v20, v98
	v_dot2c_f32_f16_e32 v115, v56, v92
	v_dot2c_f32_f16_e32 v95, v50, v50
	v_dot2c_f32_f16_e32 v105, v21, v99
	v_dot2c_f32_f16_e32 v115, v57, v93
	v_dot2c_f32_f16_e32 v95, v51, v51
	s_waitcnt lgkmcnt(1)
	v_dot2c_f32_f16_e32 v105, v14, v100
	v_dot2c_f32_f16_e32 v115, v50, v96
	v_dot2c_f32_f16_e32 v95, v52, v52
	v_dot2c_f32_f16_e32 v105, v15, v101
	v_dot2c_f32_f16_e32 v115, v51, v97
	v_dot2c_f32_f16_e32 v95, v53, v53
	v_dot2c_f32_f16_e32 v105, v16, v102
	v_dot2c_f32_f16_e32 v115, v52, v98
	v_dot2c_f32_f16_e32 v95, v46, v46
	v_dot2c_f32_f16_e32 v105, v17, v103
	v_dot2c_f32_f16_e32 v115, v53, v99
	v_dot2c_f32_f16_e32 v95, v47, v47
	s_waitcnt lgkmcnt(0)
	v_dot2c_f32_f16_e32 v105, v10, v108
	v_dot2c_f32_f16_e32 v104, v12, v12
	v_dot2c_f32_f16_e32 v115, v46, v100
	v_dot2c_f32_f16_e32 v95, v48, v48
	v_dot2c_f32_f16_e32 v105, v11, v109
	v_dot2c_f32_f16_e32 v104, v13, v13
	v_dot2c_f32_f16_e32 v115, v47, v101
	v_dot2c_f32_f16_e32 v95, v49, v49
	v_dot2c_f32_f16_e32 v105, v12, v110
	v_dot2c_f32_f16_e32 v115, v48, v102
	v_dot2c_f32_f16_e32 v95, v42, v42
	v_mov_b32_e32 v74, v104
	v_dot2c_f32_f16_e32 v105, v13, v111
	v_dot2c_f32_f16_e32 v115, v49, v103
	v_dot2c_f32_f16_e32 v95, v43, v43
	v_permlane16_swap_b32_e32 v104, v74
	v_dot2c_f32_f16_e32 v115, v42, v108
	v_dot2c_f32_f16_e32 v95, v44, v44
	v_add_f32_e32 v133, v104, v74
	v_mov_b32_e32 v74, v105
	v_dot2c_f32_f16_e32 v115, v43, v109
	v_dot2c_f32_f16_e32 v95, v45, v45
	v_permlane16_swap_b32_e32 v105, v74
	v_dot2c_f32_f16_e32 v115, v44, v110
	v_add_f32_e32 v137, v105, v74
	v_mov_b32_e32 v74, v95
	v_dot2c_f32_f16_e32 v115, v45, v111
	s_nop 0
	v_permlane16_swap_b32_e32 v95, v74
	v_add_f32_e32 v135, v95, v74
	v_mov_b32_e32 v74, v115
	s_nop 1
	v_permlane16_swap_b32_e32 v115, v74
	v_add_f32_e32 v139, v115, v74
	v_lshlrev_b32_e32 v74, 8, v107
	v_lshlrev_b32_e32 v75, 3, v114
	s_movk_i32 s0, 0x78
	v_and_or_b32 v76, v75, s0, v74
	v_lshlrev_b32_e32 v75, 3, v141
	v_and_or_b32 v77, v75, s0, v74
	v_lshlrev_b32_e32 v75, 3, v142
	v_and_or_b32 v78, v75, s0, v74
	v_lshlrev_b32_e32 v75, 3, v143
	v_and_or_b32 v79, v75, s0, v74
	s_add_u32 s0, s26, 0x8000
	v_or_b32_e32 v108, 0x8000, v112
	v_mov_b32_e32 v123, 0
	s_addc_u32 s1, s27, 0
	v_readfirstlane_b32 s4, v108
	s_waitcnt vmcnt(0)
	s_barrier
	v_lshl_add_u64 v[74:75], s[0:1], 0, v[122:123]
	s_mov_b32 m0, s4
	s_nop 0
	global_load_lds_dwordx4 v[74:75], off
	s_addk_i32 s4, 0x400
	v_mov_b32_e32 v107, v123
	v_lshl_add_u64 v[74:75], s[0:1], 0, v[106:107]
	s_add_u32 s0, s26, 0xc000
	s_mov_b32 m0, s4
	s_nop 0
	global_load_lds_dwordx4 v[74:75], off
	s_addc_u32 s1, s27, 0
	v_or_b32_e32 v109, 0xc000, v112
	v_lshl_add_u64 v[74:75], s[0:1], 0, v[122:123]
	v_readfirstlane_b32 s4, v109
	s_mov_b32 m0, s4
	s_nop 0
	global_load_lds_dwordx4 v[74:75], off
	s_addk_i32 s4, 0x400
	v_lshl_add_u64 v[74:75], s[0:1], 0, v[106:107]
	s_mov_b32 m0, s4
	s_nop 0
	global_load_lds_dwordx4 v[74:75], off
	v_mov_b32_e32 v134, v133
	v_mov_b32_e32 v138, v137
	v_mov_b32_e32 v136, v135
	v_mov_b32_e32 v140, v139
	v_lshlrev_b32_e32 v144, 1, v76
	v_lshlrev_b32_e32 v143, 1, v77
	v_lshlrev_b32_e32 v142, 1, v78
	v_lshlrev_b32_e32 v141, 1, v79
	s_add_u32 s0, s26, 0x14000
	v_mov_b32_e32 v74, 0x7f61b1e6
	v_permlane32_swap_b32_e32 v133, v134
	v_permlane32_swap_b32_e32 v137, v138
	v_permlane32_swap_b32_e32 v135, v136
	v_permlane32_swap_b32_e32 v139, v140
	v_or_b32_e32 v160, 0x10000, v144
	v_or_b32_e32 v158, 0x10000, v143
	v_or_b32_e32 v156, 0x10000, v142
	v_or_b32_e32 v154, 0x10000, v141
	v_or_b32_e32 v159, 0x12000, v144
	v_or_b32_e32 v157, 0x12000, v143
	v_or_b32_e32 v155, 0x12000, v142
	v_or_b32_e32 v153, 0x12000, v141
	v_or_b32_e32 v152, 0x14000, v144
	v_or_b32_e32 v150, 0x14000, v143
	v_or_b32_e32 v148, 0x14000, v142
	v_or_b32_e32 v146, 0x14000, v141
	v_or_b32_e32 v151, 0x16000, v144
	v_or_b32_e32 v149, 0x16000, v143
	v_or_b32_e32 v147, 0x16000, v142
	v_or_b32_e32 v145, 0x16000, v141
	s_addc_u32 s1, s27, 0
	v_mov_b32_e32 v98, 0x7f800000
	s_mov_b32 s22, 0
	v_mov_b32_e32 v100, 0x7f800000
	v_mov_b32_e32 v99, 0x7f800000
	v_mov_b32_e32 v111, 0x7f800000
	v_mov_b32_e32 v101, 0x7f800000
	v_mov_b32_e32 v110, 0x7f800000
	v_mov_b32_e32 v75, v74
	v_mov_b32_e32 v76, v74
	v_mov_b32_e32 v77, v74
	v_mov_b32_e32 v78, v74
	v_mov_b32_e32 v79, v74
	v_mov_b32_e32 v80, v74
	v_mov_b32_e32 v81, v74
	v_mov_b32_e32 v82, v74
	v_mov_b32_e32 v83, v74
	v_mov_b32_e32 v84, v74
	v_mov_b32_e32 v85, v74
	v_mov_b32_e32 v86, v74
	v_mov_b32_e32 v87, v74
	v_mov_b32_e32 v88, v74
	v_mov_b32_e32 v89, v74
	v_mov_b32_e32 v247, 0xfffffc00
	v_readfirstlane_b32 s96, v1
	s_nop 3
	s_cmp_lt_u32 s96, 4
	s_cbranch_scc0 .Lmy_prio_done
	s_setprio 1
.Lmy_prio_done:
.LBB1_7:
	s_add_u32 s4, s0, 0xffffc000
	v_readfirstlane_b32 s8, v112
	s_addc_u32 s5, s1, -1
	s_add_i32 s35, s8, 0x10000
	v_lshl_add_u64 v[96:97], s[4:5], 0, v[122:123]
	s_mov_b32 m0, s35
	s_nop 0
	global_load_lds_dwordx4 v[96:97], off
	s_add_i32 s34, s8, 0x10400
	v_lshl_add_u64 v[102:103], s[4:5], 0, v[106:107]
	s_mov_b32 m0, s34
	s_nop 0
	global_load_lds_dwordx4 v[102:103], off
	v_lshl_add_u64 v[90:91], s[0:1], 0, v[122:123]
	s_add_i32 s6, s8, 0x14000
	s_mov_b32 m0, s6
	s_nop 0
	global_load_lds_dwordx4 v[90:91], off
	v_lshl_add_u64 v[92:93], s[0:1], 0, v[106:107]
	s_add_i32 s7, s8, 0x14400
	s_mov_b32 m0, s7
	s_nop 0
	global_load_lds_dwordx4 v[92:93], off
	ds_read_b128 v[90:93], v144
	ds_read_b128 v[118:121], v144 offset:8192
	v_add_u32_e32 v95, s3, v94
	v_add_u32_e32 v96, 0x18060, v95
	v_add_u32_e32 v97, 0x180a0, v95
	ds_read_b128 v[102:105], v96
	ds_read_b128 v[162:165], v97
	s_lshl_b32 s24, s22, 5
	s_or_b32 s70, s24, 1
	s_or_b32 s71, s24, 2
	s_or_b32 s72, s24, 3
	s_or_b32 s73, s24, 17
	s_or_b32 s74, s24, 18
	s_or_b32 s75, s24, 19
	v_and_or_b32 v86, v86, v247, s24
	v_med3_f32 v111, v101, v111, v86
	v_med3_f32 v101, v110, v101, v86
	v_min_f32 v110, v110, v86
	s_waitcnt lgkmcnt(1)
	v_mfma_f32_16x16x32_f16 v[114:117], v[90:93], v[38:41], v[102:105]
	s_or_b32 s41, s24, 16
	ds_read_b128 v[166:169], v143 offset:8448
	ds_read_b128 v[170:173], v142 offset:8448
	v_mfma_f32_16x16x32_f16 v[90:93], v[90:93], v[70:73], v[102:105]
	v_and_or_b32 v96, v89, v247, s72
	ds_read_b128 v[102:105], v143
	v_and_or_b32 v97, v87, v247, s70
	v_and_or_b32 v161, v88, v247, s71
	s_waitcnt lgkmcnt(3)
	v_mfma_f32_16x16x32_f16 v[86:89], v[118:121], v[38:41], v[162:165]
	ds_read_b128 v[174:177], v141 offset:8448
	v_med3_f32 v111, v101, v111, v97
	v_med3_f32 v101, v110, v101, v97
	v_mfma_f32_16x16x32_f16 v[118:121], v[118:121], v[70:73], v[162:165]
	ds_read_b128 v[162:165], v143 offset:8192
	v_and_or_b32 v230, v82, v247, s24
	v_and_or_b32 v231, v83, v247, s70
	s_waitcnt lgkmcnt(2)
	v_mfma_f32_16x16x32_f16 v[114:117], v[102:105], v[34:37], v[114:117]
	v_min_f32 v97, v110, v97
	ds_read_b128 v[202:205], v144 offset:24576
	v_med3_f32 v110, v101, v111, v161
	v_mfma_f32_16x16x32_f16 v[90:93], v[102:105], v[66:69], v[90:93]
	v_and_or_b32 v232, v84, v247, s71
	v_and_or_b32 v233, v85, v247, s72
	s_waitcnt lgkmcnt(1)
	v_mfma_f32_16x16x32_f16 v[82:85], v[162:165], v[34:37], v[86:89]
	v_med3_f32 v101, v97, v101, v161
	v_min_f32 v97, v97, v161
	v_med3_f32 v98, v100, v98, v230
	v_mfma_f32_16x16x32_f16 v[102:105], v[162:165], v[66:69], v[118:121]
	v_and_or_b32 v234, v78, v247, s41
	s_nop 0
	ds_read_b128 v[86:89], v142
	ds_read_b128 v[118:121], v142 offset:8192
	v_and_or_b32 v235, v79, v247, s73
	v_and_or_b32 v236, v80, v247, s74
	s_waitcnt lgkmcnt(1)
	v_mfma_f32_16x16x32_f16 v[114:117], v[86:89], v[30:33], v[114:117]
	ds_read_b128 v[162:165], v144 offset:8448
	v_med3_f32 v100, v99, v100, v230
	ds_read_b128 v[178:181], v143 offset:16384
	v_mfma_f32_16x16x32_f16 v[86:89], v[86:89], v[62:65], v[90:93]
	v_and_or_b32 v237, v81, v247, s75
	v_and_or_b32 v238, v74, v247, s41
	s_waitcnt lgkmcnt(2)
	v_mfma_f32_16x16x32_f16 v[78:81], v[118:121], v[30:33], v[82:85]
	ds_read_b128 v[206:209], v143 offset:24576
	s_add_i32 s9, s23, 0xffffff70
	s_or_b32 s76, s9, 1
	s_or_b32 s77, s9, 2
	s_or_b32 s78, s9, 3
	s_or_b32 s79, s9, 17
	s_or_b32 s80, s9, 18
	s_or_b32 s81, s9, 19
	ds_read_b128 v[182:185], v142 offset:16384
	ds_read_b128 v[82:85], v141
	v_mfma_f32_16x16x32_f16 v[90:93], v[118:121], v[62:65], v[102:105]
	v_and_or_b32 v239, v75, v247, s73
	v_and_or_b32 v240, v76, v247, s74
	v_and_or_b32 v241, v77, v247, s75
	s_waitcnt lgkmcnt(0)
	v_mfma_f32_16x16x32_f16 v[74:77], v[82:85], v[26:29], v[114:117]
	ds_read_b128 v[102:105], v144 offset:256
	s_nop 1
	ds_read_b128 v[114:117], v143 offset:256
	ds_read_b128 v[118:121], v141 offset:256
	v_mfma_f32_16x16x32_f16 v[82:85], v[82:85], v[58:61], v[86:89]
	ds_read_b128 v[210:213], v142 offset:24576
	s_add_i32 s25, s23, 0xffffff80
	ds_read_b128 v[186:189], v141 offset:16384
	ds_read_b128 v[86:89], v141 offset:8192
	s_waitcnt lgkmcnt(0)
	v_mfma_f32_16x16x32_f16 v[78:81], v[86:89], v[26:29], v[78:81]
	ds_read_b128 v[214:217], v141 offset:24576
	ds_read_b128 v[190:193], v144 offset:16640
	s_add_u32 s4, s0, 0x4000
	v_mfma_f32_16x16x32_f16 v[86:89], v[86:89], v[58:61], v[90:93]
	s_addc_u32 s5, s1, 0
	s_add_i32 s40, s8, 0x400
	s_add_u32 s6, s0, 0x8000
	ds_read_b128 v[90:93], v142 offset:256
	v_mfma_f32_16x16x32_f16 v[74:77], v[102:105], v[22:25], v[74:77]
	s_addc_u32 s7, s1, 0
	ds_read_b128 v[194:197], v143 offset:16640
	ds_read_b128 v[218:221], v143 offset:24832
	v_mfma_f32_16x16x32_f16 v[82:85], v[102:105], v[54:57], v[82:85]
	ds_read_b128 v[102:105], v144 offset:16384
	ds_read_b128 v[222:225], v142 offset:24832
	ds_read_b128 v[198:201], v141 offset:16640
	v_mfma_f32_16x16x32_f16 v[78:81], v[162:165], v[22:25], v[78:81]
	ds_read_b128 v[226:229], v141 offset:24832
	s_add_i32 s35, s23, 0xffffff90
	s_or_b32 s82, s35, 1
	s_or_b32 s83, s35, 2
	s_or_b32 s84, s35, 3
	s_or_b32 s85, s35, 17
	s_or_b32 s86, s35, 18
	s_or_b32 s87, s35, 19
	s_add_i32 s41, s23, 0xffffffa0
	v_mfma_f32_16x16x32_f16 v[86:89], v[162:165], v[54:57], v[86:89]
	ds_read_b128 v[162:165], v142 offset:16640
	s_add_i32 s24, s23, 0xffffffb0
	s_or_b32 s70, s24, 1
	s_or_b32 s71, s24, 2
	s_or_b32 s72, s24, 3
	s_or_b32 s73, s24, 17
	s_or_b32 s74, s24, 18
	s_or_b32 s75, s24, 19
	s_sub_i32 s34, s23, 64
	v_mfma_f32_16x16x32_f16 v[74:77], v[114:117], v[18:21], v[74:77]
	s_mov_b32 s22, s33
	v_mfma_f32_16x16x32_f16 v[82:85], v[114:117], v[50:53], v[82:85]
	ds_read_b128 v[114:117], v144 offset:24832
	v_mfma_f32_16x16x32_f16 v[78:81], v[166:169], v[18:21], v[78:81]
	v_mfma_f32_16x16x32_f16 v[86:89], v[166:169], v[50:53], v[86:89]
	s_waitcnt lgkmcnt(8)
	v_mfma_f32_16x16x32_f16 v[74:77], v[90:93], v[14:17], v[74:77]
	v_mfma_f32_16x16x32_f16 v[82:85], v[90:93], v[46:49], v[82:85]
	v_min_f32 v90, v99, v230
	v_med3_f32 v91, v101, v110, v96
	v_med3_f32 v92, v97, v101, v96
	v_min_f32 v93, v97, v96
	v_med3_f32 v96, v100, v98, v231
	v_add_u32_e32 v99, 0x18120, v95
	v_med3_f32 v97, v90, v100, v231
	v_min_f32 v90, v90, v231
	v_med3_f32 v110, v92, v91, v234
	v_med3_f32 v111, v93, v92, v234
	s_nop 0
	v_med3_f32 v96, v97, v96, v232
	v_med3_f32 v97, v90, v97, v232
	v_min_f32 v98, v90, v232
	v_add_u32_e32 v90, 0x180e0, v95
	v_mfma_f32_16x16x32_f16 v[78:81], v[170:173], v[14:17], v[78:81]
	v_med3_f32 v167, v98, v97, v233
	v_min_f32 v168, v98, v233
	v_mfma_f32_16x16x32_f16 v[86:89], v[170:173], v[46:49], v[86:89]
	v_mfma_f32_16x16x32_f16 v[74:77], v[118:121], v[10:13], v[74:77]
	v_mfma_f32_16x16x32_f16 v[82:85], v[118:121], v[42:45], v[82:85]
	v_min_f32 v119, v93, v234
	ds_read_b128 v[90:93], v90
	v_med3_f32 v120, v97, v96, v233
	ds_read_b128 v[96:99], v99
	s_nop 4
	v_and_or_b32 v118, v74, v247, s9
	v_and_or_b32 v121, v75, v247, s76
	v_mfma_f32_16x16x32_f16 v[78:81], v[174:177], v[10:13], v[78:81]
	s_waitcnt vmcnt(4)
	s_waitcnt lgkmcnt(0)
	s_barrier
	v_mfma_f32_16x16x32_f16 v[86:89], v[174:177], v[42:45], v[86:89]
	v_and_or_b32 v161, v76, v247, s77
	v_and_or_b32 v166, v77, v247, s78
	s_waitcnt lgkmcnt(1)
	v_mfma_f32_16x16x32_f16 v[74:77], v[102:105], v[38:41], v[90:93]
	v_mfma_f32_16x16x32_f16 v[90:93], v[102:105], v[70:73], v[90:93]
	v_and_or_b32 v104, v82, v247, s9
	v_and_or_b32 v105, v83, v247, s76
	v_med3_f32 v82, v111, v110, v235
	v_med3_f32 v83, v119, v111, v235
	v_and_or_b32 v111, v84, v247, s77
	s_waitcnt lgkmcnt(0)
	v_mfma_f32_16x16x32_f16 v[100:103], v[202:205], v[38:41], v[96:99]
	v_min_f32 v110, v119, v235
	v_med3_f32 v170, v83, v82, v236
	v_mfma_f32_16x16x32_f16 v[96:99], v[202:205], v[70:73], v[96:99]
	v_and_or_b32 v169, v78, v247, s25
	v_and_or_b32 v119, v85, v247, s78
	v_mfma_f32_16x16x32_f16 v[74:77], v[178:181], v[34:37], v[74:77]
	v_med3_f32 v171, v110, v83, v236
	v_min_f32 v110, v110, v236
	v_mfma_f32_16x16x32_f16 v[82:85], v[178:181], v[66:69], v[90:93]
	v_and_b32_e32 v172, 0xfffffc00, v81
	v_and_or_b32 v173, v79, v247, s79
	v_and_or_b32 v174, v80, v247, s80
	v_mfma_f32_16x16x32_f16 v[90:93], v[206:209], v[66:69], v[96:99]
	v_min_f32 v99, v168, v238
	v_mfma_f32_16x16x32_f16 v[78:81], v[206:209], v[34:37], v[100:103]
	s_nop 0
	v_and_or_b32 v97, v86, v247, s25
	v_and_or_b32 v98, v87, v247, s79
	v_med3_f32 v86, v167, v120, v238
	v_med3_f32 v87, v168, v167, v238
	v_med3_f32 v100, v171, v170, v237
	v_med3_f32 v101, v110, v171, v237
	v_min_f32 v102, v110, v237
	v_or3_b32 v96, s9, v172, 19
	v_mfma_f32_16x16x32_f16 v[74:77], v[182:185], v[30:33], v[74:77]
	v_med3_f32 v120, v87, v86, v239
	v_med3_f32 v167, v99, v87, v239
	v_min_f32 v99, v99, v239
	v_mfma_f32_16x16x32_f16 v[82:85], v[182:185], v[62:65], v[82:85]
	v_and_or_b32 v103, v88, v247, s80
	v_and_or_b32 v110, v89, v247, s81
	v_mfma_f32_16x16x32_f16 v[86:89], v[210:213], v[62:65], v[90:93]
	v_med3_f32 v90, v167, v120, v240
	v_med3_f32 v91, v99, v167, v240
	v_min_f32 v92, v99, v240
	v_med3_f32 v93, v101, v100, v118
	v_med3_f32 v99, v102, v101, v118
	v_min_f32 v100, v102, v118
	v_mfma_f32_16x16x32_f16 v[78:81], v[210:213], v[30:33], v[78:81]
	v_med3_f32 v90, v91, v90, v241
	v_med3_f32 v91, v92, v91, v241
	v_min_f32 v92, v92, v241
	v_med3_f32 v93, v99, v93, v121
	v_med3_f32 v99, v100, v99, v121
	v_min_f32 v100, v100, v121
	v_mfma_f32_16x16x32_f16 v[74:77], v[186:189], v[26:29], v[74:77]
	v_med3_f32 v90, v91, v90, v104
	v_med3_f32 v91, v92, v91, v104
	v_min_f32 v92, v92, v104
	v_med3_f32 v93, v99, v93, v161
	v_med3_f32 v99, v100, v99, v161
	v_min_f32 v100, v100, v161
	v_mfma_f32_16x16x32_f16 v[82:85], v[186:189], v[58:61], v[82:85]
	v_med3_f32 v90, v91, v90, v105
	v_med3_f32 v91, v92, v91, v105
	v_min_f32 v92, v92, v105
	v_med3_f32 v93, v99, v93, v166
	v_med3_f32 v99, v100, v99, v166
	v_min_f32 v100, v100, v166
	s_nop 0
	v_med3_f32 v90, v91, v90, v111
	v_med3_f32 v91, v92, v91, v111
	v_min_f32 v92, v92, v111
	v_med3_f32 v93, v99, v93, v169
	v_med3_f32 v99, v100, v99, v169
	v_min_f32 v100, v100, v169
	s_nop 0
	v_med3_f32 v90, v91, v90, v119
	v_med3_f32 v91, v92, v91, v119
	v_min_f32 v92, v92, v119
	v_med3_f32 v93, v99, v93, v173
	v_med3_f32 v99, v100, v99, v173
	v_min_f32 v100, v100, v173
	s_nop 0
	v_med3_f32 v90, v91, v90, v97
	v_med3_f32 v91, v92, v91, v97
	v_min_f32 v92, v92, v97
	v_med3_f32 v93, v99, v93, v174
	v_med3_f32 v99, v100, v99, v174
	v_min_f32 v100, v100, v174
	s_nop 0
	v_med3_f32 v90, v91, v90, v98
	v_med3_f32 v91, v92, v91, v98
	v_min_f32 v92, v92, v98
	v_med3_f32 v104, v99, v93, v96
	v_med3_f32 v105, v100, v99, v96
	v_min_f32 v111, v100, v96
	v_lshl_add_u64 v[96:97], s[6:7], 0, v[122:123]
	v_med3_f32 v100, v91, v90, v103
	v_med3_f32 v101, v92, v91, v103
	v_min_f32 v102, v92, v103
	v_lshl_add_u64 v[90:91], s[4:5], 0, v[122:123]
	v_lshl_add_u64 v[92:93], s[4:5], 0, v[106:107]
	v_readfirstlane_b32 s5, v113
	v_lshl_add_u64 v[98:99], s[6:7], 0, v[106:107]
	v_mfma_f32_16x16x32_f16 v[78:81], v[214:217], v[26:29], v[78:81]
	s_mov_b32 m0, s8
	s_nop 0
	global_load_lds_dwordx4 v[90:91], off
	s_add_i32 s6, s5, 0x400
	s_mov_b32 m0, s40
	s_nop 0
	global_load_lds_dwordx4 v[92:93], off
	v_mfma_f32_16x16x32_f16 v[86:89], v[214:217], v[58:61], v[86:89]
	s_mov_b32 m0, s5
	s_nop 0
	global_load_lds_dwordx4 v[96:97], off
	v_med3_f32 v161, v101, v100, v110
	v_med3_f32 v230, v102, v101, v110
	v_mfma_f32_16x16x32_f16 v[74:77], v[190:193], v[22:25], v[74:77]
	s_mov_b32 m0, s6
	s_nop 0
	global_load_lds_dwordx4 v[98:99], off
	ds_read_b128 v[90:93], v144 offset:32768
	v_min_f32 v110, v102, v110
	v_mfma_f32_16x16x32_f16 v[82:85], v[190:193], v[54:57], v[82:85]
	ds_read_b128 v[166:169], v143 offset:41216
	ds_read_b128 v[170:173], v142 offset:41216
	ds_read_b128 v[174:177], v141 offset:41216
	v_mfma_f32_16x16x32_f16 v[78:81], v[114:117], v[22:25], v[78:81]
	ds_read_b128 v[202:205], v144 offset:57344
	ds_read_b128 v[178:181], v143 offset:49152
	ds_read_b128 v[182:185], v142 offset:49152
	v_mfma_f32_16x16x32_f16 v[86:89], v[114:117], v[54:57], v[86:89]
	ds_read_b128 v[114:117], v144 offset:40960
	ds_read_b128 v[206:209], v143 offset:57344
	ds_read_b128 v[186:189], v141 offset:49152
	v_mfma_f32_16x16x32_f16 v[74:77], v[194:197], v[18:21], v[74:77]
	ds_read_b128 v[210:213], v142 offset:57344
	ds_read_b128 v[190:193], v144 offset:49408
	ds_read_b128 v[214:217], v141 offset:57344
	v_mfma_f32_16x16x32_f16 v[82:85], v[194:197], v[50:53], v[82:85]
	ds_read_b128 v[194:197], v143 offset:49408
	s_add_u32 s4, s0, 0xc000
	s_addc_u32 s5, s1, 0
	v_mfma_f32_16x16x32_f16 v[78:81], v[218:221], v[18:21], v[78:81]
	v_mfma_f32_16x16x32_f16 v[86:89], v[218:221], v[50:53], v[86:89]
	ds_read_b128 v[218:221], v143 offset:57600
	v_mfma_f32_16x16x32_f16 v[74:77], v[162:165], v[14:17], v[74:77]
	v_mfma_f32_16x16x32_f16 v[82:85], v[162:165], v[46:49], v[82:85]
	ds_read_b128 v[162:165], v144 offset:41216
	v_mfma_f32_16x16x32_f16 v[78:81], v[222:225], v[14:17], v[78:81]
	v_mfma_f32_16x16x32_f16 v[86:89], v[222:225], v[46:49], v[86:89]
	ds_read_b128 v[222:225], v142 offset:57600
	v_mfma_f32_16x16x32_f16 v[74:77], v[198:201], v[10:13], v[74:77]
	v_mfma_f32_16x16x32_f16 v[82:85], v[198:201], v[42:45], v[82:85]
	ds_read_b128 v[198:201], v141 offset:49408
	v_mfma_f32_16x16x32_f16 v[78:81], v[226:229], v[10:13], v[78:81]
	v_mfma_f32_16x16x32_f16 v[86:89], v[226:229], v[42:45], v[86:89]
	v_add_u32_e32 v100, 0x18160, v95
	ds_read_b128 v[96:99], v100
	s_nop 1
	v_add_u32_e32 v118, 0x181a0, v95
	v_and_or_b32 v231, v74, v247, s35
	s_waitcnt lgkmcnt(0)
	v_mfma_f32_16x16x32_f16 v[100:103], v[90:93], v[38:41], v[96:99]
	ds_read_b128 v[118:121], v118
	v_med3_f32 v104, v105, v104, v231
	v_med3_f32 v105, v111, v105, v231
	v_mfma_f32_16x16x32_f16 v[90:93], v[90:93], v[70:73], v[96:99]
	v_and_or_b32 v232, v75, v247, s82
	ds_read_b128 v[96:99], v143 offset:32768
	v_and_or_b32 v233, v76, v247, s83
	v_and_or_b32 v234, v77, v247, s84
	s_waitcnt lgkmcnt(1)
	v_mfma_f32_16x16x32_f16 v[74:77], v[114:117], v[38:41], v[118:121]
	v_min_f32 v111, v111, v231
	v_med3_f32 v104, v105, v104, v232
	ds_read_b128 v[226:229], v141 offset:57600
	v_mfma_f32_16x16x32_f16 v[114:117], v[114:117], v[70:73], v[118:121]
	v_and_or_b32 v235, v82, v247, s35
	v_and_or_b32 v236, v83, v247, s82
	s_waitcnt lgkmcnt(1)
	v_mfma_f32_16x16x32_f16 v[100:103], v[96:99], v[34:37], v[100:103]
	ds_read_b128 v[118:121], v143 offset:40960
	v_med3_f32 v105, v111, v105, v232
	v_min_f32 v111, v111, v232
	v_mfma_f32_16x16x32_f16 v[90:93], v[96:99], v[66:69], v[90:93]
	v_and_or_b32 v237, v84, v247, s83
	v_and_or_b32 v238, v85, v247, s84
	ds_read_b128 v[82:85], v142 offset:32768
	v_and_or_b32 v239, v78, v247, s41
	s_waitcnt lgkmcnt(1)
	v_mfma_f32_16x16x32_f16 v[74:77], v[118:121], v[34:37], v[74:77]
	v_med3_f32 v104, v105, v104, v233
	v_med3_f32 v105, v111, v105, v233
	v_min_f32 v111, v111, v233
	v_mfma_f32_16x16x32_f16 v[96:99], v[118:121], v[66:69], v[114:117]
	v_and_or_b32 v240, v79, v247, s85
	v_and_or_b32 v242, v81, v247, s87
	v_and_or_b32 v241, v80, v247, s86
	s_waitcnt lgkmcnt(0)
	v_mfma_f32_16x16x32_f16 v[78:81], v[82:85], v[30:33], v[100:103]
	ds_read_b128 v[118:121], v141 offset:33024
	v_med3_f32 v104, v105, v104, v234
	v_med3_f32 v105, v111, v105, v234
	v_mfma_f32_16x16x32_f16 v[82:85], v[82:85], v[62:65], v[90:93]
	ds_read_b128 v[100:103], v142 offset:40960
	ds_read_b128 v[90:93], v141 offset:32768
	v_and_or_b32 v243, v86, v247, s41
	v_and_or_b32 v244, v87, v247, s85
	s_waitcnt lgkmcnt(1)
	v_mfma_f32_16x16x32_f16 v[74:77], v[100:103], v[30:33], v[74:77]
	ds_read_b128 v[114:117], v143 offset:33024
	v_min_f32 v111, v111, v234
	v_mfma_f32_16x16x32_f16 v[96:99], v[100:103], v[62:65], v[96:99]
	v_and_or_b32 v245, v88, v247, s86
	v_and_or_b32 v246, v89, v247, s87
	ds_read_b128 v[86:89], v141 offset:40960
	ds_read_b128 v[100:103], v144 offset:33024
	s_waitcnt lgkmcnt(3)
	v_mfma_f32_16x16x32_f16 v[78:81], v[90:93], v[26:29], v[78:81]
	v_mfma_f32_16x16x32_f16 v[82:85], v[90:93], v[58:61], v[82:85]
	ds_read_b128 v[90:93], v142 offset:33024
	s_waitcnt lgkmcnt(2)
	v_mfma_f32_16x16x32_f16 v[74:77], v[86:89], v[26:29], v[74:77]
	v_mfma_f32_16x16x32_f16 v[86:89], v[86:89], v[58:61], v[96:99]
	s_waitcnt lgkmcnt(1)
	v_mfma_f32_16x16x32_f16 v[78:81], v[100:103], v[22:25], v[78:81]
	s_nop 0
	ds_read_b128 v[96:99], v144 offset:49152
	v_mfma_f32_16x16x32_f16 v[82:85], v[100:103], v[54:57], v[82:85]
	ds_read_b128 v[100:103], v142 offset:49408
	v_mfma_f32_16x16x32_f16 v[74:77], v[162:165], v[22:25], v[74:77]
	v_mfma_f32_16x16x32_f16 v[86:89], v[162:165], v[54:57], v[86:89]
	ds_read_b128 v[162:165], v144 offset:57600
	v_mfma_f32_16x16x32_f16 v[78:81], v[114:117], v[18:21], v[78:81]
	v_mfma_f32_16x16x32_f16 v[82:85], v[114:117], v[50:53], v[82:85]
	v_med3_f32 v114, v230, v161, v235
	v_med3_f32 v115, v110, v230, v235
	v_mfma_f32_16x16x32_f16 v[74:77], v[166:169], v[18:21], v[74:77]
	v_mfma_f32_16x16x32_f16 v[86:89], v[166:169], v[50:53], v[86:89]
	s_waitcnt lgkmcnt(3)
	v_mfma_f32_16x16x32_f16 v[78:81], v[90:93], v[14:17], v[78:81]
	v_mfma_f32_16x16x32_f16 v[82:85], v[90:93], v[46:49], v[82:85]
	v_min_f32 v90, v110, v235
	v_med3_f32 v91, v115, v114, v236
	s_nop 0
	v_med3_f32 v92, v90, v115, v236
	v_min_f32 v90, v90, v236
	s_nop 0
	v_med3_f32 v91, v92, v91, v237
	v_med3_f32 v92, v90, v92, v237
	v_min_f32 v90, v90, v237
	s_nop 0
	v_med3_f32 v110, v92, v91, v238
	v_med3_f32 v161, v90, v92, v238
	v_min_f32 v166, v90, v238
	v_med3_f32 v90, v105, v104, v239
	v_med3_f32 v104, v111, v105, v239
	v_add_u32_e32 v91, 0x181e0, v95
	v_add_u32_e32 v105, 0x18220, v95
	v_mfma_f32_16x16x32_f16 v[74:77], v[170:173], v[14:17], v[74:77]
	ds_read_b128 v[114:117], v105
	v_min_f32 v111, v111, v239
	v_mfma_f32_16x16x32_f16 v[86:89], v[170:173], v[46:49], v[86:89]
	v_mfma_f32_16x16x32_f16 v[78:81], v[118:121], v[10:13], v[78:81]
	v_mfma_f32_16x16x32_f16 v[82:85], v[118:121], v[42:45], v[82:85]
	v_med3_f32 v119, v104, v90, v240
	ds_read_b128 v[90:93], v91
	s_nop 5
	v_and_or_b32 v118, v78, v247, s24
	v_and_or_b32 v120, v79, v247, s70
	v_mfma_f32_16x16x32_f16 v[74:77], v[174:177], v[10:13], v[74:77]
	v_med3_f32 v104, v111, v104, v240
	v_min_f32 v111, v111, v240
	s_waitcnt vmcnt(4)
	v_mfma_f32_16x16x32_f16 v[86:89], v[174:177], v[42:45], v[86:89]
	v_and_or_b32 v121, v80, v247, s71
	v_and_or_b32 v167, v81, v247, s72
	s_waitcnt lgkmcnt(0)
	v_mfma_f32_16x16x32_f16 v[78:81], v[96:99], v[38:41], v[90:93]
	s_waitcnt lgkmcnt(0)
	s_barrier
	v_mfma_f32_16x16x32_f16 v[90:93], v[96:99], v[70:73], v[90:93]
	v_and_or_b32 v105, v82, v247, s24
	v_and_or_b32 v168, v83, v247, s70
	v_med3_f32 v82, v104, v119, v241
	v_med3_f32 v83, v111, v104, v241
	v_min_f32 v104, v111, v241
	v_and_or_b32 v111, v84, v247, s71
	v_mfma_f32_16x16x32_f16 v[96:99], v[202:205], v[38:41], v[114:117]
	v_med3_f32 v170, v83, v82, v242
	v_med3_f32 v171, v104, v83, v242
	v_min_f32 v104, v104, v242
	v_mfma_f32_16x16x32_f16 v[114:117], v[202:205], v[70:73], v[114:117]
	v_and_or_b32 v119, v85, v247, s72
	v_and_or_b32 v169, v74, v247, s34
	v_mfma_f32_16x16x32_f16 v[78:81], v[178:181], v[34:37], v[78:81]
	v_mfma_f32_16x16x32_f16 v[82:85], v[178:181], v[66:69], v[90:93]
	v_and_b32_e32 v172, 0xfffffc00, v77
	v_and_or_b32 v173, v75, v247, s73
	v_and_or_b32 v174, v76, v247, s74
	v_mfma_f32_16x16x32_f16 v[74:77], v[206:209], v[34:37], v[96:99]
	v_med3_f32 v96, v161, v110, v243
	v_med3_f32 v97, v166, v161, v243
	v_min_f32 v98, v166, v243
	v_mfma_f32_16x16x32_f16 v[90:93], v[206:209], v[66:69], v[114:117]
	v_and_or_b32 v110, v86, v247, s34
	s_nop 0
	v_or3_b32 v99, s24, v172, 19
	v_and_or_b32 v114, v87, v247, s73
	v_mfma_f32_16x16x32_f16 v[78:81], v[182:185], v[30:33], v[78:81]
	v_med3_f32 v86, v97, v96, v244
	v_med3_f32 v87, v98, v97, v244
	v_min_f32 v96, v98, v244
	v_mfma_f32_16x16x32_f16 v[82:85], v[182:185], v[62:65], v[82:85]
	v_and_or_b32 v97, v88, v247, s74
	v_and_or_b32 v98, v89, v247, s75
	v_med3_f32 v115, v87, v86, v245
	v_mfma_f32_16x16x32_f16 v[74:77], v[210:213], v[30:33], v[74:77]
	v_med3_f32 v116, v96, v87, v245
	v_min_f32 v96, v96, v245
	v_mfma_f32_16x16x32_f16 v[86:89], v[210:213], v[62:65], v[90:93]
	v_med3_f32 v90, v116, v115, v246
	v_med3_f32 v91, v96, v116, v246
	v_min_f32 v92, v96, v246
	v_mfma_f32_16x16x32_f16 v[78:81], v[186:189], v[26:29], v[78:81]
	v_med3_f32 v93, v171, v170, v118
	v_med3_f32 v90, v91, v90, v105
	v_med3_f32 v91, v92, v91, v105
	v_mfma_f32_16x16x32_f16 v[82:85], v[186:189], v[58:61], v[82:85]
	v_min_f32 v92, v92, v105
	v_med3_f32 v96, v104, v171, v118
	v_med3_f32 v90, v91, v90, v168
	v_mfma_f32_16x16x32_f16 v[74:77], v[214:217], v[26:29], v[74:77]
	v_med3_f32 v93, v96, v93, v120
	v_med3_f32 v91, v92, v91, v168
	v_min_f32 v92, v92, v168
	v_mfma_f32_16x16x32_f16 v[86:89], v[214:217], v[58:61], v[86:89]
	v_min_f32 v104, v104, v118
	v_med3_f32 v90, v91, v90, v111
	v_med3_f32 v91, v92, v91, v111
	v_mfma_f32_16x16x32_f16 v[78:81], v[190:193], v[22:25], v[78:81]
	v_med3_f32 v96, v104, v96, v120
	v_min_f32 v92, v92, v111
	v_min_f32 v104, v104, v120
	v_mfma_f32_16x16x32_f16 v[82:85], v[190:193], v[54:57], v[82:85]
	v_med3_f32 v93, v96, v93, v121
	v_med3_f32 v96, v104, v96, v121
	v_med3_f32 v90, v91, v90, v119
	v_mfma_f32_16x16x32_f16 v[74:77], v[162:165], v[22:25], v[74:77]
	v_med3_f32 v93, v96, v93, v167
	v_med3_f32 v91, v92, v91, v119
	v_min_f32 v92, v92, v119
	v_mfma_f32_16x16x32_f16 v[86:89], v[162:165], v[54:57], v[86:89]
	v_min_f32 v104, v104, v121
	v_med3_f32 v90, v91, v90, v110
	v_med3_f32 v91, v92, v91, v110
	v_mfma_f32_16x16x32_f16 v[78:81], v[194:197], v[18:21], v[78:81]
	v_med3_f32 v96, v104, v96, v167
	v_min_f32 v92, v92, v110
	v_min_f32 v104, v104, v167
	v_mfma_f32_16x16x32_f16 v[82:85], v[194:197], v[50:53], v[82:85]
	v_med3_f32 v93, v96, v93, v169
	v_med3_f32 v96, v104, v96, v169
	v_med3_f32 v90, v91, v90, v114
	v_mfma_f32_16x16x32_f16 v[74:77], v[218:221], v[18:21], v[74:77]
	v_med3_f32 v93, v96, v93, v173
	v_med3_f32 v91, v92, v91, v114
	v_min_f32 v92, v92, v114
	v_mfma_f32_16x16x32_f16 v[86:89], v[218:221], v[50:53], v[86:89]
	v_min_f32 v104, v104, v169
	v_med3_f32 v90, v91, v90, v97
	v_med3_f32 v91, v92, v91, v97
	v_mfma_f32_16x16x32_f16 v[78:81], v[100:103], v[14:17], v[78:81]
	v_med3_f32 v96, v104, v96, v173
	v_min_f32 v92, v92, v97
	v_min_f32 v104, v104, v173
	v_mfma_f32_16x16x32_f16 v[82:85], v[100:103], v[46:49], v[82:85]
	v_med3_f32 v93, v96, v93, v174
	v_med3_f32 v96, v104, v96, v174
	v_med3_f32 v111, v91, v90, v98
	v_mfma_f32_16x16x32_f16 v[74:77], v[222:225], v[14:17], v[74:77]
	v_med3_f32 v105, v96, v93, v99
	v_med3_f32 v161, v92, v91, v98
	v_min_f32 v230, v92, v98
	v_mfma_f32_16x16x32_f16 v[86:89], v[222:225], v[46:49], v[86:89]
	v_min_f32 v104, v104, v174
	v_mfma_f32_16x16x32_f16 v[78:81], v[198:201], v[10:13], v[78:81]
	v_med3_f32 v110, v104, v96, v99
	v_min_f32 v104, v104, v99
	v_mfma_f32_16x16x32_f16 v[82:85], v[198:201], v[42:45], v[82:85]
	v_readfirstlane_b32 s6, v108
	v_lshl_add_u64 v[90:91], s[4:5], 0, v[122:123]
	v_lshl_add_u64 v[92:93], s[4:5], 0, v[106:107]
	s_add_i32 s4, s6, 0x400
	s_mov_b32 m0, s6
	s_nop 0
	global_load_lds_dwordx4 v[90:91], off
	s_add_u32 s6, s0, 0x10000
	s_mov_b32 m0, s4
	s_nop 0
	global_load_lds_dwordx4 v[92:93], off
	s_addc_u32 s7, s1, 0
	v_readfirstlane_b32 s5, v109
	v_lshl_add_u64 v[90:91], s[6:7], 0, v[122:123]
	s_mov_b32 m0, s5
	s_nop 0
	global_load_lds_dwordx4 v[90:91], off
	s_add_i32 s8, s5, 0x400
	v_mfma_f32_16x16x32_f16 v[74:77], v[226:229], v[10:13], v[74:77]
	s_sub_i32 s9, s23, 48
	s_or_b32 s76, s9, 1
	s_or_b32 s77, s9, 2
	s_or_b32 s78, s9, 3
	s_or_b32 s79, s9, 17
	s_or_b32 s80, s9, 18
	s_or_b32 s81, s9, 19
	s_sub_i32 s24, s23, 32
	s_or_b32 s70, s24, 1
	s_or_b32 s71, s24, 2
	s_or_b32 s72, s24, 3
	s_or_b32 s73, s24, 17
	s_or_b32 s74, s24, 18
	s_or_b32 s75, s24, 19
	s_add_i32 s4, s23, -16
	s_or_b32 s88, s4, 1
	s_or_b32 s89, s4, 2
	s_or_b32 s90, s4, 3
	s_or_b32 s91, s4, 17
	s_or_b32 s92, s4, 18
	s_or_b32 s93, s4, 19
	v_mfma_f32_16x16x32_f16 v[86:89], v[226:229], v[42:45], v[86:89]
	v_lshl_add_u64 v[92:93], s[6:7], 0, v[106:107]
	s_mov_b32 m0, s8
	s_nop 0
	global_load_lds_dwordx4 v[92:93], off
	ds_read_b128 v[90:93], v160
	ds_read_b128 v[114:117], v159
	v_add_u32_e32 v96, 0x18260, v95
	ds_read_b128 v[96:99], v96
	v_add_u32_e32 v118, 0x182a0, v95
	ds_read_b128 v[118:121], v118
	v_and_or_b32 v162, v78, v247, s9
	s_waitcnt lgkmcnt(1)
	v_mfma_f32_16x16x32_f16 v[100:103], v[90:93], v[38:41], v[96:99]
	v_med3_f32 v105, v110, v105, v162
	v_med3_f32 v110, v104, v110, v162
	v_min_f32 v104, v104, v162
	v_mfma_f32_16x16x32_f16 v[90:93], v[90:93], v[70:73], v[96:99]
	v_and_or_b32 v228, v81, v247, s78
	ds_read_b128 v[96:99], v158
	v_and_or_b32 v226, v79, v247, s76
	v_and_or_b32 v227, v80, v247, s77
	s_waitcnt lgkmcnt(1)
	v_mfma_f32_16x16x32_f16 v[78:81], v[114:117], v[38:41], v[118:121]
	ds_read_b128 v[166:169], v155 offset:256
	v_med3_f32 v105, v110, v105, v226
	v_med3_f32 v110, v104, v110, v226
	v_mfma_f32_16x16x32_f16 v[114:117], v[114:117], v[70:73], v[118:121]
	ds_read_b128 v[118:121], v157
	v_and_or_b32 v229, v82, v247, s9
	v_and_or_b32 v231, v83, v247, s76
	s_waitcnt lgkmcnt(2)
	v_mfma_f32_16x16x32_f16 v[100:103], v[96:99], v[34:37], v[100:103]
	ds_read_b128 v[162:165], v157 offset:256
	v_med3_f32 v105, v110, v105, v227
	v_min_f32 v104, v104, v226
	v_mfma_f32_16x16x32_f16 v[90:93], v[96:99], v[66:69], v[90:93]
	v_and_or_b32 v232, v84, v247, s77
	v_and_or_b32 v233, v85, v247, s78
	ds_read_b128 v[82:85], v156
	s_waitcnt lgkmcnt(2)
	v_mfma_f32_16x16x32_f16 v[96:99], v[118:121], v[66:69], v[114:117]
	v_med3_f32 v110, v104, v110, v227
	v_med3_f32 v111, v161, v111, v229
	ds_read_b128 v[170:173], v152
	v_mfma_f32_16x16x32_f16 v[78:81], v[118:121], v[34:37], v[78:81]
	v_and_or_b32 v234, v74, v247, s24
	ds_read_b128 v[114:117], v155
	v_and_or_b32 v235, v75, v247, s79
	v_and_or_b32 v236, v76, v247, s80
	s_waitcnt lgkmcnt(2)
	v_mfma_f32_16x16x32_f16 v[100:103], v[82:85], v[30:33], v[100:103]
	ds_read_b128 v[118:121], v154 offset:256
	v_min_f32 v104, v104, v227
	ds_read_b128 v[198:201], v151
	v_mfma_f32_16x16x32_f16 v[82:85], v[82:85], v[62:65], v[90:93]
	v_and_or_b32 v237, v77, v247, s81
	v_and_or_b32 v238, v86, v247, s24
	s_waitcnt lgkmcnt(2)
	v_mfma_f32_16x16x32_f16 v[74:77], v[114:117], v[30:33], v[78:81]
	ds_read_b128 v[174:177], v150
	ds_read_b128 v[202:205], v149
	ds_read_b128 v[178:181], v148
	ds_read_b128 v[78:81], v154
	v_mfma_f32_16x16x32_f16 v[90:93], v[114:117], v[62:65], v[96:99]
	v_and_or_b32 v239, v87, v247, s79
	v_and_or_b32 v240, v88, v247, s80
	v_and_or_b32 v241, v89, v247, s81
	s_waitcnt lgkmcnt(0)
	v_mfma_f32_16x16x32_f16 v[86:89], v[78:81], v[26:29], v[100:103]
	ds_read_b128 v[96:99], v160 offset:256
	ds_read_b128 v[114:117], v159 offset:256
	s_nop 0
	ds_read_b128 v[100:103], v156 offset:256
	v_mfma_f32_16x16x32_f16 v[78:81], v[78:81], v[58:61], v[82:85]
	ds_read_b128 v[206:209], v147
	ds_read_b128 v[182:185], v146
	ds_read_b128 v[186:189], v152 offset:256
	ds_read_b128 v[82:85], v153
	s_waitcnt lgkmcnt(0)
	v_mfma_f32_16x16x32_f16 v[74:77], v[82:85], v[26:29], v[74:77]
	ds_read_b128 v[210:213], v151 offset:256
	ds_read_b128 v[214:217], v149 offset:256
	ds_read_b128 v[190:193], v148 offset:256
	v_mfma_f32_16x16x32_f16 v[82:85], v[82:85], v[58:61], v[90:93]
	ds_read_b128 v[218:221], v147 offset:256
	ds_read_b128 v[194:197], v146 offset:256
	ds_read_b128 v[222:225], v145 offset:256
	ds_read_b128 v[90:93], v158 offset:256
	v_mfma_f32_16x16x32_f16 v[86:89], v[96:99], v[22:25], v[86:89]
	s_addk_i32 s3, 0x300
	v_mfma_f32_16x16x32_f16 v[78:81], v[96:99], v[54:57], v[78:81]
	ds_read_b128 v[96:99], v153 offset:256
	v_mfma_f32_16x16x32_f16 v[74:77], v[114:117], v[22:25], v[74:77]
	v_mfma_f32_16x16x32_f16 v[82:85], v[114:117], v[54:57], v[82:85]
	ds_read_b128 v[114:117], v150 offset:256
	s_waitcnt lgkmcnt(2)
	v_mfma_f32_16x16x32_f16 v[86:89], v[90:93], v[18:21], v[86:89]
	v_mfma_f32_16x16x32_f16 v[78:81], v[90:93], v[50:53], v[78:81]
	ds_read_b128 v[90:93], v145
	v_mfma_f32_16x16x32_f16 v[74:77], v[162:165], v[18:21], v[74:77]
	v_mfma_f32_16x16x32_f16 v[82:85], v[162:165], v[50:53], v[82:85]
	v_mfma_f32_16x16x32_f16 v[86:89], v[100:103], v[14:17], v[86:89]
	v_mfma_f32_16x16x32_f16 v[78:81], v[100:103], v[46:49], v[78:81]
	v_med3_f32 v100, v230, v161, v229
	v_min_f32 v101, v230, v229
	v_med3_f32 v102, v110, v105, v228
	v_med3_f32 v103, v104, v110, v228
	v_min_f32 v104, v104, v228
	s_nop 0
	v_med3_f32 v105, v100, v111, v231
	v_med3_f32 v100, v101, v100, v231
	v_min_f32 v101, v101, v231
	v_med3_f32 v161, v103, v102, v234
	v_med3_f32 v163, v104, v103, v234
	v_min_f32 v104, v104, v234
	s_nop 0
	v_med3_f32 v105, v100, v105, v232
	v_med3_f32 v110, v101, v100, v232
	v_add_u32_e32 v100, 0x182e0, v95
	v_add_u32_e32 v95, 0x18320, v95
	v_mfma_f32_16x16x32_f16 v[74:77], v[166:169], v[14:17], v[74:77]
	v_min_f32 v111, v101, v232
	ds_read_b128 v[100:103], v100
	v_med3_f32 v161, v163, v161, v235
	v_mfma_f32_16x16x32_f16 v[82:85], v[166:169], v[46:49], v[82:85]
	v_med3_f32 v105, v110, v105, v233
	v_med3_f32 v110, v111, v110, v233
	v_min_f32 v111, v111, v233
	v_mfma_f32_16x16x32_f16 v[86:89], v[118:121], v[10:13], v[86:89]
	v_med3_f32 v163, v104, v163, v235
	v_min_f32 v104, v104, v235
	v_mfma_f32_16x16x32_f16 v[78:81], v[118:121], v[42:45], v[78:81]
	v_med3_f32 v161, v163, v161, v236
	v_med3_f32 v163, v104, v163, v236
	s_nop 6
	v_and_or_b32 v162, v86, v247, s4
	v_and_or_b32 v164, v87, v247, s88
	s_waitcnt lgkmcnt(3)
	v_mfma_f32_16x16x32_f16 v[74:77], v[96:99], v[10:13], v[74:77]
	v_mfma_f32_16x16x32_f16 v[82:85], v[96:99], v[42:45], v[82:85]
	ds_read_b128 v[96:99], v95
	v_and_or_b32 v165, v88, v247, s89
	v_and_or_b32 v166, v89, v247, s90
	s_waitcnt lgkmcnt(1)
	v_mfma_f32_16x16x32_f16 v[86:89], v[170:173], v[38:41], v[100:103]
	s_waitcnt vmcnt(4)
	s_waitcnt lgkmcnt(0)
	s_barrier
	v_mfma_f32_16x16x32_f16 v[100:103], v[170:173], v[70:73], v[100:103]
	v_and_or_b32 v95, v78, v247, s4
	v_and_or_b32 v167, v79, v247, s88
	v_and_or_b32 v168, v80, v247, s89
	s_waitcnt lgkmcnt(0)
	v_mfma_f32_16x16x32_f16 v[118:121], v[198:201], v[38:41], v[96:99]
	v_mfma_f32_16x16x32_f16 v[96:99], v[198:201], v[70:73], v[96:99]
	v_and_or_b32 v169, v81, v247, s90
	v_and_or_b32 v170, v74, v247, s23
	v_mfma_f32_16x16x32_f16 v[78:81], v[174:177], v[34:37], v[86:89]
	v_mfma_f32_16x16x32_f16 v[86:89], v[174:177], v[66:69], v[100:103]
	v_min_f32 v103, v104, v236
	v_med3_f32 v104, v163, v161, v237
	s_nop 1
	v_and_or_b32 v101, v75, v247, s91
	v_and_or_b32 v102, v76, v247, s92
	v_and_or_b32 v100, v77, v247, s93
	v_mfma_f32_16x16x32_f16 v[74:77], v[202:205], v[34:37], v[118:121]
	v_med3_f32 v118, v103, v163, v237
	v_min_f32 v103, v103, v237
	v_mfma_f32_16x16x32_f16 v[96:99], v[202:205], v[66:69], v[96:99]
	v_and_or_b32 v119, v82, v247, s23
	v_and_or_b32 v120, v83, v247, s91
	v_med3_f32 v82, v110, v105, v238
	v_med3_f32 v83, v111, v110, v238
	v_mfma_f32_16x16x32_f16 v[78:81], v[178:181], v[30:33], v[78:81]
	v_min_f32 v110, v111, v238
	v_med3_f32 v111, v83, v82, v239
	s_addk_i32 s23, 0xc0
	v_mfma_f32_16x16x32_f16 v[86:89], v[178:181], v[62:65], v[86:89]
	v_and_or_b32 v105, v84, v247, s92
	v_and_or_b32 v121, v85, v247, s93
	v_med3_f32 v161, v110, v83, v239
	v_mfma_f32_16x16x32_f16 v[74:77], v[206:209], v[30:33], v[74:77]
	s_add_u32 s0, s0, 0x18000
	s_addc_u32 s1, s1, 0
	s_add_i32 s33, s33, 6
	v_mfma_f32_16x16x32_f16 v[82:85], v[206:209], v[62:65], v[96:99]
	v_min_f32 v96, v110, v239
	v_med3_f32 v97, v161, v111, v240
	v_med3_f32 v99, v118, v104, v162
	v_mfma_f32_16x16x32_f16 v[78:81], v[182:185], v[26:29], v[78:81]
	v_med3_f32 v98, v96, v161, v240
	v_min_f32 v96, v96, v240
	v_med3_f32 v104, v103, v118, v162
	v_mfma_f32_16x16x32_f16 v[86:89], v[182:185], v[58:61], v[86:89]
	v_med3_f32 v97, v98, v97, v241
	v_med3_f32 v98, v96, v98, v241
	v_min_f32 v96, v96, v241
	v_mfma_f32_16x16x32_f16 v[74:77], v[90:93], v[26:29], v[74:77]
	s_cmpk_eq_i32 s3, 0xf00
	v_mfma_f32_16x16x32_f16 v[82:85], v[90:93], v[58:61], v[82:85]
	v_min_f32 v90, v103, v162
	v_med3_f32 v91, v104, v99, v164
	v_med3_f32 v93, v98, v97, v95
	v_mfma_f32_16x16x32_f16 v[78:81], v[186:189], v[22:25], v[78:81]
	v_med3_f32 v92, v90, v104, v164
	v_min_f32 v90, v90, v164
	v_med3_f32 v97, v96, v98, v95
	v_mfma_f32_16x16x32_f16 v[86:89], v[186:189], v[54:57], v[86:89]
	v_med3_f32 v91, v92, v91, v165
	v_med3_f32 v92, v90, v92, v165
	v_min_f32 v90, v90, v165
	v_mfma_f32_16x16x32_f16 v[74:77], v[210:213], v[22:25], v[74:77]
	v_min_f32 v95, v96, v95
	v_med3_f32 v91, v92, v91, v166
	v_med3_f32 v93, v97, v93, v167
	v_mfma_f32_16x16x32_f16 v[82:85], v[210:213], v[54:57], v[82:85]
	v_med3_f32 v96, v95, v97, v167
	v_med3_f32 v92, v90, v92, v166
	v_min_f32 v90, v90, v166
	v_mfma_f32_16x16x32_f16 v[78:81], v[114:117], v[18:21], v[78:81]
	v_min_f32 v95, v95, v167
	v_med3_f32 v93, v96, v93, v168
	v_med3_f32 v91, v92, v91, v170
	v_mfma_f32_16x16x32_f16 v[86:89], v[114:117], v[50:53], v[86:89]
	v_med3_f32 v96, v95, v96, v168
	v_min_f32 v95, v95, v168
	v_med3_f32 v92, v90, v92, v170
	v_mfma_f32_16x16x32_f16 v[74:77], v[214:217], v[18:21], v[74:77]
	v_med3_f32 v97, v96, v93, v169
	v_med3_f32 v96, v95, v96, v169
	v_min_f32 v90, v90, v170
	v_mfma_f32_16x16x32_f16 v[82:85], v[214:217], v[50:53], v[82:85]
	v_med3_f32 v91, v92, v91, v101
	v_med3_f32 v98, v90, v92, v101
	v_min_f32 v99, v90, v101
	v_min_f32 v95, v95, v169
	v_mfma_f32_16x16x32_f16 v[78:81], v[190:193], v[14:17], v[78:81]
	v_med3_f32 v101, v98, v91, v102
	v_med3_f32 v103, v95, v96, v119
	v_min_f32 v95, v95, v119
	v_mfma_f32_16x16x32_f16 v[90:93], v[190:193], v[46:49], v[86:89]
	v_med3_f32 v86, v99, v98, v102
	v_min_f32 v87, v99, v102
	v_med3_f32 v102, v96, v97, v119
	v_mfma_f32_16x16x32_f16 v[74:77], v[218:221], v[14:17], v[74:77]
	v_med3_f32 v111, v86, v101, v100
	v_med3_f32 v101, v87, v86, v100
	v_min_f32 v110, v87, v100
	v_mfma_f32_16x16x32_f16 v[96:99], v[218:221], v[46:49], v[82:85]
	v_med3_f32 v100, v103, v102, v120
	v_med3_f32 v102, v95, v103, v120
	v_min_f32 v95, v95, v120
	v_mfma_f32_16x16x32_f16 v[86:89], v[194:197], v[10:13], v[78:81]
	v_mfma_f32_16x16x32_f16 v[82:85], v[194:197], v[42:45], v[90:93]
	v_med3_f32 v90, v102, v100, v105
	v_med3_f32 v91, v95, v102, v105
	v_min_f32 v92, v95, v105
	v_mfma_f32_16x16x32_f16 v[78:81], v[222:225], v[10:13], v[74:77]
	v_med3_f32 v100, v92, v91, v121
	v_mfma_f32_16x16x32_f16 v[74:77], v[222:225], v[42:45], v[96:99]
	v_med3_f32 v98, v91, v90, v121
	v_min_f32 v99, v92, v121
	s_cbranch_scc0 .LBB1_7
	s_add_u32 s0, s26, 0x88000
	v_readfirstlane_b32 s3, v112
	v_and_b32_e32 v90, 16, v0
	s_addc_u32 s1, s27, 0
	s_add_i32 s6, s3, 0x10000
	v_mov_b32_e32 v123, 0
	v_cmp_eq_u32_e64 s[4:5], 0, v90
	v_lshl_add_u64 v[90:91], s[0:1], 0, v[122:123]
	s_mov_b32 m0, s6
	s_nop 0
	global_load_lds_dwordx4 v[90:91], off
	s_add_i32 s6, s3, 0x10400
	v_mov_b32_e32 v107, v123
	v_lshl_add_u64 v[90:91], s[0:1], 0, v[106:107]
	s_add_u32 s0, s26, 0x8c000
	s_mov_b32 m0, s6
	s_nop 0
	global_load_lds_dwordx4 v[90:91], off
	s_addc_u32 s1, s27, 0
	s_add_i32 s6, s3, 0x14000
	v_lshl_add_u64 v[90:91], s[0:1], 0, v[122:123]
	s_mov_b32 m0, s6
	s_nop 0
	global_load_lds_dwordx4 v[90:91], off
	s_add_i32 s3, s3, 0x14400
	v_lshl_add_u64 v[90:91], s[0:1], 0, v[106:107]
	s_mov_b32 m0, s3
	s_nop 0
	global_load_lds_dwordx4 v[90:91], off
	ds_read_b128 v[90:93], v144
	ds_read_b128 v[114:117], v144 offset:8192
	v_add_u32_e32 v161, 0x18060, v94
	ds_read_b128 v[94:97], v161 offset:3840
	ds_read_b128 v[118:121], v161 offset:3904
	ds_read_b128 v[162:165], v143
	s_waitcnt lgkmcnt(2)
	v_mfma_f32_16x16x32_f16 v[102:105], v[90:93], v[38:41], v[94:97]
	ds_read_b128 v[166:169], v142
	ds_read_b128 v[174:177], v142 offset:8192
	ds_read_b128 v[178:181], v144 offset:24576
	v_mfma_f32_16x16x32_f16 v[90:93], v[90:93], v[70:73], v[94:97]
	ds_read_b128 v[182:185], v161 offset:4032
	ds_read_b128 v[186:189], v143 offset:16384
	s_add_u32 s0, s26, 0x90000
	s_waitcnt lgkmcnt(6)
	v_mfma_f32_16x16x32_f16 v[94:97], v[114:117], v[38:41], v[118:121]
	s_addc_u32 s1, s27, 0
	v_cmp_gt_u32_e64 s[6:7], 32, v131
	v_mfma_f32_16x16x32_f16 v[114:117], v[114:117], v[70:73], v[118:121]
	s_nop 2
	ds_read_b128 v[118:121], v143 offset:8192
	s_waitcnt lgkmcnt(6)
	v_mfma_f32_16x16x32_f16 v[102:105], v[162:165], v[34:37], v[102:105]
	v_mfma_f32_16x16x32_f16 v[162:165], v[162:165], v[66:69], v[90:93]
	s_waitcnt lgkmcnt(0)
	v_mfma_f32_16x16x32_f16 v[92:95], v[118:121], v[34:37], v[94:97]
	v_mfma_f32_16x16x32_f16 v[170:173], v[118:121], v[66:69], v[114:117]
	v_and_b32_e32 v78, 0xfffffc00, v78
	v_or_b32_e32 v90, 0x3b0, v78
	v_and_b32_e32 v78, 0xfffffc00, v79
	v_or_b32_e32 v91, 0x3b1, v78
	v_mfma_f32_16x16x32_f16 v[102:105], v[166:169], v[30:33], v[102:105]
	v_mfma_f32_16x16x32_f16 v[162:165], v[166:169], v[62:65], v[162:165]
	v_and_b32_e32 v78, 0xfffffc00, v80
	v_or_b32_e32 v118, 0x3b2, v78
	v_and_b32_e32 v78, 0xfffffc00, v81
	v_or_b32_e32 v115, 0x3b3, v78
	v_and_b32_e32 v74, 0xfffffc00, v74
	v_mfma_f32_16x16x32_f16 v[78:81], v[174:177], v[30:33], v[92:95]
	s_nop 2
	ds_read_b128 v[92:95], v141
	v_mfma_f32_16x16x32_f16 v[166:169], v[174:177], v[62:65], v[170:173]
	v_or_b32_e32 v114, 0x3b0, v74
	v_and_b32_e32 v74, 0xfffffc00, v75
	v_or_b32_e32 v116, 0x3b1, v74
	v_and_b32_e32 v74, 0xfffffc00, v76
	v_or_b32_e32 v117, 0x3b2, v74
	v_and_b32_e32 v96, 0xfffffc00, v77
	v_or_b32_e32 v119, 0x3b3, v96
	s_waitcnt lgkmcnt(0)
	v_mfma_f32_16x16x32_f16 v[74:77], v[92:95], v[26:29], v[102:105]
	ds_read_b128 v[170:173], v144 offset:16384
	ds_read_b128 v[174:177], v161 offset:3968
	v_mfma_f32_16x16x32_f16 v[92:95], v[92:95], v[58:61], v[162:165]
	ds_read_b128 v[102:105], v141 offset:8192
	s_nop 1
	ds_read_b128 v[162:165], v144 offset:256
	s_waitcnt lgkmcnt(1)
	v_mfma_f32_16x16x32_f16 v[78:81], v[102:105], v[26:29], v[78:81]
	v_mfma_f32_16x16x32_f16 v[102:105], v[102:105], v[58:61], v[166:169]
	s_waitcnt lgkmcnt(0)
	v_mfma_f32_16x16x32_f16 v[74:77], v[162:165], v[22:25], v[74:77]
	s_nop 0
	ds_read_b128 v[166:169], v141 offset:8448
	v_mfma_f32_16x16x32_f16 v[92:95], v[162:165], v[54:57], v[92:95]
	ds_read_b128 v[162:165], v144 offset:8448
	s_waitcnt lgkmcnt(0)
	v_mfma_f32_16x16x32_f16 v[78:81], v[162:165], v[22:25], v[78:81]
	v_mfma_f32_16x16x32_f16 v[102:105], v[162:165], v[54:57], v[102:105]
	ds_read_b128 v[162:165], v143 offset:256
	s_waitcnt lgkmcnt(0)
	v_mfma_f32_16x16x32_f16 v[74:77], v[162:165], v[18:21], v[74:77]
	v_mfma_f32_16x16x32_f16 v[92:95], v[162:165], v[50:53], v[92:95]
	ds_read_b128 v[162:165], v143 offset:8448
	s_waitcnt lgkmcnt(0)
	v_mfma_f32_16x16x32_f16 v[78:81], v[162:165], v[18:21], v[78:81]
	v_mfma_f32_16x16x32_f16 v[102:105], v[162:165], v[50:53], v[102:105]
	ds_read_b128 v[162:165], v142 offset:256
	s_waitcnt lgkmcnt(0)
	v_mfma_f32_16x16x32_f16 v[74:77], v[162:165], v[14:17], v[74:77]
	v_mfma_f32_16x16x32_f16 v[92:95], v[162:165], v[46:49], v[92:95]
	ds_read_b128 v[162:165], v142 offset:8448
	s_waitcnt lgkmcnt(0)
	v_mfma_f32_16x16x32_f16 v[78:81], v[162:165], v[14:17], v[78:81]
	v_mfma_f32_16x16x32_f16 v[102:105], v[162:165], v[46:49], v[102:105]
	ds_read_b128 v[162:165], v141 offset:256
	s_waitcnt lgkmcnt(0)
	v_mfma_f32_16x16x32_f16 v[74:77], v[162:165], v[10:13], v[74:77]
	v_mfma_f32_16x16x32_f16 v[92:95], v[162:165], v[42:45], v[92:95]
	s_nop 6
	v_and_b32_e32 v74, 0xfffffc00, v74
	v_or_b32_e32 v120, 0x3c0, v74
	v_and_b32_e32 v74, 0xfffffc00, v75
	v_or_b32_e32 v121, 0x3c1, v74
	v_and_b32_e32 v74, 0xfffffc00, v76
	v_mfma_f32_16x16x32_f16 v[78:81], v[166:169], v[10:13], v[78:81]
	v_mfma_f32_16x16x32_f16 v[102:105], v[166:169], v[42:45], v[102:105]
	v_or_b32_e32 v162, 0x3c2, v74
	v_and_b32_e32 v74, 0xfffffc00, v77
	v_or_b32_e32 v163, 0x3c3, v74
	v_and_b32_e32 v74, 0xfffffc00, v92
	v_or_b32_e32 v166, 0x3c0, v74
	v_mfma_f32_16x16x32_f16 v[74:77], v[170:173], v[38:41], v[174:177]
	v_mfma_f32_16x16x32_f16 v[174:177], v[170:173], v[70:73], v[174:177]
	v_and_b32_e32 v92, 0xfffffc00, v93
	v_or_b32_e32 v168, 0x3c1, v92
	v_and_b32_e32 v92, 0xfffffc00, v94
	v_or_b32_e32 v169, 0x3c2, v92
	v_and_b32_e32 v96, 0xfffffc00, v95
	v_mfma_f32_16x16x32_f16 v[92:95], v[178:181], v[38:41], v[182:185]
	v_mfma_f32_16x16x32_f16 v[178:181], v[178:181], v[70:73], v[182:185]
	v_and_b32_e32 v78, 0xfffffc00, v78
	v_or_b32_e32 v171, 0x3d0, v78
	v_and_b32_e32 v78, 0xfffffc00, v79
	ds_read_b128 v[182:185], v143 offset:24576
	v_or_b32_e32 v170, 0x3c3, v96
	v_or_b32_e32 v172, 0x3d1, v78
	v_mfma_f32_16x16x32_f16 v[74:77], v[186:189], v[34:37], v[74:77]
	v_mfma_f32_16x16x32_f16 v[174:177], v[186:189], v[66:69], v[174:177]
	v_and_b32_e32 v78, 0xfffffc00, v80
	v_or_b32_e32 v173, 0x3d2, v78
	v_and_b32_e32 v78, 0xfffffc00, v81
	v_or_b32_e32 v198, 0x3d3, v78
	v_and_b32_e32 v96, 0xfffffc00, v102
	s_waitcnt lgkmcnt(0)
	v_mfma_f32_16x16x32_f16 v[78:81], v[182:185], v[34:37], v[92:95]
	ds_read_b128 v[186:189], v141 offset:24832
	s_nop 1
	ds_read_b128 v[92:95], v142 offset:16384
	v_mfma_f32_16x16x32_f16 v[178:181], v[182:185], v[66:69], v[178:181]
	v_or_b32_e32 v164, 0x3d0, v96
	v_and_b32_e32 v96, 0xfffffc00, v103
	v_or_b32_e32 v161, 0x3d1, v96
	v_and_b32_e32 v96, 0xfffffc00, v104
	v_or_b32_e32 v165, 0x3d2, v96
	s_waitcnt lgkmcnt(0)
	v_mfma_f32_16x16x32_f16 v[74:77], v[92:95], v[30:33], v[74:77]
	ds_read_b128 v[182:185], v141 offset:16640
	v_mfma_f32_16x16x32_f16 v[92:95], v[92:95], v[62:65], v[174:177]
	v_and_b32_e32 v96, 0xfffffc00, v105
	s_nop 1
	ds_read_b128 v[174:177], v142 offset:24576
	s_waitcnt lgkmcnt(0)
	v_mfma_f32_16x16x32_f16 v[78:81], v[174:177], v[30:33], v[78:81]
	v_mfma_f32_16x16x32_f16 v[102:105], v[174:177], v[62:65], v[178:181]
	ds_read_b128 v[174:177], v141 offset:16384
	s_waitcnt lgkmcnt(0)
	v_mfma_f32_16x16x32_f16 v[74:77], v[174:177], v[26:29], v[74:77]
	ds_read_b128 v[178:181], v142 offset:24832
	v_mfma_f32_16x16x32_f16 v[92:95], v[174:177], v[58:61], v[92:95]
	ds_read_b128 v[174:177], v141 offset:24576
	s_waitcnt lgkmcnt(0)
	v_mfma_f32_16x16x32_f16 v[78:81], v[174:177], v[26:29], v[78:81]
	v_mfma_f32_16x16x32_f16 v[102:105], v[174:177], v[58:61], v[102:105]
	ds_read_b128 v[174:177], v144 offset:16640
	s_waitcnt lgkmcnt(0)
	v_mfma_f32_16x16x32_f16 v[74:77], v[174:177], v[22:25], v[74:77]
	v_mfma_f32_16x16x32_f16 v[92:95], v[174:177], v[54:57], v[92:95]
	ds_read_b128 v[174:177], v144 offset:24832
	s_waitcnt lgkmcnt(0)
	v_mfma_f32_16x16x32_f16 v[78:81], v[174:177], v[22:25], v[78:81]
	v_mfma_f32_16x16x32_f16 v[102:105], v[174:177], v[54:57], v[102:105]
	ds_read_b128 v[174:177], v143 offset:16640
	s_waitcnt lgkmcnt(0)
	v_mfma_f32_16x16x32_f16 v[74:77], v[174:177], v[18:21], v[74:77]
	v_mfma_f32_16x16x32_f16 v[92:95], v[174:177], v[50:53], v[92:95]
	ds_read_b128 v[174:177], v143 offset:24832
	s_waitcnt lgkmcnt(0)
	v_mfma_f32_16x16x32_f16 v[78:81], v[174:177], v[18:21], v[78:81]
	v_mfma_f32_16x16x32_f16 v[78:81], v[178:181], v[14:17], v[78:81]
	v_mfma_f32_16x16x32_f16 v[78:81], v[186:189], v[10:13], v[78:81]
	v_mfma_f32_16x16x32_f16 v[102:105], v[174:177], v[50:53], v[102:105]
	ds_read_b128 v[174:177], v142 offset:16640
	s_waitcnt vmcnt(4)
	s_waitcnt lgkmcnt(0)
	s_waitcnt lgkmcnt(0)
	v_mfma_f32_16x16x32_f16 v[74:77], v[174:177], v[14:17], v[74:77]
	s_barrier
	s_nop 2
	v_and_b32_e32 v78, 0xfffffc00, v78
	v_or_b32_e32 v78, 0x3f0, v78
	v_mfma_f32_16x16x32_f16 v[92:95], v[174:177], v[46:49], v[92:95]
	v_and_b32_e32 v79, 0xfffffc00, v79
	v_or_b32_e32 v79, 0x3f1, v79
	v_mfma_f32_16x16x32_f16 v[174:177], v[178:181], v[46:49], v[102:105]
	v_mfma_f32_16x16x32_f16 v[102:105], v[182:185], v[10:13], v[74:77]
	v_or_b32_e32 v167, 0x3d3, v96
	v_readfirstlane_b32 s3, v112
	v_lshl_add_u64 v[96:97], s[0:1], 0, v[122:123]
	s_mov_b32 m0, s3
	s_nop 0
	global_load_lds_dwordx4 v[96:97], off
	s_addk_i32 s3, 0x400
	v_lshl_add_u64 v[96:97], s[0:1], 0, v[106:107]
	s_add_u32 s0, s26, 0x94000
	s_mov_b32 m0, s3
	s_nop 0
	global_load_lds_dwordx4 v[96:97], off
	s_addc_u32 s1, s27, 0
	v_readfirstlane_b32 s3, v113
	v_lshl_add_u64 v[74:75], s[0:1], 0, v[122:123]
	s_mov_b32 m0, s3
	s_nop 0
	global_load_lds_dwordx4 v[74:75], off
	s_addk_i32 s3, 0x400
	v_lshl_add_u64 v[74:75], s[0:1], 0, v[106:107]
	s_mov_b32 m0, s3
	s_nop 0
	global_load_lds_dwordx4 v[74:75], off
	v_mfma_f32_16x16x32_f16 v[74:77], v[186:189], v[42:45], v[174:177]
	ds_read_b128 v[190:193], v143 offset:32768
	ds_read_b128 v[194:197], v144 offset:41216
	s_add_u32 s0, s26, 0x98000
	ds_read_b128 v[174:177], v144 offset:32768
	v_mfma_f32_16x16x32_f16 v[94:97], v[182:185], v[42:45], v[92:95]
	ds_read_b128 v[182:185], v144 offset:40960
	v_and_b32_e32 v86, 0xfffffc00, v86
	v_or_b32_e32 v86, 0x3a0, v86
	s_waitcnt lgkmcnt(1)
	v_mfma_f32_16x16x32_f16 v[178:181], v[174:177], v[38:41], 0
	v_med3_f32 v92, v101, v111, v86
	v_med3_f32 v93, v110, v101, v86
	v_min_f32 v86, v110, v86
	v_mfma_f32_16x16x32_f16 v[174:177], v[174:177], v[70:73], 0
	ds_read_b128 v[110:113], v143 offset:33024
	v_and_b32_e32 v87, 0xfffffc00, v87
	v_or_b32_e32 v87, 0x3a1, v87
	v_mfma_f32_16x16x32_f16 v[178:181], v[190:193], v[34:37], v[178:181]
	v_and_b32_e32 v88, 0xfffffc00, v88
	v_and_b32_e32 v89, 0xfffffc00, v89
	v_and_b32_e32 v82, 0xfffffc00, v82
	v_mfma_f32_16x16x32_f16 v[174:177], v[190:193], v[66:69], v[174:177]
	ds_read_b128 v[190:193], v143 offset:40960
	v_or_b32_e32 v88, 0x3a2, v88
	v_or_b32_e32 v89, 0x3a3, v89
	s_waitcnt lgkmcnt(2)
	v_mfma_f32_16x16x32_f16 v[186:189], v[182:185], v[38:41], 0
	v_or_b32_e32 v82, 0x3a0, v82
	v_and_b32_e32 v83, 0xfffffc00, v83
	v_med3_f32 v98, v100, v98, v82
	v_mfma_f32_16x16x32_f16 v[182:185], v[182:185], v[70:73], 0
	v_or_b32_e32 v83, 0x3a1, v83
	v_med3_f32 v92, v93, v92, v87
	v_med3_f32 v93, v86, v93, v87
	s_waitcnt lgkmcnt(0)
	v_mfma_f32_16x16x32_f16 v[186:189], v[190:193], v[34:37], v[186:189]
	v_min_f32 v86, v86, v87
	v_med3_f32 v87, v93, v92, v88
	v_and_b32_e32 v84, 0xfffffc00, v84
	v_mfma_f32_16x16x32_f16 v[182:185], v[190:193], v[66:69], v[182:185]
	ds_read_b128 v[190:193], v142 offset:32768
	v_med3_f32 v92, v86, v93, v88
	v_min_f32 v86, v86, v88
	s_waitcnt lgkmcnt(0)
	v_mfma_f32_16x16x32_f16 v[178:181], v[190:193], v[30:33], v[178:181]
	v_med3_f32 v93, v92, v87, v89
	v_med3_f32 v92, v86, v92, v89
	v_and_b32_e32 v85, 0xfffffc00, v85
	v_mfma_f32_16x16x32_f16 v[174:177], v[190:193], v[62:65], v[174:177]
	ds_read_b128 v[190:193], v142 offset:40960
	v_or_b32_e32 v84, 0x3a2, v84
	v_or_b32_e32 v85, 0x3a3, v85
	s_waitcnt lgkmcnt(0)
	v_mfma_f32_16x16x32_f16 v[186:189], v[190:193], v[30:33], v[186:189]
	s_addc_u32 s1, s27, 0
	v_and_b32_e32 v102, 0xfffffc00, v102
	v_or_b32_e32 v102, 0x3e0, v102
	v_mfma_f32_16x16x32_f16 v[182:185], v[190:193], v[62:65], v[182:185]
	ds_read_b128 v[190:193], v141 offset:32768
	v_and_b32_e32 v103, 0xfffffc00, v103
	v_or_b32_e32 v103, 0x3e1, v103
	s_waitcnt lgkmcnt(0)
	v_mfma_f32_16x16x32_f16 v[178:181], v[190:193], v[26:29], v[178:181]
	v_and_b32_e32 v94, 0xfffffc00, v94
	v_or_b32_e32 v94, 0x3e0, v94
	v_and_b32_e32 v95, 0xfffffc00, v95
	v_mfma_f32_16x16x32_f16 v[174:177], v[190:193], v[58:61], v[174:177]
	ds_read_b128 v[190:193], v141 offset:40960
	v_or_b32_e32 v95, 0x3e1, v95
	v_and_b32_e32 v74, 0xfffffc00, v74
	s_waitcnt lgkmcnt(0)
	v_mfma_f32_16x16x32_f16 v[186:189], v[190:193], v[26:29], v[186:189]
	v_or_b32_e32 v74, 0x3f0, v74
	v_and_b32_e32 v75, 0xfffffc00, v75
	v_or_b32_e32 v75, 0x3f1, v75
	v_mfma_f32_16x16x32_f16 v[182:185], v[190:193], v[58:61], v[182:185]
	ds_read_b128 v[190:193], v144 offset:33024
	s_waitcnt lgkmcnt(0)
	v_mfma_f32_16x16x32_f16 v[178:181], v[190:193], v[22:25], v[178:181]
	v_mfma_f32_16x16x32_f16 v[174:177], v[190:193], v[54:57], v[174:177]
	ds_read_b128 v[190:193], v143 offset:41216
	v_mfma_f32_16x16x32_f16 v[186:189], v[194:197], v[22:25], v[186:189]
	v_mfma_f32_16x16x32_f16 v[182:185], v[194:197], v[54:57], v[182:185]
	v_min_f32 v194, v86, v89
	ds_read_b128 v[86:89], v142 offset:33024
	v_mfma_f32_16x16x32_f16 v[178:181], v[110:113], v[18:21], v[178:181]
	v_mfma_f32_16x16x32_f16 v[110:113], v[110:113], v[50:53], v[174:177]
	s_waitcnt lgkmcnt(1)
	v_mfma_f32_16x16x32_f16 v[174:177], v[190:193], v[18:21], v[186:189]
	v_med3_f32 v186, v99, v100, v82
	v_min_f32 v82, v99, v82
	s_nop 0
	v_med3_f32 v187, v186, v98, v83
	v_mfma_f32_16x16x32_f16 v[98:101], v[190:193], v[50:53], v[182:185]
	v_med3_f32 v186, v82, v186, v83
	v_min_f32 v82, v82, v83
	s_nop 0
	v_med3_f32 v83, v186, v187, v84
	v_med3_f32 v186, v82, v186, v84
	s_nop 1
	ds_read_b128 v[182:185], v142 offset:41216
	v_min_f32 v82, v82, v84
	v_med3_f32 v190, v186, v83, v85
	s_waitcnt lgkmcnt(0)
	v_mfma_f32_16x16x32_f16 v[174:177], v[182:185], v[14:17], v[174:177]
	v_med3_f32 v191, v82, v186, v85
	ds_read_b128 v[186:189], v141 offset:33024
	v_min_f32 v192, v82, v85
	v_mfma_f32_16x16x32_f16 v[82:85], v[182:185], v[46:49], v[98:101]
	ds_read_b128 v[182:185], v141 offset:41216
	v_mfma_f32_16x16x32_f16 v[178:181], v[86:89], v[14:17], v[178:181]
	v_mfma_f32_16x16x32_f16 v[110:113], v[86:89], v[46:49], v[110:113]
	v_med3_f32 v86, v92, v93, v90
	v_med3_f32 v92, v194, v92, v90
	v_min_f32 v90, v194, v90
	s_waitcnt lgkmcnt(0)
	v_mfma_f32_16x16x32_f16 v[82:85], v[182:185], v[42:45], v[82:85]
	v_med3_f32 v93, v92, v86, v91
	v_med3_f32 v98, v90, v92, v91
	v_min_f32 v99, v90, v91
	v_mfma_f32_16x16x32_f16 v[86:89], v[186:189], v[10:13], v[178:181]
	v_med3_f32 v178, v98, v93, v118
	v_med3_f32 v179, v99, v98, v118
	v_min_f32 v118, v99, v118
	v_mfma_f32_16x16x32_f16 v[90:93], v[186:189], v[42:45], v[110:113]
	v_med3_f32 v193, v179, v178, v115
	v_med3_f32 v194, v118, v179, v115
	v_min_f32 v118, v118, v115
	v_mfma_f32_16x16x32_f16 v[98:101], v[182:185], v[10:13], v[174:177]
	v_med3_f32 v115, v191, v190, v114
	s_nop 2
	ds_read_b128 v[110:113], v143 offset:49152
	v_med3_f32 v182, v192, v191, v114
	v_min_f32 v114, v192, v114
	s_waitcnt lgkmcnt(0)
	v_mfma_f32_16x16x32_f16 v[178:181], v[110:113], v[34:37], 0
	ds_read_b128 v[174:177], v143 offset:57344
	v_med3_f32 v115, v182, v115, v116
	v_med3_f32 v190, v114, v182, v116
	ds_read_b128 v[182:185], v142 offset:49152
	v_min_f32 v114, v114, v116
	v_med3_f32 v115, v190, v115, v117
	v_mfma_f32_16x16x32_f16 v[110:113], v[110:113], v[66:69], 0
	v_med3_f32 v190, v114, v190, v117
	v_min_f32 v191, v114, v117
	v_fma_mix_f32 v86, v86, v38, 0 op_sel_hi:[0,1,0]
	s_waitcnt lgkmcnt(1)
	v_mfma_f32_16x16x32_f16 v[186:189], v[174:177], v[34:37], 0
	v_med3_f32 v192, v190, v115, v119
	v_med3_f32 v190, v191, v190, v119
	v_min_f32 v191, v191, v119
	v_mfma_f32_16x16x32_f16 v[114:117], v[174:177], v[66:69], 0
	ds_read_b128 v[174:177], v142 offset:57344
	v_med3_f32 v119, v194, v193, v120
	v_med3_f32 v193, v118, v194, v120
	v_min_f32 v118, v118, v120
	s_waitcnt lgkmcnt(1)
	v_mfma_f32_16x16x32_f16 v[178:181], v[182:185], v[30:33], v[178:181]
	v_med3_f32 v119, v193, v119, v121
	v_med3_f32 v120, v118, v193, v121
	v_min_f32 v118, v118, v121
	v_mfma_f32_16x16x32_f16 v[110:113], v[182:185], v[62:65], v[110:113]
	v_med3_f32 v119, v120, v119, v162
	ds_read_b128 v[182:185], v141 offset:49152
	v_med3_f32 v193, v118, v120, v162
	v_min_f32 v162, v118, v162
	s_waitcnt lgkmcnt(1)
	v_mfma_f32_16x16x32_f16 v[186:189], v[174:177], v[30:33], v[186:189]
	v_med3_f32 v194, v193, v119, v163
	ds_read_b128 v[118:121], v141 offset:57344
	v_med3_f32 v193, v162, v193, v163
	v_mfma_f32_16x16x32_f16 v[114:117], v[174:177], v[62:65], v[114:117]
	v_min_f32 v162, v162, v163
	v_med3_f32 v163, v190, v192, v166
	v_med3_f32 v190, v191, v190, v166
	s_waitcnt lgkmcnt(1)
	v_mfma_f32_16x16x32_f16 v[174:177], v[182:185], v[26:29], v[178:181]
	v_min_f32 v166, v191, v166
	v_med3_f32 v163, v190, v163, v168
	v_fma_mix_f32 v38, v87, v38, v86 op_sel:[0,1,0] op_sel_hi:[0,1,0]
	v_mfma_f32_16x16x32_f16 v[110:113], v[182:185], v[58:61], v[110:113]
	v_fma_mix_f32 v90, v90, v70, 0 op_sel_hi:[0,1,0]
	ds_read_b128 v[178:181], v144 offset:49408
	v_fma_mix_f32 v38, v88, v39, v38 op_sel_hi:[0,1,0]
	s_waitcnt lgkmcnt(1)
	v_mfma_f32_16x16x32_f16 v[182:185], v[118:121], v[26:29], v[186:189]
	v_med3_f32 v186, v166, v190, v168
	v_min_f32 v166, v166, v168
	v_fma_mix_f32 v70, v91, v70, v90 op_sel:[0,1,0] op_sel_hi:[0,1,0]
	v_mfma_f32_16x16x32_f16 v[114:117], v[118:121], v[58:61], v[114:117]
	ds_read_b128 v[118:121], v144 offset:57600
	v_med3_f32 v163, v186, v163, v169
	v_med3_f32 v168, v166, v186, v169
	s_waitcnt lgkmcnt(1)
	v_mfma_f32_16x16x32_f16 v[174:177], v[178:181], v[22:25], v[174:177]
	v_min_f32 v166, v166, v169
	v_med3_f32 v192, v168, v163, v170
	v_med3_f32 v163, v193, v194, v171
	v_mfma_f32_16x16x32_f16 v[110:113], v[178:181], v[54:57], v[110:113]
	ds_read_b128 v[178:181], v143 offset:49408
	v_med3_f32 v195, v166, v168, v170
	v_med3_f32 v168, v162, v193, v171
	s_waitcnt lgkmcnt(1)
	v_mfma_f32_16x16x32_f16 v[182:185], v[118:121], v[22:25], v[182:185]
	v_min_f32 v162, v162, v171
	v_med3_f32 v163, v168, v163, v172
	v_min_f32 v166, v166, v170
	v_mfma_f32_16x16x32_f16 v[114:117], v[118:121], v[54:57], v[114:117]
	ds_read_b128 v[118:121], v143 offset:57600
	v_med3_f32 v186, v162, v168, v172
	v_min_f32 v162, v162, v172
	s_waitcnt lgkmcnt(1)
	v_mfma_f32_16x16x32_f16 v[168:171], v[178:181], v[18:21], v[174:177]
	v_med3_f32 v172, v162, v186, v173
	v_med3_f32 v163, v186, v163, v173
	v_min_f32 v162, v162, v173
	v_mfma_f32_16x16x32_f16 v[110:113], v[178:181], v[50:53], v[110:113]
	v_med3_f32 v193, v172, v163, v198
	v_med3_f32 v194, v162, v172, v198
	s_nop 1
	ds_read_b128 v[172:175], v142 offset:49408
	s_waitcnt lgkmcnt(1)
	v_mfma_f32_16x16x32_f16 v[176:179], v[118:121], v[18:21], v[182:185]
	v_min_f32 v196, v162, v198
	ds_read_b128 v[188:191], v141 offset:57600
	v_lshl_add_u64 v[162:163], s[0:1], 0, v[122:123]
	v_readfirstlane_b32 s3, v108
	ds_read_b128 v[184:187], v142 offset:57600
	ds_read_b128 v[180:183], v141 offset:49408
	s_waitcnt vmcnt(4)
	s_waitcnt lgkmcnt(0)
	s_barrier
	s_mov_b32 m0, s3
	s_nop 0
	global_load_lds_dwordx4 v[162:163], off
	s_addk_i32 s3, 0x400
	v_lshl_add_u64 v[162:163], s[0:1], 0, v[106:107]
	s_add_u32 s0, s26, 0x9c000
	s_mov_b32 m0, s3
	s_nop 0
	global_load_lds_dwordx4 v[162:163], off
	s_addc_u32 s1, s27, 0
	v_lshl_add_u64 v[106:107], s[0:1], 0, v[106:107]
	v_readfirstlane_b32 s3, v109
	v_lshl_add_u64 v[108:109], s[0:1], 0, v[122:123]
	s_mov_b32 m0, s3
	s_nop 0
	global_load_lds_dwordx4 v[108:109], off
	s_addk_i32 s3, 0x400
	s_mov_b32 m0, s3
	s_nop 0
	global_load_lds_dwordx4 v[106:107], off
	v_mfma_f32_16x16x32_f16 v[114:117], v[118:121], v[50:53], v[114:117]
	v_med3_f32 v122, v195, v192, v164
	v_med3_f32 v162, v166, v195, v164
	v_min_f32 v163, v166, v164
	s_waitcnt lgkmcnt(3)
	v_mfma_f32_16x16x32_f16 v[118:121], v[172:175], v[14:17], v[168:171]
	v_med3_f32 v122, v162, v122, v161
	v_med3_f32 v162, v163, v162, v161
	v_min_f32 v161, v163, v161
	s_waitcnt lgkmcnt(1)
	v_mfma_f32_16x16x32_f16 v[168:171], v[184:187], v[14:17], v[176:179]
	v_med3_f32 v122, v162, v122, v165
	v_med3_f32 v166, v161, v162, v165
	v_min_f32 v161, v161, v165
	v_mfma_f32_16x16x32_f16 v[106:109], v[188:191], v[10:13], v[168:171]
	ds_read_b128 v[162:165], v154
	s_nop 0
	ds_read_b128 v[176:179], v156
	v_med3_f32 v122, v166, v122, v167
	v_mfma_f32_16x16x32_f16 v[110:113], v[172:175], v[46:49], v[110:113]
	s_nop 2
	ds_read_b128 v[168:171], v155
	v_fma_mix_f32 v38, v89, v39, v38 op_sel:[0,1,0] op_sel_hi:[0,1,0]
	v_fma_mix_f32 v70, v92, v71, v70 op_sel_hi:[0,1,0]
	v_mfma_f32_16x16x32_f16 v[172:175], v[184:187], v[46:49], v[114:117]
	ds_read_b128 v[184:187], v153
	v_fma_mix_f32 v39, v93, v71, v70 op_sel:[0,1,0] op_sel_hi:[0,1,0]
	v_fma_mix_f32 v38, v98, v40, v38 op_sel_hi:[0,1,0]
	s_waitcnt lgkmcnt(4)
	v_mfma_f32_16x16x32_f16 v[114:117], v[180:183], v[10:13], v[118:121]
	v_fma_mix_f32 v39, v82, v72, v39 op_sel_hi:[0,1,0]
	v_fma_mix_f32 v38, v99, v40, v38 op_sel:[0,1,0] op_sel_hi:[0,1,0]
	v_fma_mix_f32 v39, v83, v72, v39 op_sel:[0,1,0] op_sel_hi:[0,1,0]
	v_mfma_f32_16x16x32_f16 v[118:121], v[180:183], v[42:45], v[110:113]
	v_fma_mix_f32 v38, v100, v41, v38 op_sel_hi:[0,1,0]
	v_fma_mix_f32 v70, v84, v73, v39 op_sel_hi:[0,1,0]
	v_fma_mix_f32 v71, v101, v41, v38 op_sel:[0,1,0] op_sel_hi:[0,1,0]
	v_mfma_f32_16x16x32_f16 v[110:113], v[188:191], v[42:45], v[172:175]
	v_med3_f32 v188, v161, v166, v167
	v_min_f32 v189, v161, v167
	v_med3_f32 v161, v194, v193, v102
	s_waitcnt lgkmcnt(2)
	v_mfma_f32_16x16x32_f16 v[172:175], v[176:179], v[30:33], 0
	v_med3_f32 v190, v196, v194, v102
	v_min_f32 v102, v196, v102
	v_med3_f32 v122, v188, v122, v94
	v_mfma_f32_16x16x32_f16 v[176:179], v[176:179], v[62:65], 0
	v_med3_f32 v161, v190, v161, v103
	v_fma_mix_f32 v70, v85, v73, v70 op_sel:[0,1,0] op_sel_hi:[0,1,0]
	v_fma_mix_f32 v82, v114, v34, v71 op_sel_hi:[0,1,0]
	s_waitcnt lgkmcnt(1)
	v_mfma_f32_16x16x32_f16 v[180:183], v[168:171], v[30:33], 0
	v_fma_mix_f32 v83, v118, v66, v70 op_sel_hi:[0,1,0]
	v_fma_mix_f32 v34, v115, v34, v82 op_sel:[0,1,0] op_sel_hi:[0,1,0]
	v_fma_mix_f32 v66, v119, v66, v83 op_sel:[0,1,0] op_sel_hi:[0,1,0]
	v_mfma_f32_16x16x32_f16 v[166:169], v[168:171], v[62:65], 0
	v_fma_mix_f32 v34, v116, v35, v34 op_sel_hi:[0,1,0]
	v_fma_mix_f32 v66, v120, v67, v66 op_sel_hi:[0,1,0]
	v_fma_mix_f32 v34, v117, v35, v34 op_sel:[0,1,0] op_sel_hi:[0,1,0]
	v_mfma_f32_16x16x32_f16 v[170:173], v[162:165], v[26:29], v[172:175]
	v_fma_mix_f32 v35, v121, v67, v66 op_sel:[0,1,0] op_sel_hi:[0,1,0]
	v_fma_mix_f32 v34, v106, v36, v34 op_sel_hi:[0,1,0]
	v_fma_mix_f32 v35, v110, v68, v35 op_sel_hi:[0,1,0]
	v_mfma_f32_16x16x32_f16 v[162:165], v[162:165], v[58:61], v[176:179]
	v_fma_mix_f32 v34, v107, v36, v34 op_sel:[0,1,0] op_sel_hi:[0,1,0]
	v_fma_mix_f32 v35, v111, v68, v35 op_sel:[0,1,0] op_sel_hi:[0,1,0]
	v_fma_mix_f32 v34, v108, v37, v34 op_sel_hi:[0,1,0]
	ds_read_b128 v[174:177], v160 offset:256
	v_med3_f32 v160, v102, v190, v103
	v_min_f32 v102, v102, v103
	v_and_b32_e32 v103, 0xfffffc00, v104
	s_waitcnt lgkmcnt(1)
	v_mfma_f32_16x16x32_f16 v[178:181], v[184:187], v[26:29], v[180:183]
	v_or_b32_e32 v103, 0x3e2, v103
	v_med3_f32 v161, v160, v161, v103
	v_fma_mix_f32 v35, v112, v69, v35 op_sel_hi:[0,1,0]
	v_mfma_f32_16x16x32_f16 v[166:169], v[184:187], v[58:61], v[166:169]
	ds_read_b128 v[182:185], v159 offset:256
	v_and_b32_e32 v159, 0xfffffc00, v105
	v_med3_f32 v186, v102, v160, v103
	s_waitcnt lgkmcnt(1)
	v_mfma_f32_16x16x32_f16 v[170:173], v[174:177], v[22:25], v[170:173]
	v_min_f32 v187, v102, v103
	v_fma_mix_f32 v34, v109, v37, v34 op_sel:[0,1,0] op_sel_hi:[0,1,0]
	v_fma_mix_f32 v66, v113, v69, v35 op_sel:[0,1,0] op_sel_hi:[0,1,0]
	v_mfma_f32_16x16x32_f16 v[102:105], v[174:177], v[54:57], v[162:165]
	v_or_b32_e32 v174, 0x3e3, v159
	v_med3_f32 v190, v186, v161, v174
	ds_read_b128 v[158:161], v158 offset:256
	s_waitcnt lgkmcnt(1)
	v_mfma_f32_16x16x32_f16 v[162:165], v[182:185], v[22:25], v[178:181]
	v_med3_f32 v178, v187, v186, v174
	v_min_f32 v179, v187, v174
	ds_read_b128 v[174:177], v157 offset:256
	s_waitcnt lgkmcnt(1)
	v_mfma_f32_16x16x32_f16 v[170:173], v[158:161], v[18:21], v[170:173]
	v_med3_f32 v180, v189, v188, v94
	v_min_f32 v94, v189, v94
	v_mfma_f32_16x16x32_f16 v[102:105], v[158:161], v[50:53], v[102:105]
	ds_read_b128 v[156:159], v156 offset:256
	v_med3_f32 v122, v180, v122, v95
	v_med3_f32 v180, v94, v180, v95
	v_mfma_f32_16x16x32_f16 v[166:169], v[182:185], v[54:57], v[166:169]
	v_min_f32 v94, v94, v95
	v_and_b32_e32 v95, 0xfffffc00, v96
	v_or_b32_e32 v95, 0x3e2, v95
	s_waitcnt lgkmcnt(1)
	v_mfma_f32_16x16x32_f16 v[160:163], v[174:177], v[18:21], v[162:165]
	v_med3_f32 v122, v180, v122, v95
	v_mfma_f32_16x16x32_f16 v[164:167], v[174:177], v[50:53], v[166:169]
	ds_read_b128 v[174:177], v155 offset:256
	v_and_b32_e32 v155, 0xfffffc00, v97
	s_waitcnt lgkmcnt(1)
	v_mfma_f32_16x16x32_f16 v[168:171], v[156:159], v[14:17], v[170:173]
	v_med3_f32 v172, v94, v180, v95
	v_min_f32 v173, v94, v95
	v_mfma_f32_16x16x32_f16 v[94:97], v[156:159], v[46:49], v[102:105]
	v_or_b32_e32 v158, 0x3e3, v155
	v_med3_f32 v122, v172, v122, v158
	v_med3_f32 v182, v173, v172, v158
	v_min_f32 v183, v173, v158
	v_med3_f32 v172, v178, v190, v78
	s_nop 1
	ds_read_b128 v[102:105], v154 offset:256
	s_waitcnt lgkmcnt(1)
	v_mfma_f32_16x16x32_f16 v[154:157], v[174:177], v[14:17], v[160:163]
	v_med3_f32 v122, v182, v122, v74
	v_med3_f32 v182, v183, v182, v74
	v_min_f32 v74, v183, v74
	v_mfma_f32_16x16x32_f16 v[158:161], v[174:177], v[46:49], v[164:167]
	v_and_b32_e32 v175, 0xfffffc00, v81
	v_med3_f32 v122, v182, v122, v75
	v_med3_f32 v182, v74, v182, v75
	s_waitcnt lgkmcnt(0)
	v_mfma_f32_16x16x32_f16 v[166:169], v[102:105], v[10:13], v[168:171]
	v_min_f32 v74, v74, v75
	ds_read_b128 v[162:165], v153 offset:256
	v_med3_f32 v153, v179, v178, v78
	v_mfma_f32_16x16x32_f16 v[94:97], v[102:105], v[42:45], v[94:97]
	ds_read_b128 v[102:105], v146
	v_min_f32 v78, v179, v78
	v_med3_f32 v170, v153, v172, v79
	s_waitcnt lgkmcnt(1)
	v_mfma_f32_16x16x32_f16 v[154:157], v[162:165], v[10:13], v[154:157]
	v_med3_f32 v153, v78, v153, v79
	v_min_f32 v78, v78, v79
	v_and_b32_e32 v79, 0xfffffc00, v80
	v_or_b32_e32 v79, 0x3f2, v79
	v_mfma_f32_16x16x32_f16 v[158:161], v[162:165], v[42:45], v[158:161]
	v_med3_f32 v174, v153, v170, v79
	ds_read_b128 v[162:165], v145
	v_med3_f32 v153, v78, v153, v79
	s_waitcnt lgkmcnt(1)
	v_mfma_f32_16x16x32_f16 v[170:173], v[102:105], v[26:29], 0
	v_min_f32 v178, v78, v79
	v_or_b32_e32 v179, 0x3f3, v175
	v_med3_f32 v184, v153, v174, v179
	v_mfma_f32_16x16x32_f16 v[78:81], v[102:105], v[58:61], 0
	ds_read_b128 v[102:105], v152 offset:256
	v_med3_f32 v185, v178, v153, v179
	v_min_f32 v186, v178, v179
	ds_read_b128 v[178:181], v151 offset:256
	s_waitcnt lgkmcnt(2)
	v_mfma_f32_16x16x32_f16 v[174:177], v[162:165], v[26:29], 0
	v_and_b32_e32 v75, 0xfffffc00, v76
	v_or_b32_e32 v75, 0x3f2, v75
	v_med3_f32 v122, v182, v122, v75
	s_waitcnt lgkmcnt(1)
	v_mfma_f32_16x16x32_f16 v[170:173], v[102:105], v[22:25], v[170:173]
	v_fma_mix_f32 v67, v166, v30, v34 op_sel_hi:[0,1,0]
	v_fma_mix_f32 v30, v167, v30, v67 op_sel:[0,1,0] op_sel_hi:[0,1,0]
	v_fma_mix_f32 v30, v168, v31, v30 op_sel_hi:[0,1,0]
	v_mfma_f32_16x16x32_f16 v[78:81], v[102:105], v[54:57], v[78:81]
	ds_read_b128 v[102:105], v150 offset:256
	v_fma_mix_f32 v30, v169, v31, v30 op_sel:[0,1,0] op_sel_hi:[0,1,0]
	v_fma_mix_f32 v30, v154, v32, v30 op_sel_hi:[0,1,0]
	s_waitcnt lgkmcnt(1)
	v_mfma_f32_16x16x32_f16 v[150:153], v[178:181], v[22:25], v[174:177]
	v_fma_mix_f32 v30, v155, v32, v30 op_sel:[0,1,0] op_sel_hi:[0,1,0]
	v_fma_mix_f32 v30, v156, v33, v30 op_sel_hi:[0,1,0]
	s_nop 0
	ds_read_b128 v[174:177], v149 offset:256
	v_mfma_f32_16x16x32_f16 v[162:165], v[162:165], v[58:61], 0
	v_med3_f32 v149, v74, v182, v75
	v_mfma_f32_16x16x32_f16 v[162:165], v[178:181], v[54:57], v[162:165]
	v_min_f32 v178, v74, v75
	v_and_b32_e32 v179, 0xfffffc00, v77
	v_or_b32_e32 v179, 0x3f3, v179
	s_waitcnt lgkmcnt(1)
	v_mfma_f32_16x16x32_f16 v[74:77], v[102:105], v[50:53], v[78:81]
	v_med3_f32 v122, v149, v122, v179
	v_mfma_f32_16x16x32_f16 v[170:173], v[102:105], v[18:21], v[170:173]
	s_nop 1
	ds_read_b128 v[78:81], v148 offset:256
	s_waitcnt lgkmcnt(1)
	v_mfma_f32_16x16x32_f16 v[102:105], v[174:177], v[18:21], v[150:153]
	v_med3_f32 v152, v178, v149, v179
	v_min_f32 v153, v178, v179
	v_mfma_f32_16x16x32_f16 v[148:151], v[174:177], v[50:53], v[162:165]
	s_nop 2
	ds_read_b128 v[162:165], v147 offset:256
	s_waitcnt lgkmcnt(1)
	v_mfma_f32_16x16x32_f16 v[170:173], v[78:81], v[14:17], v[170:173]
	v_mfma_f32_16x16x32_f16 v[74:77], v[78:81], v[46:49], v[74:77]
	ds_read_b128 v[78:81], v146 offset:256
	s_waitcnt lgkmcnt(1)
	v_mfma_f32_16x16x32_f16 v[86:89], v[162:165], v[14:17], v[102:105]
	s_nop 2
	ds_read_b128 v[102:105], v145 offset:256
	s_waitcnt vmcnt(4)
	v_mfma_f32_16x16x32_f16 v[90:93], v[162:165], v[46:49], v[148:151]
	s_waitcnt lgkmcnt(0)
	s_barrier
	ds_read_b128 v[82:85], v144 offset:8448
	s_waitcnt lgkmcnt(2)
	v_mfma_f32_16x16x32_f16 v[38:41], v[78:81], v[42:45], v[74:77]
	s_nop 2
	ds_read_b128 v[74:77], v144 offset:256
	s_waitcnt lgkmcnt(2)
	v_mfma_f32_16x16x32_f16 v[70:73], v[102:105], v[42:45], v[90:93]
	s_nop 2
	ds_read_b128 v[90:93], v143 offset:256
	v_mfma_f32_16x16x32_f16 v[146:149], v[78:81], v[10:13], v[170:173]
	v_mfma_f32_16x16x32_f16 v[78:81], v[102:105], v[10:13], v[86:89]
	ds_read_b128 v[102:105], v143 offset:8448
	s_waitcnt lgkmcnt(2)
	v_mfma_f32_16x16x32_f16 v[86:89], v[74:77], v[22:25], 0
	v_mfma_f32_16x16x32_f16 v[74:77], v[74:77], v[54:57], 0
	s_waitcnt lgkmcnt(1)
	v_mfma_f32_16x16x32_f16 v[86:89], v[90:93], v[18:21], v[86:89]
	v_mfma_f32_16x16x32_f16 v[34:37], v[90:93], v[50:53], v[74:77]
	v_fma_mix_f32 v90, v94, v62, v66 op_sel_hi:[0,1,0]
	ds_read_b128 v[66:69], v142 offset:256
	v_fma_mix_f32 v62, v95, v62, v90 op_sel:[0,1,0] op_sel_hi:[0,1,0]
	ds_read_b128 v[90:93], v142 offset:8448
	v_mfma_f32_16x16x32_f16 v[98:101], v[82:85], v[22:25], 0
	v_fma_mix_f32 v62, v96, v63, v62 op_sel_hi:[0,1,0]
	v_fma_mix_f32 v31, v97, v63, v62 op_sel:[0,1,0] op_sel_hi:[0,1,0]
	v_fma_mix_f32 v31, v158, v64, v31 op_sel_hi:[0,1,0]
	v_mfma_f32_16x16x32_f16 v[82:85], v[82:85], v[54:57], 0
	v_fma_mix_f32 v31, v159, v64, v31 op_sel:[0,1,0] op_sel_hi:[0,1,0]
	v_fma_mix_f32 v31, v160, v65, v31 op_sel_hi:[0,1,0]
	v_fma_mix_f32 v62, v157, v33, v30 op_sel:[0,1,0] op_sel_hi:[0,1,0]
	s_waitcnt lgkmcnt(1)
	v_mfma_f32_16x16x32_f16 v[86:89], v[66:69], v[14:17], v[86:89]
	v_fma_mix_f32 v63, v161, v65, v31 op_sel:[0,1,0] op_sel_hi:[0,1,0]
	v_fma_mix_f32 v38, v38, v58, v63 op_sel_hi:[0,1,0]
	v_fma_mix_f32 v38, v39, v58, v38 op_sel:[0,1,0] op_sel_hi:[0,1,0]
	v_mfma_f32_16x16x32_f16 v[34:37], v[66:69], v[46:49], v[34:37]
	ds_read_b128 v[66:69], v141 offset:256
	v_fma_mix_f32 v38, v40, v59, v38 op_sel_hi:[0,1,0]
	v_mfma_f32_16x16x32_f16 v[74:77], v[102:105], v[18:21], v[98:101]
	v_mfma_f32_16x16x32_f16 v[82:85], v[102:105], v[50:53], v[82:85]
	s_waitcnt lgkmcnt(1)
	v_mfma_f32_16x16x32_f16 v[74:77], v[90:93], v[14:17], v[74:77]
	v_mfma_f32_16x16x32_f16 v[30:33], v[90:93], v[46:49], v[82:85]
	v_fma_mix_f32 v90, v146, v26, v62 op_sel_hi:[0,1,0]
	v_fma_mix_f32 v26, v147, v26, v90 op_sel:[0,1,0] op_sel_hi:[0,1,0]
	v_fma_mix_f32 v26, v148, v27, v26 op_sel_hi:[0,1,0]
	v_fma_mix_f32 v26, v149, v27, v26 op_sel:[0,1,0] op_sel_hi:[0,1,0]
	ds_read_b128 v[62:65], v141 offset:8448
	s_waitcnt lgkmcnt(1)
	v_mfma_f32_16x16x32_f16 v[82:85], v[66:69], v[10:13], v[86:89]
	v_fma_mix_f32 v27, v41, v59, v38 op_sel:[0,1,0] op_sel_hi:[0,1,0]
	v_fma_mix_f32 v26, v78, v28, v26 op_sel_hi:[0,1,0]
	v_fma_mix_f32 v27, v70, v60, v27 op_sel_hi:[0,1,0]
	v_mfma_f32_16x16x32_f16 v[34:37], v[66:69], v[42:45], v[34:37]
	ds_read_b128 v[66:69], v143 offset:16640
	v_fma_mix_f32 v26, v79, v28, v26 op_sel:[0,1,0] op_sel_hi:[0,1,0]
	v_fma_mix_f32 v27, v71, v60, v27 op_sel:[0,1,0] op_sel_hi:[0,1,0]
	v_fma_mix_f32 v26, v80, v29, v26 op_sel_hi:[0,1,0]
	v_fma_mix_f32 v58, v72, v61, v27 op_sel_hi:[0,1,0]
	v_fma_mix_f32 v59, v81, v29, v26 op_sel:[0,1,0] op_sel_hi:[0,1,0]
	v_fma_mix_f32 v70, v73, v61, v58 op_sel:[0,1,0] op_sel_hi:[0,1,0]
	v_fma_mix_f32 v71, v82, v22, v59 op_sel_hi:[0,1,0]
	ds_read_b128 v[58:61], v142 offset:16640
	v_fma_mix_f32 v34, v34, v54, v70 op_sel_hi:[0,1,0]
	v_fma_mix_f32 v22, v83, v22, v71 op_sel:[0,1,0] op_sel_hi:[0,1,0]
	v_fma_mix_f32 v34, v35, v54, v34 op_sel:[0,1,0] op_sel_hi:[0,1,0]
	v_fma_mix_f32 v22, v84, v23, v22 op_sel_hi:[0,1,0]
	v_fma_mix_f32 v34, v36, v55, v34 op_sel_hi:[0,1,0]
	ds_read_b128 v[38:41], v143 offset:24832
	v_fma_mix_f32 v22, v85, v23, v22 op_sel:[0,1,0] op_sel_hi:[0,1,0]
	v_fma_mix_f32 v23, v37, v55, v34 op_sel:[0,1,0] op_sel_hi:[0,1,0]
	ds_read_b128 v[34:37], v141 offset:16640
	s_waitcnt lgkmcnt(4)
	v_mfma_f32_16x16x32_f16 v[74:77], v[62:65], v[10:13], v[74:77]
	ds_read_b128 v[70:73], v142 offset:24832
	v_mfma_f32_16x16x32_f16 v[30:33], v[62:65], v[42:45], v[30:33]
	s_waitcnt lgkmcnt(4)
	v_mfma_f32_16x16x32_f16 v[62:65], v[66:69], v[18:21], 0
	s_nop 3
	v_fma_mix_f32 v22, v74, v24, v22 op_sel_hi:[0,1,0]
	s_nop 0
	v_fma_mix_f32 v23, v30, v56, v23 op_sel_hi:[0,1,0]
	v_fma_mix_f32 v22, v75, v24, v22 op_sel:[0,1,0] op_sel_hi:[0,1,0]
	v_mfma_f32_16x16x32_f16 v[26:29], v[66:69], v[50:53], 0
	v_fma_mix_f32 v23, v31, v56, v23 op_sel:[0,1,0] op_sel_hi:[0,1,0]
	v_fma_mix_f32 v22, v76, v25, v22 op_sel_hi:[0,1,0]
	v_fma_mix_f32 v23, v32, v57, v23 op_sel_hi:[0,1,0]
	s_waitcnt lgkmcnt(3)
	v_mfma_f32_16x16x32_f16 v[62:65], v[58:61], v[14:17], v[62:65]
	v_fma_mix_f32 v30, v77, v25, v22 op_sel:[0,1,0] op_sel_hi:[0,1,0]
	v_fma_mix_f32 v31, v33, v57, v23 op_sel:[0,1,0] op_sel_hi:[0,1,0]
	ds_read_b128 v[22:25], v141 offset:24832
	v_mfma_f32_16x16x32_f16 v[26:29], v[58:61], v[46:49], v[26:29]
	s_waitcnt vmcnt(0)
	s_waitcnt lgkmcnt(0)
	s_barrier
	s_waitcnt lgkmcnt(3)
	v_mfma_f32_16x16x32_f16 v[66:69], v[38:41], v[18:21], 0
	v_mfma_f32_16x16x32_f16 v[38:41], v[38:41], v[50:53], 0
	s_waitcnt lgkmcnt(2)
	v_mfma_f32_16x16x32_f16 v[62:65], v[34:37], v[10:13], v[62:65]
	v_mfma_f32_16x16x32_f16 v[26:29], v[34:37], v[42:45], v[26:29]
	ds_read_b128 v[34:37], v142 offset:33024
	s_nop 5
	v_fma_mix_f32 v54, v62, v18, v30 op_sel_hi:[0,1,0]
	v_fma_mix_f32 v18, v63, v18, v54 op_sel:[0,1,0] op_sel_hi:[0,1,0]
	s_waitcnt lgkmcnt(2)
	v_mfma_f32_16x16x32_f16 v[58:61], v[70:73], v[14:17], v[66:69]
	v_fma_mix_f32 v18, v64, v19, v18 op_sel_hi:[0,1,0]
	v_fma_mix_f32 v26, v26, v50, v31 op_sel_hi:[0,1,0]
	v_fma_mix_f32 v26, v27, v50, v26 op_sel:[0,1,0] op_sel_hi:[0,1,0]
	v_mfma_f32_16x16x32_f16 v[30:33], v[70:73], v[46:49], v[38:41]
	v_fma_mix_f32 v26, v28, v51, v26 op_sel_hi:[0,1,0]
	v_fma_mix_f32 v18, v65, v19, v18 op_sel:[0,1,0] op_sel_hi:[0,1,0]
	v_fma_mix_f32 v19, v29, v51, v26 op_sel:[0,1,0] op_sel_hi:[0,1,0]
	s_waitcnt lgkmcnt(1)
	v_mfma_f32_16x16x32_f16 v[38:41], v[22:25], v[10:13], v[58:61]
	ds_read_b128 v[26:29], v141 offset:33024
	v_mfma_f32_16x16x32_f16 v[22:25], v[22:25], v[42:45], v[30:33]
	s_nop 2
	ds_read_b128 v[30:33], v142 offset:41216
	s_waitcnt lgkmcnt(2)
	v_mfma_f32_16x16x32_f16 v[54:57], v[34:37], v[14:17], 0
	s_nop 1
	v_fma_mix_f32 v19, v22, v52, v19 op_sel_hi:[0,1,0]
	v_fma_mix_f32 v19, v23, v52, v19 op_sel:[0,1,0] op_sel_hi:[0,1,0]
	v_fma_mix_f32 v18, v38, v20, v18 op_sel_hi:[0,1,0]
	v_mfma_f32_16x16x32_f16 v[34:37], v[34:37], v[46:49], 0
	v_fma_mix_f32 v22, v24, v53, v19 op_sel_hi:[0,1,0]
	v_fma_mix_f32 v18, v39, v20, v18 op_sel:[0,1,0] op_sel_hi:[0,1,0]
	v_fma_mix_f32 v39, v25, v53, v22 op_sel:[0,1,0] op_sel_hi:[0,1,0]
	ds_read_b128 v[22:25], v141 offset:41216
	v_fma_mix_f32 v18, v40, v21, v18 op_sel_hi:[0,1,0]
	v_fma_mix_f32 v38, v41, v21, v18 op_sel:[0,1,0] op_sel_hi:[0,1,0]
	s_waitcnt lgkmcnt(2)
	v_mfma_f32_16x16x32_f16 v[18:21], v[26:29], v[10:13], v[54:57]
	v_mfma_f32_16x16x32_f16 v[26:29], v[26:29], v[42:45], v[34:37]
	s_waitcnt lgkmcnt(1)
	v_mfma_f32_16x16x32_f16 v[58:61], v[30:33], v[14:17], 0
	s_nop 4
	v_fma_mix_f32 v18, v18, v14, v38 op_sel_hi:[0,1,0]
	v_fma_mix_f32 v26, v26, v46, v39 op_sel_hi:[0,1,0]
	v_fma_mix_f32 v14, v19, v14, v18 op_sel:[0,1,0] op_sel_hi:[0,1,0]
	v_mfma_f32_16x16x32_f16 v[30:33], v[30:33], v[46:49], 0
	v_fma_mix_f32 v18, v27, v46, v26 op_sel:[0,1,0] op_sel_hi:[0,1,0]
	v_fma_mix_f32 v14, v20, v15, v14 op_sel_hi:[0,1,0]
	v_fma_mix_f32 v26, v28, v47, v18 op_sel_hi:[0,1,0]
	v_fma_mix_f32 v14, v21, v15, v14 op_sel:[0,1,0] op_sel_hi:[0,1,0]
	s_waitcnt lgkmcnt(0)
	v_mfma_f32_16x16x32_f16 v[18:21], v[22:25], v[10:13], v[58:61]
	v_fma_mix_f32 v15, v29, v47, v26 op_sel:[0,1,0] op_sel_hi:[0,1,0]
	ds_read_b128 v[26:29], v141 offset:49408
	v_mfma_f32_16x16x32_f16 v[22:25], v[22:25], v[42:45], v[30:33]
	s_nop 4
	v_fma_mix_f32 v14, v18, v16, v14 op_sel_hi:[0,1,0]
	s_nop 1
	v_fma_mix_f32 v15, v22, v48, v15 op_sel_hi:[0,1,0]
	v_fma_mix_f32 v14, v19, v16, v14 op_sel:[0,1,0] op_sel_hi:[0,1,0]
	v_fma_mix_f32 v15, v23, v48, v15 op_sel:[0,1,0] op_sel_hi:[0,1,0]
	v_fma_mix_f32 v14, v20, v17, v14 op_sel_hi:[0,1,0]
	v_fma_mix_f32 v18, v24, v49, v15 op_sel_hi:[0,1,0]
	v_fma_mix_f32 v22, v21, v17, v14 op_sel:[0,1,0] op_sel_hi:[0,1,0]
	v_fma_mix_f32 v30, v25, v49, v18 op_sel:[0,1,0] op_sel_hi:[0,1,0]
	ds_read_b128 v[18:21], v141 offset:57600
	s_waitcnt lgkmcnt(1)
	v_mfma_f32_16x16x32_f16 v[14:17], v[26:29], v[10:13], 0
	s_nop 7
	v_fma_mix_f32 v14, v14, v10, v22 op_sel_hi:[0,1,0]
	v_mfma_f32_16x16x32_f16 v[22:25], v[26:29], v[42:45], 0
	v_fma_mix_f32 v14, v15, v10, v14 op_sel:[0,1,0] op_sel_hi:[0,1,0]
	v_fma_mix_f32 v14, v16, v11, v14 op_sel_hi:[0,1,0]
	s_waitcnt lgkmcnt(0)
	v_mfma_f32_16x16x32_f16 v[26:29], v[18:21], v[10:13], 0
	v_fma_mix_f32 v10, v17, v11, v14 op_sel:[0,1,0] op_sel_hi:[0,1,0]
	s_nop 2
	v_fma_mix_f32 v22, v22, v42, v30 op_sel_hi:[0,1,0]
	v_fma_mix_f32 v15, v23, v42, v22 op_sel:[0,1,0] op_sel_hi:[0,1,0]
	v_fma_mix_f32 v15, v24, v43, v15 op_sel_hi:[0,1,0]
	v_fma_mix_f32 v11, v25, v43, v15 op_sel:[0,1,0] op_sel_hi:[0,1,0]
	v_fma_mix_f32 v10, v26, v12, v10 op_sel_hi:[0,1,0]
	v_mfma_f32_16x16x32_f16 v[14:17], v[18:21], v[42:45], 0
	v_fma_mix_f32 v10, v27, v12, v10 op_sel:[0,1,0] op_sel_hi:[0,1,0]
	v_fma_mix_f32 v10, v28, v13, v10 op_sel_hi:[0,1,0]
	v_lshlrev_b32_e32 v12, 2, v125
	v_fma_mix_f32 v10, v29, v13, v10 op_sel:[0,1,0] op_sel_hi:[0,1,0]
	v_or_b32_e32 v13, v12, v186
	v_mov_b32_e32 v18, v13
	v_mov_b32_e32 v19, v13
	s_nop 0
	v_fma_mix_f32 v11, v14, v44, v11 op_sel_hi:[0,1,0]
	v_or_b32_e32 v14, v12, v185
	v_permlane16_swap_b32_e32 v18, v19
	v_cndmask_b32_e64 v18, v18, v19, s[4:5]
	v_mov_b32_e32 v19, v14
	v_mov_b32_e32 v20, v14
	v_fma_mix_f32 v11, v15, v44, v11 op_sel:[0,1,0] op_sel_hi:[0,1,0]
	v_or_b32_e32 v15, v12, v184
	v_permlane16_swap_b32_e32 v19, v20
	v_cndmask_b32_e64 v19, v19, v20, s[4:5]
	v_mov_b32_e32 v20, v15
	v_mov_b32_e32 v21, v15
	v_fma_mix_f32 v11, v16, v45, v11 op_sel_hi:[0,1,0]
	v_or_b32_e32 v16, v12, v153
	v_permlane16_swap_b32_e32 v20, v21
	v_cndmask_b32_e64 v20, v20, v21, s[4:5]
	v_mov_b32_e32 v21, v16
	v_mov_b32_e32 v22, v16
	v_fma_mix_f32 v11, v17, v45, v11 op_sel:[0,1,0] op_sel_hi:[0,1,0]
	v_or_b32_e32 v17, v12, v152
	v_permlane16_swap_b32_e32 v21, v22
	v_cndmask_b32_e64 v21, v21, v22, s[4:5]
	v_mov_b32_e32 v22, v17
	v_mov_b32_e32 v23, v17
	v_med3_f32 v15, v14, v15, v18
	v_med3_f32 v14, v13, v14, v18
	v_or_b32_e32 v12, v12, v122
	s_nop 0
	v_permlane16_swap_b32_e32 v22, v23
	v_min_f32 v13, v13, v18
	v_med3_f32 v15, v14, v15, v19
	v_cndmask_b32_e64 v22, v22, v23, s[4:5]
	v_med3_f32 v14, v13, v14, v19
	v_mov_b32_e32 v23, v12
	v_mov_b32_e32 v24, v12
	v_min_f32 v13, v13, v19
	v_med3_f32 v18, v14, v15, v20
	v_med3_f32 v12, v17, v12, v21
	s_nop 1
	v_permlane16_swap_b32_e32 v23, v24
	v_med3_f32 v19, v13, v14, v20
	v_med3_f32 v14, v16, v17, v21
	v_min_f32 v15, v16, v21
	v_cndmask_b32_e64 v23, v23, v24, s[4:5]
	v_med3_f32 v12, v14, v12, v22
	v_med3_f32 v14, v15, v14, v22
	v_min_f32 v15, v15, v22
	v_min_f32 v13, v13, v20
	v_mov_b32_e32 v20, v19
	v_med3_f32 v12, v14, v12, v23
	v_med3_f32 v16, v15, v14, v23
	v_mov_b32_e32 v14, v10
	s_nop 1
	v_permlane16_swap_b32_e32 v10, v14
	v_add_f32_e32 v14, v10, v14
	v_mov_b32_e32 v10, v11
	s_nop 1
	v_permlane16_swap_b32_e32 v11, v10
	v_min_f32 v17, v15, v23
	v_add_f32_e32 v15, v11, v10
	v_mov_b32_e32 v10, v13
	v_mov_b32_e32 v11, v13
	s_nop 1
	v_permlane32_swap_b32_e32 v10, v11
	v_cndmask_b32_e64 v10, v10, v11, s[6:7]
	v_mov_b32_e32 v11, v19
	s_nop 1
	v_permlane32_swap_b32_e32 v11, v20
	v_cndmask_b32_e64 v11, v11, v20, s[6:7]
	v_mov_b32_e32 v20, v18
	v_mov_b32_e32 v21, v18
	s_nop 1
	v_permlane32_swap_b32_e32 v20, v21
	v_cndmask_b32_e64 v20, v20, v21, s[6:7]
	v_mov_b32_e32 v21, v17
	v_mov_b32_e32 v22, v17
	s_nop 1
	v_permlane32_swap_b32_e32 v21, v22
	v_cndmask_b32_e64 v21, v21, v22, s[6:7]
	v_mov_b32_e32 v22, v16
	v_mov_b32_e32 v23, v16
	v_med3_f32 v18, v19, v18, v10
	s_nop 1
	v_permlane32_swap_b32_e32 v22, v23
	v_med3_f32 v19, v13, v19, v10
	v_min_f32 v10, v13, v10
	v_cndmask_b32_e64 v22, v22, v23, s[6:7]
	v_med3_f32 v13, v19, v18, v11
	v_med3_f32 v18, v10, v19, v11
	v_min_f32 v11, v10, v11
	v_mov_b32_e32 v23, v12
	v_mov_b32_e32 v24, v12
	v_med3_f32 v10, v18, v13, v20
	v_med3_f32 v13, v11, v18, v20
	v_min_f32 v19, v11, v20
	v_med3_f32 v11, v16, v12, v21
	v_med3_f32 v12, v17, v16, v21
	s_nop 1
	v_permlane32_swap_b32_e32 v23, v24
	v_min_f32 v16, v17, v21
	v_med3_f32 v11, v12, v11, v22
	v_cndmask_b32_e64 v23, v23, v24, s[6:7]
	v_med3_f32 v12, v16, v12, v22
	v_min_f32 v17, v16, v22
	v_mov_b32_e32 v18, v15
	v_med3_f32 v11, v12, v11, v23
	v_med3_f32 v16, v17, v12, v23
	v_min_f32 v12, v17, v23
	v_mov_b32_e32 v17, v14
	s_nop 1
	v_permlane32_swap_b32_e32 v14, v17
	v_permlane32_swap_b32_e32 v15, v18
	v_cndmask_b32_e64 v12, v12, v19, s[4:5]
	s_and_saveexec_b64 s[0:1], s[6:7]
	s_cbranch_execz .LBB1_10
	v_add_f32_e32 v19, v137, v138
	v_add_f32_e32 v20, v139, v140
	v_add_f32_e32 v14, v14, v17
	v_add_f32_e32 v15, v15, v18
	v_cndmask_b32_e64 v19, v20, v19, s[4:5]
	v_cndmask_b32_e64 v14, v15, v14, s[4:5]
	v_fmac_f32_e32 v14, 2.0, v19
	s_waitcnt lgkmcnt(0)
	v_add_f32_e32 v14, s98, v14
	v_add_f32_e32 v14, v132, v14
	v_add_f32_e32 v123, v12, v14

	.amdhsa_kernel _Z6k_mainPKfS0_S0_PKDF16_S0_S0_S0_S0_S0_S0_PfP15HIP_vector_typeIiLj4EEPiS3_
		.amdhsa_group_segment_fixed_size 105056
		.amdhsa_private_segment_fixed_size 0
		.amdhsa_kernarg_size 112
		.amdhsa_user_sgpr_count 2
		.amdhsa_user_sgpr_dispatch_ptr 0
		.amdhsa_user_sgpr_queue_ptr 0
		.amdhsa_user_sgpr_kernarg_segment_ptr 1
		.amdhsa_user_sgpr_dispatch_id 0
		.amdhsa_user_sgpr_kernarg_preload_length 0
		.amdhsa_user_sgpr_kernarg_preload_offset 0
		.amdhsa_user_sgpr_private_segment_size 0
		.amdhsa_uses_dynamic_stack 0
		.amdhsa_enable_private_segment 0
		.amdhsa_system_sgpr_workgroup_id_x 1
		.amdhsa_system_sgpr_workgroup_id_y 0
		.amdhsa_system_sgpr_workgroup_id_z 0
		.amdhsa_system_sgpr_workgroup_info 0
		.amdhsa_system_vgpr_workitem_id 0
		.amdhsa_next_free_vgpr 248
		.amdhsa_next_free_sgpr 99
		.amdhsa_accum_offset 248
		.amdhsa_reserve_vcc 1
		.amdhsa_float_round_mode_32 0
		.amdhsa_float_round_mode_16_64 0
		.amdhsa_float_denorm_mode_32 3
		.amdhsa_float_denorm_mode_16_64 3
		.amdhsa_dx10_clamp 1
		.amdhsa_ieee_mode 1
		.amdhsa_fp16_overflow 0
		.amdhsa_tg_split 0
		.amdhsa_exception_fp_ieee_invalid_op 0
		.amdhsa_exception_fp_denorm_src 0
		.amdhsa_exception_fp_ieee_div_zero 0
		.amdhsa_exception_fp_ieee_overflow 0
		.amdhsa_exception_fp_ieee_underflow 0
		.amdhsa_exception_fp_ieee_inexact 0
		.amdhsa_exception_int_div_zero 0
	.end_amdhsa_kernel

_Z4k_t2PKfS0_S0_S0_S0_S0_PK15HIP_vector_typeIiLj4EEPKiPdPiS0_S0_Pf:
	s_load_dword s33, s[0:1], 0x68
	s_load_dwordx2 s[34:35], s[0:1], 0x60
	s_load_dwordx2 s[4:5], s[0:1], 0x38
	s_load_dwordx8 s[16:23], s[0:1], 0x0
	s_load_dwordx4 s[24:27], s[0:1], 0x40
	s_load_dwordx2 s[90:91], s[0:1], 0x30
	v_and_b32_e32 v66, 63, v0
	v_lshrrev_b32_e32 v1, 6, v0
	s_waitcnt lgkmcnt(0)
	s_add_i32 s3, s33, -1
	s_cmp_lg_u32 s2, s3
	v_lshlrev_b32_e32 v2, 2, v0
	v_cmp_eq_u32_e32 vcc, 0, v66
	s_cbranch_scc1 .LBB2_6
	s_load_dwordx2 s[6:7], s[0:1], 0x58
	s_waitcnt lgkmcnt(0)
	global_load_dword v3, v2, s[6:7]
	s_waitcnt vmcnt(0)
	s_nop 0
	v_add_f32_dpp v3, v3, v3 quad_perm:[1,0,3,2] row_mask:0xf bank_mask:0xf bound_ctrl:1
	s_nop 1
	v_add_f32_dpp v3, v3, v3 quad_perm:[2,3,0,1] row_mask:0xf bank_mask:0xf bound_ctrl:1
	v_mov_b32_e32 v4, v3
	s_nop 1
	v_mov_b32_dpp v4, v4 row_shl:4 row_mask:0xf bank_mask:0x5
	s_nop 1
	v_mov_b32_dpp v4, v3 row_shr:4 row_mask:0xf bank_mask:0xa
	v_add_f32_e32 v3, v3, v4
	s_nop 1
	v_add_f32_dpp v3, v3, v3 row_ror:8 row_mask:0xf bank_mask:0xf bound_ctrl:1
	v_mov_b32_e32 v4, v3
	s_nop 1
	v_permlane16_swap_b32_e32 v3, v4
	v_add_f32_e32 v3, v3, v4
	v_mov_b32_e32 v4, v3
	s_nop 1
	v_permlane32_swap_b32_e32 v3, v4
	s_and_saveexec_b64 s[6:7], vcc
	v_lshlrev_b32_e32 v5, 2, v1
	v_add_f32_e32 v3, v3, v4
	ds_write_b32 v5, v3 offset:4096
	s_or_b64 exec, exec, s[6:7]
	v_cmp_eq_u32_e32 vcc, 0, v0
	s_waitcnt lgkmcnt(0)
	s_barrier
	s_and_saveexec_b64 s[6:7], vcc
	s_cbranch_execz .LBB2_5
	v_mov_b32_e32 v3, 0
	v_mov_b32_e32 v6, 0x1004
	ds_read_b64 v[4:5], v3 offset:4096
	ds_read2_b32 v[6:7], v6 offset1:1
	s_waitcnt lgkmcnt(1)
	ds_read_b32 v5, v3 offset:4108
	s_waitcnt lgkmcnt(0)
	v_pk_add_f32 v[4:5], v[6:7], v[4:5]
	s_nop 0
	v_add_f32_e32 v3, v4, v5
	v_mul_f32_e32 v3, 0x32a00000, v3
	v_mov_b32_e32 v4, 0x4040000
	global_store_dword v4, v3, s[34:35]

.LBB2_6:
	s_load_dword s3, s[4:5], 0x0
	s_waitcnt lgkmcnt(0)
	s_lshl_b32 s42, s3, 4
	s_cmp_ge_i32 s2, s42
	s_cbranch_scc1 .LBB2_43
	s_load_dwordx2 s[4:5], s[0:1], 0x50
	v_and_b32_e32 v7, 0xc0, v0
	v_mov_b32_e32 v3, 0
	s_waitcnt lgkmcnt(0)
	global_load_dword v9, v2, s[18:19]
	global_load_dword v11, v2, s[20:21]
	v_lshlrev_b32_e32 v26, 2, v66
	v_lshlrev_b32_e32 v2, 12, v7
	v_lshlrev_b32_e32 v78, 2, v26
	v_lshl_add_u64 v[26:27], s[22:23], 0, v[2:3]
	s_load_dwordx4 s[20:23], s[0:1], 0x20
	v_mov_b32_e32 v13, 0x800
	v_lshrrev_b32_e32 v15, 1, v0
	v_lshl_or_b32 v77, v66, 3, v13
	v_and_b32_e32 v2, 0x78, v15
	v_and_b32_e32 v60, 32, v0
	v_and_b32_e32 v61, 16, v0
	s_mov_b32 s18, 0x667f3bcd
	s_mov_b32 s46, 0xcefddd8
	s_mov_b32 s48, 0x8c94b617
	s_mov_b32 s50, 0x312306d0
	s_mov_b32 s52, 0x6f4c5a9b
	s_mov_b32 s54, 0x7cfd79ae
	s_mov_b32 s56, 0x6410fdf7
	s_mov_b32 s58, 0x1f9b1786
	s_mov_b32 s60, 0xf4634b2e
	s_mov_b32 s62, 0xb42f7e4b
	s_mov_b32 s64, 0xc047288a
	s_mov_b32 s66, 0x7bbcce25
	s_mov_b32 s68, 0xae1babae
	s_mov_b32 s70, 0xe65a6063
	v_lshl_or_b32 v79, v1, 9, v77
	v_lshl_add_u64 v[28:29], s[24:25], 0, v[2:3]
	v_lshlrev_b32_e32 v2, 4, v66
	v_mbcnt_lo_u32_b32 v1, -1, 0
	s_mov_b32 s72, 0x6738ee3a
	s_mov_b32 s74, 0x28146b69
	s_mov_b32 s76, 0xa69750c4
	s_mov_b32 s78, 0x919fcca8
	s_mov_b32 s80, 0x652b82fe
	s_mov_b32 s82, 0xfefa39ef
	s_mov_b32 s84, 0x3b39803f
	s_mov_b32 s86, 0x6a5dcb37
	s_mov_b32 s88, 0x51d2ebeb
	v_lshlrev_b32_e32 v67, 3, v0
	v_and_b32_e32 v68, 15, v0
	s_lshl_b32 s43, s2, 6
	s_lshl_b32 s44, s33, 6
	v_lshlrev_b32_e32 v69, 2, v0
	v_mov_b32_e32 v4, 0x88e368f1
	v_mov_b32_e32 v5, 0x3ee4f8b5
	v_mov_b32_e32 v70, 0x100
	v_mov_b32_e32 v71, 0xffffff80
	v_mov_b32_e32 v72, 0x260
	s_mov_b32 s19, 0x3fe6a09e
	s_mov_b32 s47, 0x3e188b7a
	s_mov_b32 s49, 0xbe4aded4
	s_mov_b32 s51, 0x3e7803aa
	s_mov_b32 s53, 0xbea1b010
	s_mov_b32 s55, 0x3ec58c0e
	s_mov_b32 s57, 0xbee59e38
	s_mov_b32 s59, 0x3f0192fc
	s_mov_b32 s61, 0xbf162cf3
	s_mov_b32 s63, 0x3f2314df
	s_mov_b32 s65, 0xbf12cb68
	s_mov_b32 s67, 0xbf4038ff
	s_mov_b32 s69, 0x3f5a9466
	s_mov_b32 s71, 0xbf258be1
	v_bfrev_b32_e32 v73, 32
	v_mov_b32_e32 v6, 0x502a41cd
	v_mov_b32_e32 v8, 0xfca7ab0c
	v_mov_b32_e32 v10, 0x623fde64
	v_mov_b32_e32 v12, 0x7c89e6b0
	v_mov_b32_e32 v14, 0x14761f6e
	v_mov_b32_e32 v16, 0x1852b7b0
	v_mov_b32_e32 v18, 0x11122322
	v_mov_b32_e32 v20, 0x555502a1
	v_mov_b32_e32 v22, 0x55555511
	v_mov_b32_e32 v24, 11
	v_mov_b32_e32 v74, 0xfff00000
	v_mov_b32_e32 v75, 0x3ff00000
	v_lshlrev_b32_e32 v76, 3, v7
	v_lshl_add_u64 v[30:31], s[4:5], 0, v[2:3]
	v_lshl_add_u64 v[32:33], s[34:35], 0, v[2:3]
	s_waitcnt vmcnt(1)
	v_cvt_f64_f32_e32 v[34:35], v9
	s_waitcnt vmcnt(0)
	v_cvt_f64_f32_e32 v[36:37], v11
	v_mov_b32_e32 v38, 0xdfeb1f49
	v_mov_b32_e32 v40, 0x63844720
	v_mov_b32_e32 v42, 0x4280cfb9
	s_mov_b32 s73, 0xbf939bc1
	v_mov_b32_e32 v44, 0x4c771c5
	s_mov_b32 s75, 0x3fba4fbc
	v_mov_b32_e32 v46, 0x75531772
	s_mov_b32 s77, 0x3fe45f2d
	v_mov_b32_e32 v48, 0x149d904
	s_mov_b32 s79, 0x3fc06ebb
	v_mov_b32_e32 v50, 0xcf7e2856
	s_mov_b32 s81, 0xbff71547
	v_mov_b32_e32 v52, 0x311ee09b
	s_mov_b32 s83, 0xbfe62e42
	v_mov_b32_e32 v54, 0x1a0408d1
	s_mov_b32 s85, 0xbc7abc9e
	v_mov_b32_e32 v56, 0x6b0379b2
	s_mov_b32 s87, 0x3e5ade15
	v_mov_b32_e32 v58, 0x8214db68
	s_mov_b32 s89, 0xbe0ab15c
	v_mov_b32_e32 v7, 0xbcc145a3
	v_mov_b32_e32 v9, 0x3e928af3
	v_mov_b32_e32 v11, 0x3ec71dee
	v_mov_b32_e32 v13, 0x3efa0199
	v_mov_b32_e32 v15, 0x3f2a01a0
	v_mov_b32_e32 v17, 0x3f56c16c
	v_mov_b32_e32 v19, 0x3f811111
	v_mov_b32_e32 v21, 0x3fa55555
	v_mov_b32_e32 v23, 0x3fc55555
	v_mov_b32_e32 v25, 0x3fe00000
	v_mov_b32_e32 v39, 0x3e4d6e3d
	v_mov_b32_e32 v41, 0xbe85bfe7
	v_mov_b32_e32 v43, 0x3ebb97e4
	v_mov_b32_e32 v45, 0xbeef4ca2
	v_mov_b32_e32 v47, 0x3f1f9a2b
	v_mov_b32_e32 v49, 0xbf4c02db
	v_mov_b32_e32 v51, 0x3f7565bc
	v_mov_b32_e32 v53, 0xbf9b82ce
	v_mov_b32_e32 v55, 0x3fbce2f2
	v_mov_b32_e32 v57, 0xbfd81274
	v_mov_b32_e32 v59, 0x3fc06eba
	v_mbcnt_hi_u32_b32 v80, -1, v1
	v_cmp_eq_u32_e64 s[0:1], 0, v61
	v_cmp_eq_u32_e64 s[4:5], 0, v60
	v_cmp_gt_u32_e64 s[6:7], 64, v0
	v_cmp_eq_u32_e64 s[8:9], 0, v66
	v_cmp_eq_u32_e64 s[10:11], 0, v0
	v_cmp_gt_u32_e64 s[12:13], 48, v66
	s_branch .LBB2_9
